# adds: mixers queue ticket prefetch, batched MoE gather-offset loads, peeled first K iteration with SrcC=0 (no accumulator zeroing), leaner DSA fast path (dead flag code removed, softmax exponent as on
# speedup vs baseline: 1.0097x; 1.0097x over previous
.Lmy_z_0:
	s_add_u32 s4, s4, 0x80
	s_addc_u32 s5, s5, 0
	s_add_u32 s8, s6, 0x100
	s_addc_u32 s9, s7, 0
	s_mov_b32 s6, 0
	s_add_i32 s25, s6, 2
	s_add_u32 s28, s4, 0x80
	s_addc_u32 s7, s5, 0
	s_add_i32 s30, 0, 0x10000
	s_cmp_eq_u32 s21, s6
	s_cselect_b32 s7, s71, s7
	s_cselect_b32 s6, s70, s28
	s_cselect_b32 s29, s79, s9
	s_cselect_b32 s28, s78, s8
	s_add_i32 s40, 0, 0x14000
	v_add_u32_e32 v28, s30, v218
	v_add_u32_e32 v102, s40, v218
	ds_read_b128 v[8:11], v28
	ds_read_b128 v[12:15], v28 offset:1024
	ds_read_b128 v[24:27], v28 offset:2048
	ds_read_b128 v[28:31], v28 offset:3072
	ds_read_b128 v[40:43], v102
	ds_read_b128 v[62:65], v102 offset:1024
	ds_read_b128 v[82:85], v102 offset:2048
	ds_read_b128 v[102:105], v102 offset:3072
	v_lshl_add_u64 v[210:211], s[4:5], 0, v[186:187]
	s_add_i32 m0, s94, 0xc000
	ds_read_b128 v[122:125], v220
	ds_read_b128 v[142:145], v220 offset:1024
	ds_read_b128 v[162:165], v220 offset:2048
	ds_read_b128 v[190:193], v220 offset:3072
	ds_read_b128 v[194:197], v220 offset:4096
	ds_read_b128 v[198:201], v220 offset:5120
	ds_read_b128 v[202:205], v220 offset:6144
	ds_read_b128 v[206:209], v220 offset:7168
	global_load_lds_dwordx4 v[210:211], off
	v_lshl_add_u64 v[210:211], s[4:5], 0, v[188:189]
	s_add_i32 m0, s94, 0xe000
	s_nop 0
	global_load_lds_dwordx4 v[210:211], off
	s_waitcnt vmcnt(8)
	s_waitcnt lgkmcnt(0)
	s_barrier
	s_setprio 1
	s_waitcnt lgkmcnt(0)
	v_mfma_f32_16x16x32_bf16 v[166:169], v[8:11], v[122:125], 0
	v_mfma_f32_16x16x32_bf16 v[170:173], v[24:27], v[122:125], 0
	v_mfma_f32_16x16x32_bf16 v[150:153], v[8:11], v[162:165], 0
	v_mfma_f32_16x16x32_bf16 v[146:149], v[24:27], v[162:165], 0
	v_mfma_f32_16x16x32_bf16 v[130:133], v[8:11], v[194:197], 0
	v_mfma_f32_16x16x32_bf16 v[126:129], v[24:27], v[194:197], 0
	v_mfma_f32_16x16x32_bf16 v[110:113], v[8:11], v[202:205], 0
	v_mfma_f32_16x16x32_bf16 v[106:109], v[24:27], v[202:205], 0
	v_mfma_f32_16x16x32_bf16 v[166:169], v[12:15], v[142:145], v[166:169]
	v_mfma_f32_16x16x32_bf16 v[170:173], v[28:31], v[142:145], v[170:173]
	v_mfma_f32_16x16x32_bf16 v[150:153], v[12:15], v[190:193], v[150:153]
	v_mfma_f32_16x16x32_bf16 v[146:149], v[28:31], v[190:193], v[146:149]
	v_mfma_f32_16x16x32_bf16 v[130:133], v[12:15], v[198:201], v[130:133]
	v_mfma_f32_16x16x32_bf16 v[126:129], v[28:31], v[198:201], v[126:129]
	v_mfma_f32_16x16x32_bf16 v[110:113], v[12:15], v[206:209], v[110:113]
	v_mfma_f32_16x16x32_bf16 v[106:109], v[28:31], v[206:209], v[106:109]
	s_setprio 0
	s_setprio 1
	v_mfma_f32_16x16x32_bf16 v[158:161], v[40:43], v[122:125], 0
	v_mfma_f32_16x16x32_bf16 v[138:141], v[40:43], v[162:165], 0
	v_mfma_f32_16x16x32_bf16 v[134:137], v[82:85], v[162:165], 0
	v_mfma_f32_16x16x32_bf16 v[118:121], v[40:43], v[194:197], 0
	v_mfma_f32_16x16x32_bf16 v[114:117], v[82:85], v[194:197], 0
	v_mfma_f32_16x16x32_bf16 v[98:101], v[40:43], v[202:205], 0
	v_mfma_f32_16x16x32_bf16 v[94:97], v[82:85], v[202:205], 0
	v_mfma_f32_16x16x32_bf16 v[158:161], v[62:65], v[142:145], v[158:161]
	v_mfma_f32_16x16x32_bf16 v[122:125], v[82:85], v[122:125], 0
	v_mfma_f32_16x16x32_bf16 v[138:141], v[62:65], v[190:193], v[138:141]
	v_mfma_f32_16x16x32_bf16 v[134:137], v[102:105], v[190:193], v[134:137]
	v_mfma_f32_16x16x32_bf16 v[118:121], v[62:65], v[198:201], v[118:121]
	v_mfma_f32_16x16x32_bf16 v[114:117], v[102:105], v[198:201], v[114:117]
	v_mfma_f32_16x16x32_bf16 v[98:101], v[62:65], v[206:209], v[98:101]
	v_mfma_f32_16x16x32_bf16 v[94:97], v[102:105], v[206:209], v[94:97]
	v_mfma_f32_16x16x32_bf16 v[122:125], v[102:105], v[142:145], v[122:125]
	s_setprio 0
	s_barrier
	s_add_i32 s30, s30, s93
	v_lshl_add_u64 v[214:215], s[28:29], 0, v[176:177]
	s_mov_b32 m0, s30
	ds_read_b128 v[142:145], v220 offset:16384
	ds_read_b128 v[154:157], v220 offset:17408
	ds_read_b128 v[162:165], v220 offset:18432
	ds_read_b128 v[190:193], v220 offset:19456
	ds_read_b128 v[194:197], v220 offset:20480
	ds_read_b128 v[198:201], v220 offset:21504
	ds_read_b128 v[202:205], v220 offset:22528
	ds_read_b128 v[206:209], v220 offset:23552
	global_load_lds_dwordx4 v[214:215], off
	s_add_i32 m0, s30, 0x2000
	v_lshl_add_u64 v[216:217], s[28:29], 0, v[180:181]
	s_add_u32 s28, s28, s52
	s_addc_u32 s29, s29, s53
	s_add_i32 s30, s40, s93
	global_load_lds_dwordx4 v[216:217], off
	v_lshl_add_u64 v[222:223], s[28:29], 0, v[176:177]
	s_mov_b32 m0, s30
	v_lshl_add_u64 v[224:225], s[28:29], 0, v[180:181]
	global_load_lds_dwordx4 v[222:223], off
	s_add_i32 m0, s30, 0x2000
	v_lshl_add_u64 v[226:227], s[6:7], 0, v[174:175]
	global_load_lds_dwordx4 v[224:225], off
	s_mov_b32 m0, s94
	v_lshl_add_u64 v[228:229], s[6:7], 0, v[178:179]
	global_load_lds_dwordx4 v[226:227], off
	s_mov_b32 m0, s95
	s_nop 0
	global_load_lds_dwordx4 v[228:229], off
	s_waitcnt vmcnt(8)
	s_waitcnt lgkmcnt(0)
	s_barrier
	s_setprio 1
	s_waitcnt lgkmcnt(0)
	v_mfma_f32_16x16x32_bf16 v[90:93], v[8:11], v[142:145], 0
	v_mfma_f32_16x16x32_bf16 v[86:89], v[24:27], v[142:145], 0
	v_mfma_f32_16x16x32_bf16 v[70:73], v[8:11], v[162:165], 0
	v_mfma_f32_16x16x32_bf16 v[66:69], v[24:27], v[162:165], 0
	v_mfma_f32_16x16x32_bf16 v[50:53], v[8:11], v[194:197], 0
	v_mfma_f32_16x16x32_bf16 v[44:47], v[24:27], v[194:197], 0
	v_mfma_f32_16x16x32_bf16 v[8:11], v[8:11], v[202:205], 0
	v_mfma_f32_16x16x32_bf16 v[90:93], v[12:15], v[154:157], v[90:93]
	v_mfma_f32_16x16x32_bf16 v[86:89], v[28:31], v[154:157], v[86:89]
	v_mfma_f32_16x16x32_bf16 v[70:73], v[12:15], v[190:193], v[70:73]
	v_mfma_f32_16x16x32_bf16 v[66:69], v[28:31], v[190:193], v[66:69]
	v_mfma_f32_16x16x32_bf16 v[50:53], v[12:15], v[198:201], v[50:53]
	v_mfma_f32_16x16x32_bf16 v[44:47], v[28:31], v[198:201], v[44:47]
	v_mfma_f32_16x16x32_bf16 v[8:11], v[12:15], v[206:209], v[8:11]
	v_mfma_f32_16x16x32_bf16 v[12:15], v[24:27], v[202:205], 0
	v_mfma_f32_16x16x32_bf16 v[12:15], v[28:31], v[206:209], v[12:15]
	s_setprio 0
	s_setprio 1
	v_mfma_f32_16x16x32_bf16 v[16:19], v[40:43], v[142:145], 0
	v_mfma_f32_16x16x32_bf16 v[24:27], v[62:65], v[154:157], v[16:19]
	v_mfma_f32_16x16x32_bf16 v[16:19], v[82:85], v[142:145], 0
	v_mfma_f32_16x16x32_bf16 v[28:31], v[102:105], v[154:157], v[16:19]
	v_mfma_f32_16x16x32_bf16 v[16:19], v[40:43], v[162:165], 0
	v_mfma_f32_16x16x32_bf16 v[58:61], v[62:65], v[190:193], v[16:19]
	v_mfma_f32_16x16x32_bf16 v[16:19], v[82:85], v[162:165], 0
	v_mfma_f32_16x16x32_bf16 v[54:57], v[102:105], v[190:193], v[16:19]
	v_mfma_f32_16x16x32_bf16 v[16:19], v[40:43], v[194:197], 0
	v_mfma_f32_16x16x32_bf16 v[36:39], v[62:65], v[198:201], v[16:19]
	v_mfma_f32_16x16x32_bf16 v[16:19], v[82:85], v[194:197], 0
	v_mfma_f32_16x16x32_bf16 v[4:7], v[40:43], v[202:205], 0
	v_mfma_f32_16x16x32_bf16 v[0:3], v[82:85], v[202:205], 0
	v_mfma_f32_16x16x32_bf16 v[32:35], v[102:105], v[198:201], v[16:19]
	v_mfma_f32_16x16x32_bf16 v[4:7], v[62:65], v[206:209], v[4:7]
	v_mfma_f32_16x16x32_bf16 v[0:3], v[102:105], v[206:209], v[0:3]
	s_setprio 0
	s_barrier
	s_add_i32 s28, 0, 0x18000
	s_add_i32 s29, 0, 0x1c000
	v_add_u32_e32 v62, s28, v218
	v_add_u32_e32 v74, s29, v218
	ds_read_b128 v[16:19], v62
	ds_read_b128 v[20:23], v62 offset:1024
	ds_read_b128 v[40:43], v62 offset:2048
	ds_read_b128 v[62:65], v62 offset:3072
	ds_read_b128 v[82:85], v74
	ds_read_b128 v[102:105], v74 offset:1024
	ds_read_b128 v[142:145], v74 offset:2048
	ds_read_b128 v[162:165], v74 offset:3072
	s_add_u32 s6, s6, s52
	s_addc_u32 s7, s7, s53
	s_mov_b32 m0, s96
	v_lshl_add_u64 v[154:155], s[6:7], 0, v[174:175]
	ds_read_b128 v[74:77], v220 offset:32768
	ds_read_b128 v[78:81], v220 offset:33792
	ds_read_b128 v[190:193], v220 offset:34816
	ds_read_b128 v[194:197], v220 offset:35840
	ds_read_b128 v[198:201], v220 offset:36864
	ds_read_b128 v[202:205], v220 offset:37888
	ds_read_b128 v[206:209], v220 offset:38912
	ds_read_b128 v[210:213], v220 offset:39936
	global_load_lds_dwordx4 v[154:155], off
	v_lshl_add_u64 v[154:155], s[6:7], 0, v[178:179]
	s_mov_b32 m0, s97
	s_nop 0
	global_load_lds_dwordx4 v[154:155], off
	s_waitcnt vmcnt(8)
	s_waitcnt lgkmcnt(0)
	s_barrier
	s_setprio 1
	s_waitcnt lgkmcnt(0)
	v_mfma_f32_16x16x32_bf16 v[154:157], v[16:19], v[74:77], v[166:169]
	v_mfma_f32_16x16x32_bf16 v[166:169], v[20:23], v[78:81], v[154:157]
	v_mfma_f32_16x16x32_bf16 v[154:157], v[40:43], v[74:77], v[170:173]
	v_mfma_f32_16x16x32_bf16 v[150:153], v[16:19], v[190:193], v[150:153]
	v_mfma_f32_16x16x32_bf16 v[146:149], v[40:43], v[190:193], v[146:149]
	v_mfma_f32_16x16x32_bf16 v[130:133], v[16:19], v[198:201], v[130:133]
	v_mfma_f32_16x16x32_bf16 v[126:129], v[40:43], v[198:201], v[126:129]
	v_mfma_f32_16x16x32_bf16 v[110:113], v[16:19], v[206:209], v[110:113]
	v_mfma_f32_16x16x32_bf16 v[106:109], v[40:43], v[206:209], v[106:109]
	v_mfma_f32_16x16x32_bf16 v[170:173], v[62:65], v[78:81], v[154:157]
	v_mfma_f32_16x16x32_bf16 v[150:153], v[20:23], v[194:197], v[150:153]
	v_mfma_f32_16x16x32_bf16 v[146:149], v[62:65], v[194:197], v[146:149]
	v_mfma_f32_16x16x32_bf16 v[130:133], v[20:23], v[202:205], v[130:133]
	v_mfma_f32_16x16x32_bf16 v[126:129], v[62:65], v[202:205], v[126:129]
	v_mfma_f32_16x16x32_bf16 v[110:113], v[20:23], v[210:213], v[110:113]
	v_mfma_f32_16x16x32_bf16 v[106:109], v[62:65], v[210:213], v[106:109]
	s_setprio 0
	s_setprio 1
	v_mfma_f32_16x16x32_bf16 v[154:157], v[82:85], v[74:77], v[158:161]
	v_mfma_f32_16x16x32_bf16 v[74:77], v[142:145], v[74:77], v[122:125]
	v_mfma_f32_16x16x32_bf16 v[158:161], v[102:105], v[78:81], v[154:157]
	v_mfma_f32_16x16x32_bf16 v[154:157], v[162:165], v[78:81], v[74:77]
	v_mfma_f32_16x16x32_bf16 v[74:77], v[82:85], v[190:193], v[138:141]
	v_mfma_f32_16x16x32_bf16 v[138:141], v[102:105], v[194:197], v[74:77]
	v_mfma_f32_16x16x32_bf16 v[74:77], v[142:145], v[190:193], v[134:137]
	v_mfma_f32_16x16x32_bf16 v[134:137], v[162:165], v[194:197], v[74:77]
	v_mfma_f32_16x16x32_bf16 v[74:77], v[82:85], v[198:201], v[118:121]
	v_mfma_f32_16x16x32_bf16 v[118:121], v[102:105], v[202:205], v[74:77]
	v_mfma_f32_16x16x32_bf16 v[74:77], v[142:145], v[198:201], v[114:117]
	v_mfma_f32_16x16x32_bf16 v[114:117], v[162:165], v[202:205], v[74:77]
	v_mfma_f32_16x16x32_bf16 v[74:77], v[82:85], v[206:209], v[98:101]
	v_mfma_f32_16x16x32_bf16 v[98:101], v[102:105], v[210:213], v[74:77]
	v_mfma_f32_16x16x32_bf16 v[74:77], v[142:145], v[206:209], v[94:97]
	v_mfma_f32_16x16x32_bf16 v[94:97], v[162:165], v[210:213], v[74:77]
	s_setprio 0
	s_barrier
	s_add_i32 s6, s28, s93
	v_lshl_add_u64 v[78:79], v[214:215], 0, s[34:35]
	s_mov_b32 m0, s6
	s_nop 1
	ds_read_b128 v[74:77], v220 offset:49152
	ds_read_b128 v[122:125], v220 offset:50176
	ds_read_b128 v[190:193], v220 offset:51200
	ds_read_b128 v[194:197], v220 offset:52224
	ds_read_b128 v[198:201], v220 offset:53248
	ds_read_b128 v[202:205], v220 offset:54272
	ds_read_b128 v[206:209], v220 offset:55296
	ds_read_b128 v[210:213], v220 offset:56320
	global_load_lds_dwordx4 v[78:79], off
	v_lshl_add_u64 v[78:79], v[216:217], 0, s[34:35]
	s_add_i32 m0, s6, 0x2000
	s_add_i32 s6, s29, s93
	global_load_lds_dwordx4 v[78:79], off
	v_lshl_add_u64 v[78:79], v[222:223], 0, s[34:35]
	s_mov_b32 m0, s6
	s_nop 0
	global_load_lds_dwordx4 v[78:79], off
	v_lshl_add_u64 v[78:79], v[224:225], 0, s[34:35]
	s_add_i32 m0, s6, 0x2000
	s_nop 0
	global_load_lds_dwordx4 v[78:79], off
	v_lshl_add_u64 v[78:79], v[226:227], 0, s[34:35]
	s_mov_b32 m0, s26
	s_nop 0
	global_load_lds_dwordx4 v[78:79], off
	v_lshl_add_u64 v[78:79], v[228:229], 0, s[34:35]
	s_mov_b32 m0, s56
	s_nop 0
	global_load_lds_dwordx4 v[78:79], off
	s_waitcnt vmcnt(8)
	s_waitcnt lgkmcnt(0)
	s_barrier
	s_setprio 1
	s_waitcnt lgkmcnt(0)
	v_mfma_f32_16x16x32_bf16 v[78:81], v[16:19], v[74:77], v[90:93]
	v_mfma_f32_16x16x32_bf16 v[70:73], v[16:19], v[190:193], v[70:73]
	v_mfma_f32_16x16x32_bf16 v[50:53], v[16:19], v[198:201], v[50:53]
	v_mfma_f32_16x16x32_bf16 v[8:11], v[16:19], v[206:209], v[8:11]
	v_mfma_f32_16x16x32_bf16 v[90:93], v[20:23], v[122:125], v[78:81]
	v_mfma_f32_16x16x32_bf16 v[78:81], v[40:43], v[74:77], v[86:89]
	v_mfma_f32_16x16x32_bf16 v[70:73], v[20:23], v[194:197], v[70:73]
	v_mfma_f32_16x16x32_bf16 v[66:69], v[40:43], v[190:193], v[66:69]
	v_mfma_f32_16x16x32_bf16 v[50:53], v[20:23], v[202:205], v[50:53]
	v_mfma_f32_16x16x32_bf16 v[44:47], v[40:43], v[198:201], v[44:47]
	v_mfma_f32_16x16x32_bf16 v[20:23], v[20:23], v[210:213], v[8:11]
	v_mfma_f32_16x16x32_bf16 v[8:11], v[40:43], v[206:209], v[12:15]
	v_mfma_f32_16x16x32_bf16 v[86:89], v[62:65], v[122:125], v[78:81]
	v_mfma_f32_16x16x32_bf16 v[66:69], v[62:65], v[194:197], v[66:69]
	v_mfma_f32_16x16x32_bf16 v[44:47], v[62:65], v[202:205], v[44:47]
	v_mfma_f32_16x16x32_bf16 v[16:19], v[62:65], v[210:213], v[8:11]
	s_setprio 0
	s_setprio 1
	v_mfma_f32_16x16x32_bf16 v[8:11], v[82:85], v[74:77], v[24:27]
	v_mfma_f32_16x16x32_bf16 v[78:81], v[102:105], v[122:125], v[8:11]
	v_mfma_f32_16x16x32_bf16 v[8:11], v[142:145], v[74:77], v[28:31]
	v_mfma_f32_16x16x32_bf16 v[74:77], v[162:165], v[122:125], v[8:11]
	v_mfma_f32_16x16x32_bf16 v[8:11], v[82:85], v[190:193], v[58:61]
	v_mfma_f32_16x16x32_bf16 v[58:61], v[102:105], v[194:197], v[8:11]
	v_mfma_f32_16x16x32_bf16 v[8:11], v[142:145], v[190:193], v[54:57]
	v_mfma_f32_16x16x32_bf16 v[54:57], v[162:165], v[194:197], v[8:11]
	v_mfma_f32_16x16x32_bf16 v[8:11], v[82:85], v[198:201], v[36:39]
	v_mfma_f32_16x16x32_bf16 v[36:39], v[102:105], v[202:205], v[8:11]
	v_mfma_f32_16x16x32_bf16 v[8:11], v[142:145], v[198:201], v[32:35]
	v_mfma_f32_16x16x32_bf16 v[4:7], v[82:85], v[206:209], v[4:7]
	v_mfma_f32_16x16x32_bf16 v[0:3], v[142:145], v[206:209], v[0:3]
	v_mfma_f32_16x16x32_bf16 v[32:35], v[162:165], v[202:205], v[8:11]
	v_mfma_f32_16x16x32_bf16 v[4:7], v[102:105], v[210:213], v[4:7]
	v_mfma_f32_16x16x32_bf16 v[0:3], v[162:165], v[210:213], v[0:3]
	s_setprio 0
	s_barrier
	s_add_u32 s4, s4, 0x100
	s_addc_u32 s5, s5, 0
	s_add_u32 s8, s8, 0x100
	s_addc_u32 s9, s9, 0
	s_cmp_ge_i32 s25, s91
	s_mov_b32 s6, s25

.LBB0_519:
	s_andn2_b64 vcc, exec, s[4:5]
	s_cbranch_vccnz .LBB0_967
	s_load_dword s6, s[54:55], 0xd4
	s_load_dwordx2 s[4:5], s[54:55], 0xc0
	s_mov_b32 s30, s26
	v_mov_b32_e32 v146, v235
	s_waitcnt lgkmcnt(0)
	s_ashr_i32 s7, s6, 31
	s_lshl_b64 s[18:19], s[6:7], 11
	s_lshl_b64 s[20:21], s[6:7], 12
	s_lshl_b64 s[24:25], s[6:7], 7
	s_add_u32 s12, s20, s24
	s_addc_u32 s17, s21, s25
	s_add_u32 s12, s4, s12
	s_addc_u32 s17, s5, s17
	s_add_u32 s88, s12, 0x18422000
	s_mul_i32 s24, s6, 0x3c00
	s_addc_u32 s89, s17, 0
	s_mul_hi_i32 s1, s6, 0x3c00
	s_load_dwordx2 s[20:21], s[54:55], 0x8
	s_load_dwordx2 s[8:9], s[54:55], 0x28
	s_add_u32 s66, s88, s24
	s_mul_i32 s26, s6, 0x180
	s_addc_u32 s67, s89, s1
	s_mul_hi_i32 s25, s6, 0x180
	s_add_u32 s17, s66, s26
	s_addc_u32 s85, s67, s25
	s_lshl_b32 s26, s30, 7
	s_lshl_b64 s[24:25], s[26:27], 2
	s_waitcnt lgkmcnt(0)
	s_add_u32 s8, s8, s24
	s_addc_u32 s9, s9, s25
	v_writelane_b32 v255, s8, 46
	s_mul_i32 s29, s6, 0xc00
	s_mul_hi_i32 s28, s6, 0xc00
	v_writelane_b32 v255, s9, 47
	s_mov_b32 s84, s17
	v_readlane_b32 s1, v255, 38
	s_lshl_b32 s26, s1, 6
	s_lshl_b64 s[8:9], s[26:27], 2
	s_add_u32 s1, s4, s8
	s_addc_u32 s8, s5, s9
	s_add_u32 s92, s1, 0x8000
	v_readlane_b32 s12, v255, 34
	s_addc_u32 s93, s8, 0
	s_mul_hi_u32 s8, s6, s12
	s_mul_i32 s9, s7, s12
	s_lshl_b32 s1, s30, 16
	s_add_i32 s9, s8, s9
	s_mul_i32 s8, s6, s12
	s_add_u32 s8, s8, s1
	s_addc_u32 s9, s9, 0
	s_lshl_b64 s[8:9], s[8:9], 10
	s_add_u32 s94, s20, s8
	s_addc_u32 s95, s21, s9
	s_add_u32 s1, s17, s29
	s_addc_u32 s8, s85, s28
	s_add_u32 s96, s1, s18
	s_addc_u32 s97, s8, s19
	s_lshr_b32 s9, s7, 21
	s_add_i32 s9, s6, s9
	s_ashr_i32 s12, s9, 11
	s_lshr_b32 s9, s7, 28
	s_add_i32 s9, s6, s9
	s_lshl_b32 s78, s12, 2
	s_ashr_i32 s17, s9, 4
	s_lshr_b32 s20, s7, 25
	s_lshl_b32 s9, s12, 6
	s_add_i32 s20, s6, s20
	s_add_i32 s79, s78, s17
	s_ashr_i32 s20, s20, 7
	s_add_i32 s9, s79, s9
	v_readlane_b32 s24, v255, 30
	s_lshl_b32 s21, s12, 3
	s_add_i32 s90, s9, s20
	v_readlane_b32 s25, v255, 31
	v_readlane_b32 s26, v255, 18
	v_writelane_b32 v255, s9, 42
	s_sub_u32 s9, 0, s18
	s_subb_u32 s18, 0, s19
	s_add_u32 s28, s1, s9
	s_addc_u32 s29, s8, s18
	s_lshl_b64 s[8:9], s[6:7], 10
	s_add_u32 s1, s28, s8
	v_writelane_b32 v255, s1, 53
	v_writelane_b32 v255, s28, 44
	s_addc_u32 s1, s29, s9
	s_abs_i32 s91, s21
	v_cvt_f32_u32_e32 v0, s91
	v_writelane_b32 v255, s29, 45
	v_writelane_b32 v255, s1, 52
	v_writelane_b32 v255, s21, 50
	v_rcp_iflag_f32_e32 v0, v0
	s_add_i32 s1, s17, -1
	v_writelane_b32 v255, s1, 48
	s_bfe_i32 s1, s12, 0x1001c
	v_mul_f32_e32 v0, 0x4f7ffffe, v0
	v_cvt_u32_f32_e32 v0, v0
	v_writelane_b32 v255, s1, 54
	s_sub_i32 s1, 0, s91
	v_readfirstlane_b32 s7, v0
	s_mul_i32 s1, s1, s7
	s_mul_hi_u32 s1, s7, s1
	s_add_i32 s1, s7, s1
	v_writelane_b32 v255, s1, 55
	s_mul_hi_i32 s1, s6, 0x4d80
	s_mulk_i32 s6, 0x4d80
	s_add_u32 s4, s4, s6
	s_addc_u32 s1, s5, s1
	s_add_u32 s4, s4, 0x1842e400
	v_writelane_b32 v255, s4, 56
	s_addc_u32 s1, s1, 0
	v_writelane_b32 v255, s1, 57
	v_cmp_eq_u32_e32 vcc, 0, v146
	s_and_saveexec_b64 s[4:5], vcc
	s_cbranch_execz .Lmy_q0
	v_mov_b32_e32 v253, 1
	global_atomic_add v253, v48, v253, s[92:93] sc0
.Lmy_q0:
	s_or_b64 exec, exec, s[4:5]
	s_branch .LBB0_524

.LBB0_524:
	v_cmp_eq_u32_e32 vcc, 0, v146
	s_barrier
	s_and_saveexec_b64 s[4:5], vcc
	s_cbranch_execz .LBB0_528
	s_mov_b64 s[8:9], exec
	s_waitcnt vmcnt(0)
	v_mbcnt_lo_u32_b32 v0, s8, 0
	v_mbcnt_hi_u32_b32 v0, s9, v0
	v_cmp_eq_u32_e32 vcc, 0, v0
	s_and_saveexec_b64 s[6:7], vcc
	s_cbranch_execz .LBB0_527
	v_mov_b32_e32 v1, v253

.LBB0_528:
	s_or_b64 exec, exec, s[4:5]
	s_waitcnt vmcnt(0)
	v_mov_b32_e32 v0, s26
	s_waitcnt lgkmcnt(0)
	s_barrier
	ds_read_b32 v0, v0
	s_mov_b64 s[4:5], -1
	s_waitcnt lgkmcnt(0)
	v_cmp_le_i32_e32 vcc, s90, v0
	v_readfirstlane_b32 s1, v0
	s_cbranch_vccnz .LBB0_523
	v_mov_b32_e32 v146, v235
	v_cmp_eq_u32_e32 vcc, 0, v146
	s_and_saveexec_b64 s[6:7], vcc
	s_cbranch_execz .Lmy_q1
	v_mov_b32_e32 v253, 1
	global_atomic_add v253, v48, v253, s[92:93] sc0
.Lmy_q1:
	s_or_b64 exec, exec, s[6:7]
	s_mov_b64 s[6:7], -1
	v_readfirstlane_b32 s4, v146
	s_ashr_i32 s4, s4, 6
	v_and_b32_e32 v245, 63, v146
	s_cmp_le_i32 s78, s1
	s_cbranch_scc0 .LBB0_891
	s_cmp_ge_i32 s1, s79
	s_cbranch_scc0 .LBB0_541
	v_readlane_b32 s5, v255, 42
	s_cmp_ge_i32 s1, s5
	s_cbranch_scc0 .LBB0_533
	v_readlane_b32 s5, v255, 42
	s_sub_i32 s26, s1, s5
	s_lshl_b64 s[6:7], s[26:27], 12
	v_ashrrev_i32_e32 v147, 31, v146
	v_lshl_add_u64 v[80:81], s[6:7], 0, v[146:147]
	v_lshlrev_b64 v[0:1], 5, v[80:81]
	v_lshl_add_u64 v[0:1], s[94:95], 0, v[0:1]
	global_load_dwordx4 v[72:75], v[0:1], off offset:16
	global_load_dwordx4 v[76:79], v[0:1], off
	s_mov_b64 s[6:7], 0x200
	v_lshl_add_u64 v[70:71], v[80:81], 0, s[6:7]
	v_lshlrev_b64 v[0:1], 5, v[70:71]
	v_lshl_add_u64 v[0:1], s[94:95], 0, v[0:1]
	global_load_dwordx4 v[50:53], v[0:1], off offset:16
	global_load_dwordx4 v[54:57], v[0:1], off
	s_mov_b64 s[6:7], 0x400
	v_lshl_add_u64 v[68:69], v[80:81], 0, s[6:7]
	v_lshlrev_b64 v[0:1], 5, v[68:69]
	v_lshl_add_u64 v[0:1], s[94:95], 0, v[0:1]
	global_load_dwordx4 v[36:39], v[0:1], off offset:16
	global_load_dwordx4 v[44:47], v[0:1], off
	s_mov_b64 s[6:7], 0x600
	v_lshl_add_u64 v[66:67], v[80:81], 0, s[6:7]
	v_lshlrev_b64 v[0:1], 5, v[66:67]
	v_lshl_add_u64 v[0:1], s[94:95], 0, v[0:1]
	global_load_dwordx4 v[32:35], v[0:1], off offset:16
	global_load_dwordx4 v[40:43], v[0:1], off
	s_mov_b64 s[6:7], 0x800
	v_lshl_add_u64 v[60:61], v[80:81], 0, s[6:7]
	v_lshlrev_b64 v[0:1], 5, v[60:61]
	v_lshl_add_u64 v[0:1], s[94:95], 0, v[0:1]
	global_load_dwordx4 v[8:11], v[0:1], off offset:16
	global_load_dwordx4 v[20:23], v[0:1], off
	s_mov_b64 s[6:7], 0xa00
	v_lshl_add_u64 v[62:63], v[80:81], 0, s[6:7]
	v_lshlrev_b64 v[0:1], 5, v[62:63]
	v_lshl_add_u64 v[0:1], s[94:95], 0, v[0:1]
	global_load_dwordx4 v[12:15], v[0:1], off offset:16
	global_load_dwordx4 v[24:27], v[0:1], off
	s_mov_b64 s[6:7], 0xc00
	v_lshl_add_u64 v[58:59], v[80:81], 0, s[6:7]
	v_lshlrev_b64 v[0:1], 5, v[58:59]
	v_lshl_add_u64 v[4:5], s[94:95], 0, v[0:1]
	global_load_dwordx4 v[0:3], v[4:5], off offset:16
	s_nop 0
	global_load_dwordx4 v[4:7], v[4:5], off
	s_mov_b64 s[6:7], 0xe00
	v_lshl_add_u64 v[64:65], v[80:81], 0, s[6:7]
	v_lshlrev_b64 v[16:17], 5, v[64:65]
	v_lshl_add_u64 v[28:29], s[94:95], 0, v[16:17]
	global_load_dwordx4 v[16:19], v[28:29], off offset:16
	s_nop 0
	global_load_dwordx4 v[28:31], v[28:29], off
	v_lshl_add_u64 v[80:81], v[80:81], 4, s[96:97]
	v_lshl_add_u64 v[70:71], v[70:71], 4, s[96:97]
	v_readlane_b32 s26, v255, 18
	s_mov_b64 s[6:7], 0
	s_waitcnt vmcnt(14)
	v_and_b32_sdwa v49, v78, v236 dst_sel:DWORD dst_unused:UNUSED_PAD src0_sel:WORD_1 src1_sel:DWORD
	v_and_b32_sdwa v82, v76, v236 dst_sel:DWORD dst_unused:UNUSED_PAD src0_sel:WORD_1 src1_sel:DWORD
	v_add3_u32 v49, v78, v49, s75
	v_and_b32_sdwa v78, v79, v236 dst_sel:DWORD dst_unused:UNUSED_PAD src0_sel:WORD_1 src1_sel:DWORD
	v_add3_u32 v76, v76, v82, s75
	v_and_b32_sdwa v82, v77, v236 dst_sel:DWORD dst_unused:UNUSED_PAD src0_sel:WORD_1 src1_sel:DWORD
	v_add3_u32 v78, v79, v78, s75
	v_add3_u32 v77, v77, v82, s75
	v_and_b32_e32 v78, 0xffff0000, v78
	v_and_b32_e32 v79, 0xffff0000, v77
	v_or_b32_sdwa v77, v78, v49 dst_sel:DWORD dst_unused:UNUSED_PAD src0_sel:DWORD src1_sel:WORD_1
	v_and_b32_sdwa v49, v74, v236 dst_sel:DWORD dst_unused:UNUSED_PAD src0_sel:WORD_1 src1_sel:DWORD
	v_and_b32_sdwa v78, v72, v236 dst_sel:DWORD dst_unused:UNUSED_PAD src0_sel:WORD_1 src1_sel:DWORD
	v_add3_u32 v49, v74, v49, s75
	v_and_b32_sdwa v74, v75, v236 dst_sel:DWORD dst_unused:UNUSED_PAD src0_sel:WORD_1 src1_sel:DWORD
	v_add3_u32 v72, v72, v78, s75
	v_and_b32_sdwa v78, v73, v236 dst_sel:DWORD dst_unused:UNUSED_PAD src0_sel:WORD_1 src1_sel:DWORD
	v_add3_u32 v74, v75, v74, s75
	v_add3_u32 v73, v73, v78, s75
	v_and_b32_e32 v74, 0xffff0000, v74
	v_or_b32_sdwa v76, v79, v76 dst_sel:DWORD dst_unused:UNUSED_PAD src0_sel:DWORD src1_sel:WORD_1
	v_and_b32_e32 v73, 0xffff0000, v73
	v_or_b32_sdwa v79, v74, v49 dst_sel:DWORD dst_unused:UNUSED_PAD src0_sel:DWORD src1_sel:WORD_1
	s_waitcnt vmcnt(12)
	v_and_b32_sdwa v49, v56, v236 dst_sel:DWORD dst_unused:UNUSED_PAD src0_sel:WORD_1 src1_sel:DWORD
	v_or_b32_sdwa v78, v73, v72 dst_sel:DWORD dst_unused:UNUSED_PAD src0_sel:DWORD src1_sel:WORD_1
	v_and_b32_sdwa v72, v54, v236 dst_sel:DWORD dst_unused:UNUSED_PAD src0_sel:WORD_1 src1_sel:DWORD
	v_add3_u32 v49, v56, v49, s75
	v_and_b32_sdwa v56, v57, v236 dst_sel:DWORD dst_unused:UNUSED_PAD src0_sel:WORD_1 src1_sel:DWORD
	v_add3_u32 v54, v54, v72, s75
	v_and_b32_sdwa v72, v55, v236 dst_sel:DWORD dst_unused:UNUSED_PAD src0_sel:WORD_1 src1_sel:DWORD
	v_add3_u32 v56, v57, v56, s75
	v_add3_u32 v55, v55, v72, s75
	v_and_b32_e32 v56, 0xffff0000, v56
	v_and_b32_e32 v57, 0xffff0000, v55
	v_or_b32_sdwa v55, v56, v49 dst_sel:DWORD dst_unused:UNUSED_PAD src0_sel:DWORD src1_sel:WORD_1
	v_and_b32_sdwa v49, v52, v236 dst_sel:DWORD dst_unused:UNUSED_PAD src0_sel:WORD_1 src1_sel:DWORD
	v_add3_u32 v49, v52, v49, s75
	v_and_b32_sdwa v52, v53, v236 dst_sel:DWORD dst_unused:UNUSED_PAD src0_sel:WORD_1 src1_sel:DWORD
	v_add3_u32 v52, v53, v52, s75
	v_and_b32_e32 v52, 0xffff0000, v52
	v_or_b32_sdwa v54, v57, v54 dst_sel:DWORD dst_unused:UNUSED_PAD src0_sel:DWORD src1_sel:WORD_1
	v_or_b32_sdwa v57, v52, v49 dst_sel:DWORD dst_unused:UNUSED_PAD src0_sel:DWORD src1_sel:WORD_1
	s_waitcnt vmcnt(10)
	v_and_b32_sdwa v49, v46, v236 dst_sel:DWORD dst_unused:UNUSED_PAD src0_sel:WORD_1 src1_sel:DWORD
	v_and_b32_sdwa v52, v44, v236 dst_sel:DWORD dst_unused:UNUSED_PAD src0_sel:WORD_1 src1_sel:DWORD
	v_add3_u32 v46, v46, v49, s75
	v_and_b32_sdwa v49, v47, v236 dst_sel:DWORD dst_unused:UNUSED_PAD src0_sel:WORD_1 src1_sel:DWORD
	v_add3_u32 v44, v44, v52, s75
	v_and_b32_sdwa v52, v45, v236 dst_sel:DWORD dst_unused:UNUSED_PAD src0_sel:WORD_1 src1_sel:DWORD
	v_add3_u32 v47, v47, v49, s75
	v_add3_u32 v45, v45, v52, s75
	v_and_b32_e32 v47, 0xffff0000, v47
	v_and_b32_e32 v49, 0xffff0000, v45
	v_or_b32_sdwa v45, v47, v46 dst_sel:DWORD dst_unused:UNUSED_PAD src0_sel:DWORD src1_sel:WORD_1
	v_and_b32_sdwa v47, v36, v236 dst_sel:DWORD dst_unused:UNUSED_PAD src0_sel:WORD_1 src1_sel:DWORD
	v_and_b32_sdwa v46, v38, v236 dst_sel:DWORD dst_unused:UNUSED_PAD src0_sel:WORD_1 src1_sel:DWORD
	v_add3_u32 v36, v36, v47, s75
	v_and_b32_sdwa v47, v37, v236 dst_sel:DWORD dst_unused:UNUSED_PAD src0_sel:WORD_1 src1_sel:DWORD
	v_add3_u32 v38, v38, v46, s75
	v_and_b32_sdwa v46, v39, v236 dst_sel:DWORD dst_unused:UNUSED_PAD src0_sel:WORD_1 src1_sel:DWORD
	v_add3_u32 v37, v37, v47, s75
	v_add3_u32 v39, v39, v46, s75
	v_and_b32_e32 v37, 0xffff0000, v37
	v_and_b32_e32 v39, 0xffff0000, v39
	v_or_b32_sdwa v46, v37, v36 dst_sel:DWORD dst_unused:UNUSED_PAD src0_sel:DWORD src1_sel:WORD_1
	s_waitcnt vmcnt(8)
	v_and_b32_sdwa v37, v40, v236 dst_sel:DWORD dst_unused:UNUSED_PAD src0_sel:WORD_1 src1_sel:DWORD
	v_or_b32_sdwa v47, v39, v38 dst_sel:DWORD dst_unused:UNUSED_PAD src0_sel:DWORD src1_sel:WORD_1
	v_add3_u32 v38, v40, v37, s75
	v_and_b32_sdwa v37, v43, v236 dst_sel:DWORD dst_unused:UNUSED_PAD src0_sel:WORD_1 src1_sel:DWORD
	v_and_b32_sdwa v39, v41, v236 dst_sel:DWORD dst_unused:UNUSED_PAD src0_sel:WORD_1 src1_sel:DWORD
	v_and_b32_sdwa v36, v42, v236 dst_sel:DWORD dst_unused:UNUSED_PAD src0_sel:WORD_1 src1_sel:DWORD
	v_add3_u32 v37, v43, v37, s75
	v_add3_u32 v39, v41, v39, s75
	v_add3_u32 v36, v42, v36, s75
	v_and_b32_e32 v37, 0xffff0000, v37
	v_and_b32_e32 v39, 0xffff0000, v39
	v_or_b32_sdwa v37, v37, v36 dst_sel:DWORD dst_unused:UNUSED_PAD src0_sel:DWORD src1_sel:WORD_1
	v_or_b32_sdwa v36, v39, v38 dst_sel:DWORD dst_unused:UNUSED_PAD src0_sel:DWORD src1_sel:WORD_1
	v_and_b32_sdwa v38, v34, v236 dst_sel:DWORD dst_unused:UNUSED_PAD src0_sel:WORD_1 src1_sel:DWORD
	v_add3_u32 v34, v34, v38, s75
	v_and_b32_sdwa v38, v35, v236 dst_sel:DWORD dst_unused:UNUSED_PAD src0_sel:WORD_1 src1_sel:DWORD
	v_and_b32_sdwa v39, v32, v236 dst_sel:DWORD dst_unused:UNUSED_PAD src0_sel:WORD_1 src1_sel:DWORD
	v_add3_u32 v35, v35, v38, s75
	v_add3_u32 v32, v32, v39, s75
	v_and_b32_sdwa v39, v33, v236 dst_sel:DWORD dst_unused:UNUSED_PAD src0_sel:WORD_1 src1_sel:DWORD
	v_and_b32_e32 v35, 0xffff0000, v35
	v_add3_u32 v33, v33, v39, s75
	v_or_b32_sdwa v39, v35, v34 dst_sel:DWORD dst_unused:UNUSED_PAD src0_sel:DWORD src1_sel:WORD_1
	s_waitcnt vmcnt(6)
	v_and_b32_sdwa v34, v22, v236 dst_sel:DWORD dst_unused:UNUSED_PAD src0_sel:WORD_1 src1_sel:DWORD
	v_and_b32_sdwa v35, v20, v236 dst_sel:DWORD dst_unused:UNUSED_PAD src0_sel:WORD_1 src1_sel:DWORD
	v_add3_u32 v22, v22, v34, s75
	v_and_b32_sdwa v34, v23, v236 dst_sel:DWORD dst_unused:UNUSED_PAD src0_sel:WORD_1 src1_sel:DWORD
	v_add3_u32 v20, v20, v35, s75
	v_and_b32_sdwa v35, v21, v236 dst_sel:DWORD dst_unused:UNUSED_PAD src0_sel:WORD_1 src1_sel:DWORD
	v_add3_u32 v23, v23, v34, s75
	v_add3_u32 v21, v21, v35, s75
	v_and_b32_e32 v23, 0xffff0000, v23
	v_and_b32_e32 v34, 0xffff0000, v21
	v_or_b32_sdwa v21, v23, v22 dst_sel:DWORD dst_unused:UNUSED_PAD src0_sel:DWORD src1_sel:WORD_1
	v_and_b32_sdwa v23, v8, v236 dst_sel:DWORD dst_unused:UNUSED_PAD src0_sel:WORD_1 src1_sel:DWORD
	v_and_b32_sdwa v22, v10, v236 dst_sel:DWORD dst_unused:UNUSED_PAD src0_sel:WORD_1 src1_sel:DWORD
	v_add3_u32 v8, v8, v23, s75
	v_and_b32_sdwa v23, v9, v236 dst_sel:DWORD dst_unused:UNUSED_PAD src0_sel:WORD_1 src1_sel:DWORD
	v_add3_u32 v10, v10, v22, s75
	v_and_b32_sdwa v22, v11, v236 dst_sel:DWORD dst_unused:UNUSED_PAD src0_sel:WORD_1 src1_sel:DWORD
	v_add3_u32 v9, v9, v23, s75
	v_add3_u32 v11, v11, v22, s75
	v_and_b32_e32 v9, 0xffff0000, v9
	v_and_b32_e32 v11, 0xffff0000, v11
	v_or_b32_sdwa v22, v9, v8 dst_sel:DWORD dst_unused:UNUSED_PAD src0_sel:DWORD src1_sel:WORD_1
	s_waitcnt vmcnt(4)
	v_and_b32_sdwa v9, v24, v236 dst_sel:DWORD dst_unused:UNUSED_PAD src0_sel:WORD_1 src1_sel:DWORD
	v_or_b32_sdwa v23, v11, v10 dst_sel:DWORD dst_unused:UNUSED_PAD src0_sel:DWORD src1_sel:WORD_1
	v_add3_u32 v10, v24, v9, s75
	v_and_b32_sdwa v9, v27, v236 dst_sel:DWORD dst_unused:UNUSED_PAD src0_sel:WORD_1 src1_sel:DWORD
	v_and_b32_sdwa v11, v25, v236 dst_sel:DWORD dst_unused:UNUSED_PAD src0_sel:WORD_1 src1_sel:DWORD
	v_and_b32_sdwa v8, v26, v236 dst_sel:DWORD dst_unused:UNUSED_PAD src0_sel:WORD_1 src1_sel:DWORD
	v_add3_u32 v9, v27, v9, s75
	v_add3_u32 v11, v25, v11, s75
	v_add3_u32 v8, v26, v8, s75
	v_and_b32_e32 v9, 0xffff0000, v9
	v_and_b32_e32 v11, 0xffff0000, v11
	v_or_b32_sdwa v9, v9, v8 dst_sel:DWORD dst_unused:UNUSED_PAD src0_sel:DWORD src1_sel:WORD_1
	v_or_b32_sdwa v8, v11, v10 dst_sel:DWORD dst_unused:UNUSED_PAD src0_sel:DWORD src1_sel:WORD_1
	v_and_b32_sdwa v10, v14, v236 dst_sel:DWORD dst_unused:UNUSED_PAD src0_sel:WORD_1 src1_sel:DWORD
	v_and_b32_sdwa v11, v12, v236 dst_sel:DWORD dst_unused:UNUSED_PAD src0_sel:WORD_1 src1_sel:DWORD
	v_add3_u32 v12, v12, v11, s75
	v_add3_u32 v10, v14, v10, s75
	v_and_b32_sdwa v11, v15, v236 dst_sel:DWORD dst_unused:UNUSED_PAD src0_sel:WORD_1 src1_sel:DWORD
	v_and_b32_sdwa v14, v13, v236 dst_sel:DWORD dst_unused:UNUSED_PAD src0_sel:WORD_1 src1_sel:DWORD
	v_and_b32_e32 v33, 0xffff0000, v33
	v_add3_u32 v11, v15, v11, s75
	v_add3_u32 v13, v13, v14, s75
	v_or_b32_sdwa v38, v33, v32 dst_sel:DWORD dst_unused:UNUSED_PAD src0_sel:DWORD src1_sel:WORD_1
	v_lshl_add_u64 v[32:33], v[60:61], 4, s[96:97]
	v_or_b32_sdwa v20, v34, v20 dst_sel:DWORD dst_unused:UNUSED_PAD src0_sel:DWORD src1_sel:WORD_1
	v_and_b32_e32 v11, 0xffff0000, v11
	v_and_b32_e32 v13, 0xffff0000, v13
	global_store_dwordx4 v[32:33], v[20:23], off
	v_or_b32_sdwa v11, v11, v10 dst_sel:DWORD dst_unused:UNUSED_PAD src0_sel:DWORD src1_sel:WORD_1
	v_or_b32_sdwa v10, v13, v12 dst_sel:DWORD dst_unused:UNUSED_PAD src0_sel:DWORD src1_sel:WORD_1
	v_lshl_add_u64 v[20:21], v[62:63], 4, s[96:97]
	global_store_dwordx4 v[20:21], v[8:11], off
	v_and_b32_sdwa v56, v50, v236 dst_sel:DWORD dst_unused:UNUSED_PAD src0_sel:WORD_1 src1_sel:DWORD
	v_add3_u32 v50, v50, v56, s75
	s_waitcnt vmcnt(4)
	v_and_b32_sdwa v10, v6, v236 dst_sel:DWORD dst_unused:UNUSED_PAD src0_sel:WORD_1 src1_sel:DWORD
	v_and_b32_sdwa v11, v4, v236 dst_sel:DWORD dst_unused:UNUSED_PAD src0_sel:WORD_1 src1_sel:DWORD
	v_add3_u32 v6, v6, v10, s75
	v_and_b32_sdwa v10, v7, v236 dst_sel:DWORD dst_unused:UNUSED_PAD src0_sel:WORD_1 src1_sel:DWORD
	v_add3_u32 v4, v4, v11, s75
	v_and_b32_sdwa v11, v5, v236 dst_sel:DWORD dst_unused:UNUSED_PAD src0_sel:WORD_1 src1_sel:DWORD
	v_add3_u32 v7, v7, v10, s75
	v_add3_u32 v5, v5, v11, s75
	v_and_b32_e32 v7, 0xffff0000, v7
	v_and_b32_e32 v10, 0xffff0000, v5
	v_or_b32_sdwa v5, v7, v6 dst_sel:DWORD dst_unused:UNUSED_PAD src0_sel:DWORD src1_sel:WORD_1
	v_and_b32_sdwa v7, v0, v236 dst_sel:DWORD dst_unused:UNUSED_PAD src0_sel:WORD_1 src1_sel:DWORD
	v_and_b32_sdwa v6, v2, v236 dst_sel:DWORD dst_unused:UNUSED_PAD src0_sel:WORD_1 src1_sel:DWORD
	v_add3_u32 v0, v0, v7, s75
	v_and_b32_sdwa v7, v1, v236 dst_sel:DWORD dst_unused:UNUSED_PAD src0_sel:WORD_1 src1_sel:DWORD
	v_add3_u32 v2, v2, v6, s75
	v_and_b32_sdwa v6, v3, v236 dst_sel:DWORD dst_unused:UNUSED_PAD src0_sel:WORD_1 src1_sel:DWORD
	v_add3_u32 v1, v1, v7, s75
	v_add3_u32 v3, v3, v6, s75
	v_and_b32_e32 v1, 0xffff0000, v1
	v_and_b32_e32 v3, 0xffff0000, v3
	v_or_b32_sdwa v6, v1, v0 dst_sel:DWORD dst_unused:UNUSED_PAD src0_sel:DWORD src1_sel:WORD_1
	s_waitcnt vmcnt(2)
	v_and_b32_sdwa v1, v28, v236 dst_sel:DWORD dst_unused:UNUSED_PAD src0_sel:WORD_1 src1_sel:DWORD
	v_or_b32_sdwa v7, v3, v2 dst_sel:DWORD dst_unused:UNUSED_PAD src0_sel:DWORD src1_sel:WORD_1
	v_add3_u32 v2, v28, v1, s75
	v_and_b32_sdwa v1, v31, v236 dst_sel:DWORD dst_unused:UNUSED_PAD src0_sel:WORD_1 src1_sel:DWORD
	v_and_b32_sdwa v3, v29, v236 dst_sel:DWORD dst_unused:UNUSED_PAD src0_sel:WORD_1 src1_sel:DWORD
	v_and_b32_sdwa v0, v30, v236 dst_sel:DWORD dst_unused:UNUSED_PAD src0_sel:WORD_1 src1_sel:DWORD
	v_add3_u32 v1, v31, v1, s75
	v_add3_u32 v3, v29, v3, s75
	v_add3_u32 v0, v30, v0, s75
	v_and_b32_e32 v1, 0xffff0000, v1
	v_and_b32_e32 v3, 0xffff0000, v3
	v_and_b32_sdwa v56, v51, v236 dst_sel:DWORD dst_unused:UNUSED_PAD src0_sel:WORD_1 src1_sel:DWORD
	v_lshl_add_u64 v[8:9], v[58:59], 4, s[96:97]
	v_or_b32_sdwa v4, v10, v4 dst_sel:DWORD dst_unused:UNUSED_PAD src0_sel:DWORD src1_sel:WORD_1
	v_or_b32_sdwa v1, v1, v0 dst_sel:DWORD dst_unused:UNUSED_PAD src0_sel:DWORD src1_sel:WORD_1
	v_or_b32_sdwa v0, v3, v2 dst_sel:DWORD dst_unused:UNUSED_PAD src0_sel:DWORD src1_sel:WORD_1
	v_and_b32_sdwa v3, v16, v236 dst_sel:DWORD dst_unused:UNUSED_PAD src0_sel:WORD_1 src1_sel:DWORD
	v_add3_u32 v51, v51, v56, s75
	global_store_dwordx4 v[8:9], v[4:7], off
	v_and_b32_e32 v51, 0xffff0000, v51
	v_and_b32_sdwa v2, v18, v236 dst_sel:DWORD dst_unused:UNUSED_PAD src0_sel:WORD_1 src1_sel:DWORD
	v_add3_u32 v6, v16, v3, s75
	v_and_b32_sdwa v3, v19, v236 dst_sel:DWORD dst_unused:UNUSED_PAD src0_sel:WORD_1 src1_sel:DWORD
	v_and_b32_sdwa v7, v17, v236 dst_sel:DWORD dst_unused:UNUSED_PAD src0_sel:WORD_1 src1_sel:DWORD
	v_add3_u32 v3, v19, v3, s75
	v_add3_u32 v7, v17, v7, s75
	v_or_b32_sdwa v56, v51, v50 dst_sel:DWORD dst_unused:UNUSED_PAD src0_sel:DWORD src1_sel:WORD_1
	v_lshl_add_u64 v[50:51], v[68:69], 4, s[96:97]
	v_or_b32_sdwa v44, v49, v44 dst_sel:DWORD dst_unused:UNUSED_PAD src0_sel:DWORD src1_sel:WORD_1
	v_add3_u32 v2, v18, v2, s75
	v_and_b32_e32 v3, 0xffff0000, v3
	v_and_b32_e32 v7, 0xffff0000, v7
	global_store_dwordx4 v[50:51], v[44:47], off
	v_lshl_add_u64 v[4:5], v[64:65], 4, s[96:97]
	v_or_b32_sdwa v3, v3, v2 dst_sel:DWORD dst_unused:UNUSED_PAD src0_sel:DWORD src1_sel:WORD_1
	v_lshl_add_u64 v[44:45], v[66:67], 4, s[96:97]
	v_or_b32_sdwa v2, v7, v6 dst_sel:DWORD dst_unused:UNUSED_PAD src0_sel:DWORD src1_sel:WORD_1
	global_store_dwordx4 v[80:81], v[76:79], off
	global_store_dwordx4 v[70:71], v[54:57], off
	global_store_dwordx4 v[44:45], v[36:39], off
	global_store_dwordx4 v[4:5], v[0:3], off

.Lmy_dsa_fast:
	v_addc_co_u32_e32 v45, vcc, 0, v45, vcc
	global_load_dwordx4 v[44:47], v[44:45], off
	s_nop 0
	global_load_dwordx4 v[138:141], v[134:135], off offset:64
	s_waitcnt vmcnt(1)
	v_cndmask_b32_e64 v137, v47, 0, s[38:39]
	v_cndmask_b32_e64 v136, v46, 0, s[38:39]
	v_cndmask_b32_e64 v135, v45, 0, s[38:39]
	v_cndmask_b32_e64 v134, v44, 0, s[38:39]
	s_waitcnt vmcnt(0)
	v_cndmask_b32_e64 v47, v141, 0, s[38:39]
	v_cndmask_b32_e64 v46, v140, 0, s[38:39]
	v_cndmask_b32_e64 v45, v139, 0, s[38:39]
	v_cndmask_b32_e64 v44, v138, 0, s[38:39]
	ds_bpermute_b32 v102, v248, v0
	ds_bpermute_b32 v103, v248, v1
	ds_bpermute_b32 v104, v248, v2
	ds_bpermute_b32 v105, v248, v3
	ds_bpermute_b32 v106, v248, v4
	ds_bpermute_b32 v107, v248, v5
	ds_bpermute_b32 v108, v248, v6
	ds_bpermute_b32 v109, v248, v7
	ds_bpermute_b32 v110, v248, v8
	ds_bpermute_b32 v111, v248, v9
	ds_bpermute_b32 v112, v248, v10
	ds_bpermute_b32 v113, v248, v11
	ds_bpermute_b32 v114, v248, v12
	ds_bpermute_b32 v115, v248, v13
	ds_bpermute_b32 v116, v248, v14
	ds_bpermute_b32 v117, v248, v15
	s_waitcnt lgkmcnt(12)
	v_mfma_f32_16x16x32_bf16 v[140:143], v[102:105], v[134:137], 0
	s_waitcnt lgkmcnt(8)
	v_mfma_f32_16x16x32_bf16 v[142:145], v[106:109], v[44:47], v[140:143]
	ds_bpermute_b32 v102, v248, v16
	ds_bpermute_b32 v103, v248, v17
	ds_bpermute_b32 v104, v248, v18
	ds_bpermute_b32 v105, v248, v19
	ds_bpermute_b32 v106, v248, v20
	ds_bpermute_b32 v107, v248, v21
	ds_bpermute_b32 v108, v248, v22
	ds_bpermute_b32 v109, v248, v23
	s_nop 1
	v_pk_mul_f32 v[142:143], v[142:143], s[74:75] op_sel_hi:[1,0]
	v_pk_mul_f32 v[140:141], v[144:145], s[74:75] op_sel_hi:[1,0]
	v_max3_f32 v49, v142, s82, v143
	v_max3_f32 v49, v49, v140, v141
	s_waitcnt lgkmcnt(12)
	v_mfma_f32_16x16x32_bf16 v[154:157], v[110:113], v[134:137], 0
	s_waitcnt lgkmcnt(8)
	v_mfma_f32_16x16x32_bf16 v[154:157], v[114:117], v[44:47], v[154:157]
	ds_bpermute_b32 v110, v248, v24
	ds_bpermute_b32 v111, v248, v25
	ds_bpermute_b32 v112, v248, v26
	ds_bpermute_b32 v113, v248, v27
	ds_bpermute_b32 v114, v248, v28
	ds_bpermute_b32 v115, v248, v29
	ds_bpermute_b32 v116, v248, v30
	ds_bpermute_b32 v117, v248, v31
	s_nop 1
	v_pk_mul_f32 v[144:145], v[154:155], s[74:75] op_sel_hi:[1,0]
	v_pk_mul_f32 v[138:139], v[156:157], s[74:75] op_sel_hi:[1,0]
	v_max3_f32 v49, v49, v144, v145
	v_max3_f32 v49, v49, v138, v139
	s_waitcnt lgkmcnt(12)
	v_mfma_f32_16x16x32_bf16 v[156:159], v[102:105], v[134:137], 0
	s_waitcnt lgkmcnt(8)
	v_mfma_f32_16x16x32_bf16 v[158:161], v[106:109], v[44:47], v[156:159]
	ds_bpermute_b32 v102, v248, v32
	ds_bpermute_b32 v103, v248, v33
	ds_bpermute_b32 v104, v248, v34
	ds_bpermute_b32 v105, v248, v35
	ds_bpermute_b32 v106, v248, v36
	ds_bpermute_b32 v107, v248, v37
	ds_bpermute_b32 v108, v248, v38
	ds_bpermute_b32 v109, v248, v39
	s_nop 1
	v_pk_mul_f32 v[158:159], v[158:159], s[74:75] op_sel_hi:[1,0]
	v_pk_mul_f32 v[156:157], v[160:161], s[74:75] op_sel_hi:[1,0]
	v_max3_f32 v49, v49, v158, v159
	v_max3_f32 v49, v49, v156, v157
	s_waitcnt lgkmcnt(12)
	v_mfma_f32_16x16x32_bf16 v[160:163], v[110:113], v[134:137], 0
	s_waitcnt lgkmcnt(8)
	v_mfma_f32_16x16x32_bf16 v[160:163], v[114:117], v[44:47], v[160:163]
	ds_bpermute_b32 v110, v248, v40
	ds_bpermute_b32 v111, v248, v41
	ds_bpermute_b32 v112, v248, v42
	ds_bpermute_b32 v113, v248, v43
	ds_bpermute_b32 v114, v248, v50
	ds_bpermute_b32 v115, v248, v51
	ds_bpermute_b32 v116, v248, v52
	ds_bpermute_b32 v117, v248, v53
	s_nop 1
	v_pk_mul_f32 v[160:161], v[160:161], s[74:75] op_sel_hi:[1,0]
	v_pk_mul_f32 v[154:155], v[162:163], s[74:75] op_sel_hi:[1,0]
	v_max3_f32 v49, v49, v160, v161
	v_max3_f32 v49, v49, v154, v155
	s_waitcnt lgkmcnt(12)
	v_mfma_f32_16x16x32_bf16 v[164:167], v[102:105], v[134:137], 0
	s_waitcnt lgkmcnt(8)
	v_mfma_f32_16x16x32_bf16 v[166:169], v[106:109], v[44:47], v[164:167]
	ds_bpermute_b32 v102, v248, v54
	ds_bpermute_b32 v103, v248, v55
	ds_bpermute_b32 v104, v248, v56
	ds_bpermute_b32 v105, v248, v57
	ds_bpermute_b32 v106, v248, v58
	ds_bpermute_b32 v107, v248, v59
	ds_bpermute_b32 v108, v248, v60
	ds_bpermute_b32 v109, v248, v61
	s_nop 1
	v_pk_mul_f32 v[166:167], v[166:167], s[74:75] op_sel_hi:[1,0]
	v_pk_mul_f32 v[164:165], v[168:169], s[74:75] op_sel_hi:[1,0]
	v_max3_f32 v49, v49, v166, v167
	v_max3_f32 v49, v49, v164, v165
	s_waitcnt lgkmcnt(12)
	v_mfma_f32_16x16x32_bf16 v[168:171], v[110:113], v[134:137], 0
	s_waitcnt lgkmcnt(8)
	v_mfma_f32_16x16x32_bf16 v[168:171], v[114:117], v[44:47], v[168:171]
	ds_bpermute_b32 v110, v248, v62
	ds_bpermute_b32 v111, v248, v63
	ds_bpermute_b32 v112, v248, v64
	ds_bpermute_b32 v113, v248, v65
	ds_bpermute_b32 v114, v248, v66
	ds_bpermute_b32 v115, v248, v67
	ds_bpermute_b32 v116, v248, v68
	ds_bpermute_b32 v117, v248, v69
	s_nop 1
	v_pk_mul_f32 v[168:169], v[168:169], s[74:75] op_sel_hi:[1,0]
	v_pk_mul_f32 v[162:163], v[170:171], s[74:75] op_sel_hi:[1,0]
	v_max3_f32 v49, v49, v168, v169
	v_max3_f32 v49, v49, v162, v163
	s_waitcnt lgkmcnt(12)
	v_mfma_f32_16x16x32_bf16 v[172:175], v[102:105], v[134:137], 0
	s_waitcnt lgkmcnt(8)
	v_mfma_f32_16x16x32_bf16 v[174:177], v[106:109], v[44:47], v[172:175]
	s_nop 7
	v_pk_mul_f32 v[174:175], v[174:175], s[74:75] op_sel_hi:[1,0]
	v_pk_mul_f32 v[172:173], v[176:177], s[74:75] op_sel_hi:[1,0]
	v_max3_f32 v49, v49, v174, v175
	v_max3_f32 v49, v49, v172, v173
	s_waitcnt lgkmcnt(4)
	v_mfma_f32_16x16x32_bf16 v[176:179], v[110:113], v[134:137], 0
	s_waitcnt lgkmcnt(0)
	v_mfma_f32_16x16x32_bf16 v[176:179], v[114:117], v[44:47], v[176:179]
	s_nop 7
	v_pk_mul_f32 v[176:177], v[176:177], s[74:75] op_sel_hi:[1,0]
	v_pk_mul_f32 v[170:171], v[178:179], s[74:75] op_sel_hi:[1,0]
	v_max3_f32 v49, v49, v176, v177
	v_max3_f32 v49, v49, v170, v171
	s_lshl_b32 s6, s6, 9
	s_add_i32 s19, s6, 0
	s_add_i32 s19, s19, 0x20000
	v_lshl_add_u32 v151, v147, 1, s19
	ds_read_u16 v0, v151 offset:256
	ds_read_u16 v8, v151 offset:288
	ds_read_u16 v16, v151 offset:320
	ds_read_u16 v24, v151 offset:352
	ds_read_u16 v32, v151 offset:384
	ds_read_u16 v40, v151 offset:416
	ds_read_u16 v54, v151 offset:448
	ds_read_u16 v62, v151 offset:480
	s_waitcnt lgkmcnt(0)
	v_lshl_or_b32 v4, v0, 8, v246
	global_load_dwordx4 v[0:3], v4, s[50:51]
	global_load_dwordx4 v[4:7], v4, s[50:51] offset:64
	v_lshl_or_b32 v12, v8, 8, v246
	global_load_dwordx4 v[8:11], v12, s[50:51]
	global_load_dwordx4 v[12:15], v12, s[50:51] offset:64
	v_lshl_or_b32 v20, v16, 8, v246
	global_load_dwordx4 v[16:19], v20, s[50:51]
	global_load_dwordx4 v[20:23], v20, s[50:51] offset:64
	v_lshl_or_b32 v28, v24, 8, v246
	global_load_dwordx4 v[24:27], v28, s[50:51]
	global_load_dwordx4 v[28:31], v28, s[50:51] offset:64
	v_lshl_or_b32 v36, v32, 8, v246
	global_load_dwordx4 v[32:35], v36, s[50:51]
	global_load_dwordx4 v[36:39], v36, s[50:51] offset:64
	v_lshl_or_b32 v50, v40, 8, v246
	global_load_dwordx4 v[40:43], v50, s[50:51]
	global_load_dwordx4 v[50:53], v50, s[50:51] offset:64
	v_lshl_or_b32 v58, v54, 8, v246
	global_load_dwordx4 v[54:57], v58, s[50:51]
	global_load_dwordx4 v[58:61], v58, s[50:51] offset:64
	v_lshl_or_b32 v66, v62, 8, v246
	global_load_dwordx4 v[62:65], v66, s[50:51]
	global_load_dwordx4 v[66:69], v66, s[50:51] offset:64
	s_xor_b64 s[6:7], s[44:45], -1
	s_ashr_i32 s53, s52, 31
	s_waitcnt vmcnt(15)
	ds_bpermute_b32 v102, v248, v0
	ds_bpermute_b32 v103, v248, v1
	ds_bpermute_b32 v104, v248, v2
	ds_bpermute_b32 v105, v248, v3
	s_waitcnt vmcnt(14)
	ds_bpermute_b32 v106, v248, v4
	ds_bpermute_b32 v107, v248, v5
	ds_bpermute_b32 v108, v248, v6
	ds_bpermute_b32 v109, v248, v7
	s_waitcnt vmcnt(13)
	ds_bpermute_b32 v110, v248, v8
	ds_bpermute_b32 v111, v248, v9
	ds_bpermute_b32 v112, v248, v10
	ds_bpermute_b32 v113, v248, v11
	s_waitcnt vmcnt(12)
	ds_bpermute_b32 v114, v248, v12
	ds_bpermute_b32 v115, v248, v13
	ds_bpermute_b32 v116, v248, v14
	ds_bpermute_b32 v117, v248, v15
	s_waitcnt lgkmcnt(12)
	v_mfma_f32_16x16x32_bf16 v[180:183], v[102:105], v[134:137], 0
	s_waitcnt lgkmcnt(8)
	v_mfma_f32_16x16x32_bf16 v[182:185], v[106:109], v[44:47], v[180:183]
	s_waitcnt vmcnt(11)
	ds_bpermute_b32 v102, v248, v16
	ds_bpermute_b32 v103, v248, v17
	ds_bpermute_b32 v104, v248, v18
	ds_bpermute_b32 v105, v248, v19
	s_waitcnt vmcnt(10)
	ds_bpermute_b32 v106, v248, v20
	ds_bpermute_b32 v107, v248, v21
	ds_bpermute_b32 v108, v248, v22
	ds_bpermute_b32 v109, v248, v23
	s_nop 1
	v_pk_mul_f32 v[182:183], v[182:183], s[74:75] op_sel_hi:[1,0]
	v_pk_mul_f32 v[180:181], v[184:185], s[74:75] op_sel_hi:[1,0]
	v_max3_f32 v49, v49, v182, v183
	v_max3_f32 v49, v49, v180, v181
	s_waitcnt lgkmcnt(12)
	v_mfma_f32_16x16x32_bf16 v[184:187], v[110:113], v[134:137], 0
	s_waitcnt lgkmcnt(8)
	v_mfma_f32_16x16x32_bf16 v[184:187], v[114:117], v[44:47], v[184:187]
	s_waitcnt vmcnt(9)
	ds_bpermute_b32 v110, v248, v24
	ds_bpermute_b32 v111, v248, v25
	ds_bpermute_b32 v112, v248, v26
	ds_bpermute_b32 v113, v248, v27
	s_waitcnt vmcnt(8)
	ds_bpermute_b32 v114, v248, v28
	ds_bpermute_b32 v115, v248, v29
	ds_bpermute_b32 v116, v248, v30
	ds_bpermute_b32 v117, v248, v31
	s_nop 1
	v_pk_mul_f32 v[184:185], v[184:185], s[74:75] op_sel_hi:[1,0]
	v_pk_mul_f32 v[178:179], v[186:187], s[74:75] op_sel_hi:[1,0]
	v_max3_f32 v49, v49, v184, v185
	v_max3_f32 v49, v49, v178, v179
	s_waitcnt lgkmcnt(12)
	v_mfma_f32_16x16x32_bf16 v[188:191], v[102:105], v[134:137], 0
	s_waitcnt lgkmcnt(8)
	v_mfma_f32_16x16x32_bf16 v[190:193], v[106:109], v[44:47], v[188:191]
	s_waitcnt vmcnt(7)
	ds_bpermute_b32 v102, v248, v32
	ds_bpermute_b32 v103, v248, v33
	ds_bpermute_b32 v104, v248, v34
	ds_bpermute_b32 v105, v248, v35
	s_waitcnt vmcnt(6)
	ds_bpermute_b32 v106, v248, v36
	ds_bpermute_b32 v107, v248, v37
	ds_bpermute_b32 v108, v248, v38
	ds_bpermute_b32 v109, v248, v39
	s_nop 1
	v_pk_mul_f32 v[190:191], v[190:191], s[74:75] op_sel_hi:[1,0]
	v_pk_mul_f32 v[188:189], v[192:193], s[74:75] op_sel_hi:[1,0]
	v_max3_f32 v49, v49, v190, v191
	v_max3_f32 v49, v49, v188, v189
	s_waitcnt lgkmcnt(12)
	v_mfma_f32_16x16x32_bf16 v[192:195], v[110:113], v[134:137], 0
	s_waitcnt lgkmcnt(8)
	v_mfma_f32_16x16x32_bf16 v[192:195], v[114:117], v[44:47], v[192:195]
	s_waitcnt vmcnt(5)
	ds_bpermute_b32 v110, v248, v40
	ds_bpermute_b32 v111, v248, v41
	ds_bpermute_b32 v112, v248, v42
	ds_bpermute_b32 v113, v248, v43
	s_waitcnt vmcnt(4)
	ds_bpermute_b32 v114, v248, v50
	ds_bpermute_b32 v115, v248, v51
	ds_bpermute_b32 v116, v248, v52
	ds_bpermute_b32 v117, v248, v53
	s_nop 1
	v_pk_mul_f32 v[192:193], v[192:193], s[74:75] op_sel_hi:[1,0]
	v_pk_mul_f32 v[186:187], v[194:195], s[74:75] op_sel_hi:[1,0]
	v_max3_f32 v49, v49, v192, v193
	v_max3_f32 v49, v49, v186, v187
	s_waitcnt lgkmcnt(12)
	v_mfma_f32_16x16x32_bf16 v[196:199], v[102:105], v[134:137], 0
	s_waitcnt lgkmcnt(8)
	v_mfma_f32_16x16x32_bf16 v[196:199], v[106:109], v[44:47], v[196:199]
	s_waitcnt vmcnt(3)
	ds_bpermute_b32 v102, v248, v54
	ds_bpermute_b32 v103, v248, v55
	ds_bpermute_b32 v104, v248, v56
	ds_bpermute_b32 v105, v248, v57
	s_waitcnt vmcnt(2)
	ds_bpermute_b32 v106, v248, v58
	ds_bpermute_b32 v107, v248, v59
	ds_bpermute_b32 v108, v248, v60
	ds_bpermute_b32 v109, v248, v61
	s_nop 1
	v_pk_mul_f32 v[200:201], v[196:197], s[74:75] op_sel_hi:[1,0]
	v_pk_mul_f32 v[198:199], v[198:199], s[74:75] op_sel_hi:[1,0]
	v_max3_f32 v49, v49, v200, v201
	v_max3_f32 v49, v49, v198, v199
	s_waitcnt lgkmcnt(12)
	v_mfma_f32_16x16x32_bf16 v[194:197], v[110:113], v[134:137], 0
	s_waitcnt lgkmcnt(8)
	v_mfma_f32_16x16x32_bf16 v[194:197], v[114:117], v[44:47], v[194:197]
	s_waitcnt vmcnt(1)
	ds_bpermute_b32 v110, v248, v62
	ds_bpermute_b32 v111, v248, v63
	ds_bpermute_b32 v112, v248, v64
	ds_bpermute_b32 v113, v248, v65
	s_waitcnt vmcnt(0)
	ds_bpermute_b32 v114, v248, v66
	ds_bpermute_b32 v115, v248, v67
	ds_bpermute_b32 v116, v248, v68
	ds_bpermute_b32 v117, v248, v69
	s_nop 1
	v_pk_mul_f32 v[202:203], v[194:195], s[74:75] op_sel_hi:[1,0]
	v_pk_mul_f32 v[194:195], v[196:197], s[74:75] op_sel_hi:[1,0]
	v_max3_f32 v49, v49, v202, v203
	v_max3_f32 v49, v49, v194, v195
	s_waitcnt lgkmcnt(12)
	v_mfma_f32_16x16x32_bf16 v[206:209], v[102:105], v[134:137], 0
	s_waitcnt lgkmcnt(8)
	v_mfma_f32_16x16x32_bf16 v[206:209], v[106:109], v[44:47], v[206:209]
	s_nop 7
	v_pk_mul_f32 v[212:213], v[206:207], s[74:75] op_sel_hi:[1,0]
	v_pk_mul_f32 v[210:211], v[208:209], s[74:75] op_sel_hi:[1,0]
	v_max3_f32 v49, v49, v212, v213
	v_max3_f32 v49, v49, v210, v211
	s_waitcnt lgkmcnt(4)
	v_mfma_f32_16x16x32_bf16 v[134:137], v[110:113], v[134:137], 0
	s_waitcnt lgkmcnt(0)
	v_mfma_f32_16x16x32_bf16 v[44:47], v[114:117], v[44:47], v[134:137]
	s_nop 7
	v_pk_mul_f32 v[44:45], v[44:45], s[74:75] op_sel_hi:[1,0]
	s_nop 0
	v_max3_f32 v49, v49, v44, v45
	v_pk_mul_f32 v[204:205], v[46:47], s[74:75] op_sel_hi:[1,0]
	s_nop 0
	v_max3_f32 v49, v49, v204, v205
	s_and_b64 vcc, exec, s[44:45]
	s_cbranch_vccz .Lmy_dsa_fast_nk_skip
	ds_read_u16 v0, v251
	ds_read_u16 v8, v251 offset:32
	ds_read_u16 v16, v251 offset:64
	ds_read_u16 v24, v251 offset:96
	ds_read_u16 v32, v251 offset:128
	ds_read_u16 v40, v251 offset:160
	ds_read_u16 v54, v251 offset:192
	ds_read_u16 v62, v251 offset:224
	s_waitcnt lgkmcnt(0)
	v_lshl_or_b32 v4, v0, 8, v246
	global_load_dwordx4 v[0:3], v4, s[50:51]
	global_load_dwordx4 v[4:7], v4, s[50:51] offset:64
	v_lshl_or_b32 v12, v8, 8, v246
	global_load_dwordx4 v[8:11], v12, s[50:51]
	global_load_dwordx4 v[12:15], v12, s[50:51] offset:64
	v_lshl_or_b32 v20, v16, 8, v246
	global_load_dwordx4 v[16:19], v20, s[50:51]
	global_load_dwordx4 v[20:23], v20, s[50:51] offset:64
	v_lshl_or_b32 v28, v24, 8, v246
	global_load_dwordx4 v[24:27], v28, s[50:51]
	global_load_dwordx4 v[28:31], v28, s[50:51] offset:64
	v_lshl_or_b32 v36, v32, 8, v246
	global_load_dwordx4 v[32:35], v36, s[50:51]
	global_load_dwordx4 v[36:39], v36, s[50:51] offset:64
	v_lshl_or_b32 v50, v40, 8, v246
	global_load_dwordx4 v[40:43], v50, s[50:51]
	global_load_dwordx4 v[50:53], v50, s[50:51] offset:64
	v_lshl_or_b32 v58, v54, 8, v246
	global_load_dwordx4 v[54:57], v58, s[50:51]
	global_load_dwordx4 v[58:61], v58, s[50:51] offset:64
	v_lshl_or_b32 v66, v62, 8, v246
	global_load_dwordx4 v[62:65], v66, s[50:51]
	global_load_dwordx4 v[66:69], v66, s[50:51] offset:64
.Lmy_dsa_fast_nk_skip:
	v_lshl_add_u32 v151, v247, 1, s19
	ds_read_u16 v46, v151
	ds_read_u16 v47, v151 offset:16
	ds_read_u16 v126, v151 offset:32
	ds_read_u16 v127, v151 offset:48
	s_waitcnt lgkmcnt(3)
	v_lshl_or_b32 v46, v46, 8, v250
	s_waitcnt lgkmcnt(2)
	v_lshl_or_b32 v47, v47, 8, v250
	global_load_dwordx4 v[102:105], v46, s[50:51] offset:128
	global_load_dwordx4 v[110:113], v47, s[50:51] offset:128
	s_waitcnt lgkmcnt(1)
	v_lshl_or_b32 v46, v126, 8, v250
	s_waitcnt lgkmcnt(0)
	v_lshl_or_b32 v47, v127, 8, v250
	global_load_dwordx4 v[126:129], v46, s[50:51] offset:128
	global_load_dwordx4 v[130:133], v47, s[50:51] offset:128
	ds_read_u16 v46, v151 offset:64
	ds_read_u16 v47, v151 offset:80
	ds_read_u16 v118, v151 offset:96
	ds_read_u16 v119, v151 offset:112
	s_waitcnt lgkmcnt(3)
	v_lshl_or_b32 v46, v46, 8, v250
	s_waitcnt lgkmcnt(2)
	v_lshl_or_b32 v47, v47, 8, v250
	global_load_dwordx4 v[86:89], v46, s[50:51] offset:128
	global_load_dwordx4 v[94:97], v47, s[50:51] offset:128
	s_waitcnt lgkmcnt(1)
	v_lshl_or_b32 v46, v118, 8, v250
	s_waitcnt lgkmcnt(0)
	v_lshl_or_b32 v47, v119, 8, v250
	global_load_dwordx4 v[118:121], v46, s[50:51] offset:128
	global_load_dwordx4 v[122:125], v47, s[50:51] offset:128
	ds_read_u16 v46, v151 offset:128
	ds_read_u16 v47, v151 offset:144
	ds_read_u16 v106, v151 offset:160
	ds_read_u16 v107, v151 offset:176
	s_waitcnt lgkmcnt(3)
	v_lshl_or_b32 v46, v46, 8, v250
	s_waitcnt lgkmcnt(2)
	v_lshl_or_b32 v47, v47, 8, v250
	global_load_dwordx4 v[78:81], v46, s[50:51] offset:128
	global_load_dwordx4 v[82:85], v47, s[50:51] offset:128
	s_waitcnt lgkmcnt(1)
	v_lshl_or_b32 v46, v106, 8, v250
	s_waitcnt lgkmcnt(0)
	v_lshl_or_b32 v47, v107, 8, v250
	global_load_dwordx4 v[106:109], v46, s[50:51] offset:128
	global_load_dwordx4 v[114:117], v47, s[50:51] offset:128
	ds_read_u16 v46, v151 offset:192
	ds_read_u16 v47, v151 offset:208
	ds_read_u16 v90, v151 offset:224
	ds_read_u16 v91, v151 offset:240
	s_waitcnt lgkmcnt(3)
	v_lshl_or_b32 v46, v46, 8, v250
	s_waitcnt lgkmcnt(2)
	v_lshl_or_b32 v47, v47, 8, v250
	global_load_dwordx4 v[70:73], v46, s[50:51] offset:128
	global_load_dwordx4 v[74:77], v47, s[50:51] offset:128
	s_waitcnt lgkmcnt(1)
	v_lshl_or_b32 v46, v90, 8, v250
	s_waitcnt lgkmcnt(0)
	v_lshl_or_b32 v47, v91, 8, v250
	global_load_dwordx4 v[90:93], v46, s[50:51] offset:128
	global_load_dwordx4 v[98:101], v47, s[50:51] offset:128
	v_mov_b32_e32 v46, v49
	s_nop 1
	v_permlane32_swap_b32 v49, v46
	s_nop 1
	s_nop 0
	v_max_f32_e32 v46, v46, v46
	v_max_f32_e32 v47, v49, v49
	v_max_f32_e32 v46, v47, v46
	v_mov_b32_e32 v47, v46
	s_nop 1
	v_permlane16_swap_b32 v46, v47
	s_nop 1
	s_nop 0
	v_max_f32_e32 v47, v47, v47
	v_max_f32_e32 v46, v46, v46
	v_max_f32_e32 v49, v46, v47
	s_mov_b32 s32, 0x3fb8aa3b
	v_mul_f32_e32 v49, 0xbfb8aa3b, v49
	v_fma_f32 v135, v141, s32, v49
	v_fma_f32 v141, v158, s32, v49
	v_exp_f32_e32 v226, v141
	v_fma_f32 v141, v159, s32, v49
	v_exp_f32_e32 v227, v141
	v_fma_f32 v141, v156, s32, v49
	v_exp_f32_e32 v228, v141
	v_fma_f32 v141, v157, s32, v49
	v_exp_f32_e32 v229, v141
	v_fma_f32 v141, v160, s32, v49
	v_exp_f32_e32 v230, v141
	v_fma_f32 v141, v161, s32, v49
	v_exp_f32_e32 v231, v141
	v_fma_f32 v141, v154, s32, v49
	v_exp_f32_e32 v232, v141
	v_fma_f32 v141, v155, s32, v49
	v_exp_f32_e32 v233, v141
	v_fma_f32 v141, v166, s32, v49
	v_exp_f32_e32 v218, v141
	v_fma_f32 v141, v167, s32, v49
	v_exp_f32_e32 v219, v141
	v_fma_f32 v141, v164, s32, v49
	v_exp_f32_e32 v220, v141
	v_fma_f32 v141, v165, s32, v49
	v_exp_f32_e32 v221, v141
	v_fma_f32 v141, v168, s32, v49
	v_exp_f32_e32 v222, v141
	v_fma_f32 v141, v169, s32, v49
	v_exp_f32_e32 v223, v141
	v_fma_f32 v141, v162, s32, v49
	v_exp_f32_e32 v224, v141
	v_fma_f32 v141, v163, s32, v49
	v_exp_f32_e32 v225, v141
	v_fma_f32 v141, v174, s32, v49
	v_exp_f32_e32 v206, v141
	v_fma_f32 v141, v175, s32, v49
	v_exp_f32_e32 v207, v141
	v_fma_f32 v141, v172, s32, v49
	v_fma_f32 v46, v142, s32, v49
	v_exp_f32_e32 v208, v141
	v_fma_f32 v141, v173, s32, v49
	v_fma_f32 v47, v143, s32, v49
	v_exp_f32_e32 v46, v46
	v_fma_f32 v134, v140, s32, v49
	v_exp_f32_e32 v209, v141
	v_fma_f32 v141, v176, s32, v49
	v_exp_f32_e32 v47, v47
	v_exp_f32_e32 v134, v134
	v_exp_f32_e32 v214, v141
	v_fma_f32 v141, v177, s32, v49
	v_exp_f32_e32 v135, v135
	v_add_f32_e32 v136, 0, v46
	v_exp_f32_e32 v215, v141
	v_fma_f32 v141, v170, s32, v49
	v_add_f32_e32 v136, v47, v136
	v_add_f32_e32 v136, v134, v136
	v_exp_f32_e32 v216, v141
	v_fma_f32 v141, v171, s32, v49
	v_add_f32_e32 v140, v135, v136
	v_fma_f32 v136, v144, s32, v49
	v_fma_f32 v137, v145, s32, v49
	v_exp_f32_e32 v217, v141
	v_fma_f32 v141, v182, s32, v49
	v_exp_f32_e32 v136, v136
	v_fma_f32 v138, v138, s32, v49
	v_exp_f32_e32 v137, v137
	v_fma_f32 v139, v139, s32, v49
	v_exp_f32_e32 v182, v141
	v_fma_f32 v141, v183, s32, v49
	v_exp_f32_e32 v138, v138
	v_exp_f32_e32 v139, v139
	v_exp_f32_e32 v183, v141
	v_fma_f32 v141, v180, s32, v49
	v_add_f32_e32 v140, v136, v140
	v_add_f32_e32 v140, v137, v140
	v_exp_f32_e32 v180, v141
	v_fma_f32 v141, v181, s32, v49
	v_add_f32_e32 v140, v138, v140
	v_add_f32_e32 v140, v139, v140
	v_exp_f32_e32 v181, v141
	v_fma_f32 v141, v184, s32, v49
	v_add_f32_e32 v140, v226, v140
	v_add_f32_e32 v140, v227, v140
	v_exp_f32_e32 v184, v141
	v_fma_f32 v141, v185, s32, v49
	v_add_f32_e32 v140, v228, v140
	v_add_f32_e32 v140, v229, v140
	v_exp_f32_e32 v185, v141
	v_fma_f32 v141, v178, s32, v49
	v_add_f32_e32 v140, v230, v140
	v_add_f32_e32 v140, v231, v140
	v_exp_f32_e32 v196, v141
	v_fma_f32 v141, v179, s32, v49
	v_add_f32_e32 v140, v232, v140
	v_add_f32_e32 v140, v233, v140
	v_exp_f32_e32 v197, v141
	v_fma_f32 v141, v190, s32, v49
	v_add_f32_e32 v140, v218, v140
	v_add_f32_e32 v140, v219, v140
	v_exp_f32_e32 v172, v141
	v_fma_f32 v141, v191, s32, v49
	v_add_f32_e32 v140, v220, v140
	v_add_f32_e32 v140, v221, v140
	v_exp_f32_e32 v173, v141
	v_fma_f32 v141, v188, s32, v49
	v_add_f32_e32 v140, v222, v140
	v_add_f32_e32 v140, v223, v140
	v_exp_f32_e32 v174, v141
	v_fma_f32 v141, v189, s32, v49
	v_add_f32_e32 v140, v224, v140
	v_add_f32_e32 v140, v225, v140
	v_exp_f32_e32 v175, v141
	v_fma_f32 v141, v192, s32, v49
	v_add_f32_e32 v140, v206, v140
	v_add_f32_e32 v140, v207, v140
	v_exp_f32_e32 v176, v141
	v_fma_f32 v141, v193, s32, v49
	v_add_f32_e32 v140, v208, v140
	v_add_f32_e32 v140, v209, v140
	v_exp_f32_e32 v177, v141
	v_fma_f32 v141, v186, s32, v49
	v_add_f32_e32 v140, v214, v140
	v_add_f32_e32 v140, v215, v140
	v_exp_f32_e32 v178, v141
	v_fma_f32 v141, v187, s32, v49
	v_add_f32_e32 v140, v216, v140
	v_add_f32_e32 v140, v217, v140
	v_exp_f32_e32 v179, v141
	v_fma_f32 v141, v200, s32, v49
	v_add_f32_e32 v140, v182, v140
	v_add_f32_e32 v140, v183, v140
	v_exp_f32_e32 v164, v141
	v_fma_f32 v141, v201, s32, v49
	v_add_f32_e32 v140, v180, v140
	v_add_f32_e32 v140, v181, v140
	v_exp_f32_e32 v165, v141
	v_fma_f32 v141, v198, s32, v49
	v_add_f32_e32 v140, v184, v140
	v_add_f32_e32 v140, v185, v140
	v_exp_f32_e32 v166, v141
	v_fma_f32 v141, v199, s32, v49
	v_add_f32_e32 v140, v196, v140
	v_add_f32_e32 v140, v197, v140
	v_exp_f32_e32 v167, v141
	v_fma_f32 v141, v202, s32, v49
	v_add_f32_e32 v140, v172, v140
	v_add_f32_e32 v140, v173, v140
	v_exp_f32_e32 v168, v141
	v_fma_f32 v141, v203, s32, v49
	v_add_f32_e32 v140, v174, v140
	v_add_f32_e32 v140, v175, v140
	v_exp_f32_e32 v169, v141
	v_fma_f32 v141, v194, s32, v49
	v_add_f32_e32 v140, v176, v140
	v_add_f32_e32 v140, v177, v140
	v_exp_f32_e32 v170, v141
	v_fma_f32 v141, v195, s32, v49
	v_add_f32_e32 v140, v178, v140
	v_add_f32_e32 v140, v179, v140
	v_exp_f32_e32 v171, v141
	v_fma_f32 v141, v212, s32, v49
	v_add_f32_e32 v140, v164, v140
	v_add_f32_e32 v140, v165, v140
	v_exp_f32_e32 v154, v141
	v_fma_f32 v141, v213, s32, v49
	v_add_f32_e32 v140, v166, v140
	v_add_f32_e32 v140, v167, v140
	v_exp_f32_e32 v155, v141
	v_fma_f32 v141, v210, s32, v49
	v_fma_f32 v44, v44, s32, v49
	v_add_f32_e32 v140, v168, v140
	v_add_f32_e32 v140, v169, v140
	v_exp_f32_e32 v156, v141
	v_fma_f32 v141, v211, s32, v49
	v_exp_f32_e32 v158, v44
	v_fma_f32 v44, v45, s32, v49
	v_add_f32_e32 v140, v170, v140
	v_add_f32_e32 v140, v171, v140
	v_exp_f32_e32 v157, v141
	v_exp_f32_e32 v159, v44
	v_fma_f32 v44, v204, s32, v49
	v_add_f32_e32 v140, v154, v140
	v_add_f32_e32 v140, v155, v140
	v_exp_f32_e32 v160, v44
	v_fma_f32 v44, v205, s32, v49
	v_add_f32_e32 v140, v156, v140
	v_add_f32_e32 v140, v157, v140
	v_exp_f32_e32 v161, v44
	v_add_f32_e32 v44, v158, v140
	v_add_f32_e32 v44, v159, v44
	v_add_f32_e32 v44, v160, v44
	v_add_f32_e32 v44, v161, v44
	v_mov_b32_e32 v45, v44
	s_nop 1
	v_permlane32_swap_b32 v44, v45
	s_nop 1
	s_nop 0
	v_add_f32_e32 v44, v44, v45
	v_mov_b32_e32 v45, v44
	s_nop 1
	v_permlane16_swap_b32 v44, v45
	s_nop 1
	s_nop 0
	v_add_f32_e32 v44, v44, v45
	v_div_scale_f32 v45, s[20:21], v44, v44, 1.0
	v_rcp_f32_e32 v49, v45
	s_nop 0
	v_fma_f32 v140, -v45, v49, 1.0
	v_fmac_f32_e32 v49, v140, v49
	v_div_scale_f32 v140, vcc, 1.0, v44, 1.0
	v_mul_f32_e32 v141, v140, v49
	v_fma_f32 v142, -v45, v141, v140
	v_fmac_f32_e32 v141, v142, v49
	v_fma_f32 v45, -v45, v141, v140
	v_div_fmas_f32 v45, v45, v49, v141
	v_div_fixup_f32 v162, v45, v44, 1.0
	s_waitcnt vmcnt(15)
	ds_write_b128 v252, v[102:105]
	s_waitcnt vmcnt(14)
	ds_write_b128 v252, v[110:113] offset:1152
	s_waitcnt vmcnt(13)
	ds_write_b128 v252, v[126:129] offset:2304
	s_waitcnt vmcnt(12)
	ds_write_b128 v252, v[130:133] offset:3456
	ds_read_u16 v44, v151 offset:256
	ds_read_u16 v45, v151 offset:272
	ds_read_u16 v49, v151 offset:288
	ds_read_u16 v126, v151 offset:304
	s_waitcnt lgkmcnt(3)
	v_lshl_or_b32 v44, v44, 8, v250
	s_waitcnt lgkmcnt(2)
	v_lshl_or_b32 v45, v45, 8, v250
	global_load_dwordx4 v[102:105], v44, s[50:51] offset:128
	global_load_dwordx4 v[110:113], v45, s[50:51] offset:128
	s_waitcnt lgkmcnt(1)
	v_lshl_or_b32 v44, v49, 8, v250
	s_waitcnt lgkmcnt(0)
	v_lshl_or_b32 v45, v126, 8, v250
	global_load_dwordx4 v[126:129], v44, s[50:51] offset:128
	global_load_dwordx4 v[130:133], v45, s[50:51] offset:128
	v_pk_mul_f32 v[44:45], v[162:163], v[46:47] op_sel_hi:[0,1]
	v_pk_mul_f32 v[46:47], v[162:163], v[134:135] op_sel_hi:[0,1]
	v_cvt_pk_bf16_f32 v44, v44, v45
	v_cvt_pk_bf16_f32 v45, v46, v47
	v_pk_mul_f32 v[46:47], v[162:163], v[136:137] op_sel_hi:[0,1]
	v_pk_mul_f32 v[134:135], v[162:163], v[138:139] op_sel_hi:[0,1]
	s_waitcnt lgkmcnt(0)
	v_cvt_pk_bf16_f32 v46, v46, v47
	v_cvt_pk_bf16_f32 v47, v134, v135
	ds_read_b64_tr_b16 v[136:137], v249 offset:2304
	ds_read_b64_tr_b16 v[134:135], v249
	ds_read_b64_tr_b16 v[138:139], v249 offset:32
	ds_read_b64_tr_b16 v[186:187], v249 offset:64
	ds_read_b64_tr_b16 v[190:191], v249 offset:96
	ds_read_b64_tr_b16 v[140:141], v249 offset:2336
	ds_read_b64_tr_b16 v[188:189], v249 offset:2368
	ds_read_b64_tr_b16 v[192:193], v249 offset:2400
	s_waitcnt lgkmcnt(6)
	v_mfma_f32_16x16x32_bf16 v[142:145], v[44:47], v[134:137], 0
	s_waitcnt lgkmcnt(2)
	v_mfma_f32_16x16x32_bf16 v[138:141], v[44:47], v[138:141], 0
	s_waitcnt lgkmcnt(1)
	v_mfma_f32_16x16x32_bf16 v[134:137], v[44:47], v[186:189], 0
	s_waitcnt lgkmcnt(0)
	v_mfma_f32_16x16x32_bf16 v[44:47], v[44:47], v[190:193], 0
	s_waitcnt vmcnt(15)
	ds_write_b128 v252, v[86:89] offset:4608
	s_waitcnt vmcnt(14)
	ds_write_b128 v252, v[94:97] offset:5760
	s_waitcnt vmcnt(13)
	ds_write_b128 v252, v[118:121] offset:6912
	s_waitcnt vmcnt(12)
	ds_write_b128 v252, v[122:125] offset:8064
	ds_read_u16 v49, v151 offset:320
	ds_read_u16 v86, v151 offset:336
	ds_read_u16 v118, v151 offset:352
	ds_read_u16 v119, v151 offset:368
	s_waitcnt lgkmcnt(3)
	v_lshl_or_b32 v49, v49, 8, v250
	s_waitcnt lgkmcnt(2)
	v_lshl_or_b32 v94, v86, 8, v250
	global_load_dwordx4 v[86:89], v49, s[50:51] offset:128
	s_nop 0
	global_load_dwordx4 v[94:97], v94, s[50:51] offset:128
	s_waitcnt lgkmcnt(1)
	v_lshl_or_b32 v49, v118, 8, v250
	s_waitcnt lgkmcnt(0)
	v_lshl_or_b32 v122, v119, 8, v250
	global_load_dwordx4 v[118:121], v49, s[50:51] offset:128
	s_nop 0
	global_load_dwordx4 v[122:125], v122, s[50:51] offset:128
	v_pk_mul_f32 v[186:187], v[162:163], v[226:227] op_sel_hi:[0,1]
	v_pk_mul_f32 v[188:189], v[162:163], v[228:229] op_sel_hi:[0,1]
	v_cvt_pk_bf16_f32 v186, v186, v187
	v_cvt_pk_bf16_f32 v187, v188, v189
	v_pk_mul_f32 v[188:189], v[162:163], v[230:231] op_sel_hi:[0,1]
	v_pk_mul_f32 v[190:191], v[162:163], v[232:233] op_sel_hi:[0,1]
	v_cvt_pk_bf16_f32 v188, v188, v189
	v_cvt_pk_bf16_f32 v189, v190, v191
	s_waitcnt lgkmcnt(0)
	ds_read_b64_tr_b16 v[192:193], v249 offset:6912
	ds_read_b64_tr_b16 v[190:191], v249 offset:4608
	ds_read_b64_tr_b16 v[198:199], v249 offset:4640
	s_waitcnt lgkmcnt(1)
	v_mfma_f32_16x16x32_bf16 v[142:145], v[186:189], v[190:193], v[142:145]
	ds_read_b64_tr_b16 v[200:201], v249 offset:6944
	ds_read_b64_tr_b16 v[190:191], v249 offset:4672
	ds_read_b64_tr_b16 v[192:193], v249 offset:6976
	s_waitcnt lgkmcnt(0)
	v_mfma_f32_16x16x32_bf16 v[134:137], v[186:189], v[190:193], v[134:137]
	ds_read_b64_tr_b16 v[190:191], v249 offset:4704
	ds_read_b64_tr_b16 v[192:193], v249 offset:7008
	v_mfma_f32_16x16x32_bf16 v[138:141], v[186:189], v[198:201], v[138:141]
	s_waitcnt lgkmcnt(0)
	v_mfma_f32_16x16x32_bf16 v[44:47], v[186:189], v[190:193], v[44:47]
	s_waitcnt vmcnt(15)
	ds_write_b128 v252, v[78:81]
	s_waitcnt vmcnt(14)
	ds_write_b128 v252, v[82:85] offset:1152
	s_waitcnt vmcnt(13)
	ds_write_b128 v252, v[106:109] offset:2304
	s_waitcnt vmcnt(12)
	ds_write_b128 v252, v[114:117] offset:3456
	ds_read_u16 v49, v151 offset:384
	ds_read_u16 v78, v151 offset:400
	ds_read_u16 v106, v151 offset:416
	ds_read_u16 v107, v151 offset:432
	s_waitcnt lgkmcnt(3)
	v_lshl_or_b32 v49, v49, 8, v250
	s_waitcnt lgkmcnt(2)
	v_lshl_or_b32 v82, v78, 8, v250
	global_load_dwordx4 v[78:81], v49, s[50:51] offset:128
	s_nop 0
	global_load_dwordx4 v[82:85], v82, s[50:51] offset:128
	s_waitcnt lgkmcnt(1)
	v_lshl_or_b32 v49, v106, 8, v250
	s_waitcnt lgkmcnt(0)
	v_lshl_or_b32 v114, v107, 8, v250
	global_load_dwordx4 v[106:109], v49, s[50:51] offset:128
	s_nop 0
	global_load_dwordx4 v[114:117], v114, s[50:51] offset:128
	v_pk_mul_f32 v[186:187], v[162:163], v[218:219] op_sel_hi:[0,1]
	v_pk_mul_f32 v[188:189], v[162:163], v[220:221] op_sel_hi:[0,1]
	v_cvt_pk_bf16_f32 v186, v186, v187
	v_cvt_pk_bf16_f32 v187, v188, v189
	v_pk_mul_f32 v[188:189], v[162:163], v[222:223] op_sel_hi:[0,1]
	v_pk_mul_f32 v[190:191], v[162:163], v[224:225] op_sel_hi:[0,1]
	v_cvt_pk_bf16_f32 v188, v188, v189
	v_cvt_pk_bf16_f32 v189, v190, v191
	s_waitcnt lgkmcnt(0)
	ds_read_b64_tr_b16 v[192:193], v249 offset:2304
	ds_read_b64_tr_b16 v[190:191], v249
	ds_read_b64_tr_b16 v[198:199], v249 offset:32
	s_waitcnt lgkmcnt(1)
	v_mfma_f32_16x16x32_bf16 v[142:145], v[186:189], v[190:193], v[142:145]
	ds_read_b64_tr_b16 v[200:201], v249 offset:2336
	ds_read_b64_tr_b16 v[190:191], v249 offset:64
	ds_read_b64_tr_b16 v[192:193], v249 offset:2368
	s_waitcnt lgkmcnt(0)
	v_mfma_f32_16x16x32_bf16 v[134:137], v[186:189], v[190:193], v[134:137]
	ds_read_b64_tr_b16 v[190:191], v249 offset:96
	ds_read_b64_tr_b16 v[192:193], v249 offset:2400
	v_mfma_f32_16x16x32_bf16 v[138:141], v[186:189], v[198:201], v[138:141]
	s_waitcnt lgkmcnt(0)
	v_mfma_f32_16x16x32_bf16 v[44:47], v[186:189], v[190:193], v[44:47]
	s_waitcnt vmcnt(15)
	ds_write_b128 v252, v[70:73] offset:4608
	s_waitcnt vmcnt(14)
	ds_write_b128 v252, v[74:77] offset:5760
	s_waitcnt vmcnt(13)
	ds_write_b128 v252, v[90:93] offset:6912
	s_waitcnt vmcnt(12)
	ds_write_b128 v252, v[98:101] offset:8064
	ds_read_u16 v49, v151 offset:448
	ds_read_u16 v70, v151 offset:464
	ds_read_u16 v90, v151 offset:480
	ds_read_u16 v91, v151 offset:496
	s_waitcnt lgkmcnt(3)
	v_lshl_or_b32 v49, v49, 8, v250
	s_waitcnt lgkmcnt(2)
	v_lshl_or_b32 v74, v70, 8, v250
	global_load_dwordx4 v[70:73], v49, s[50:51] offset:128
	s_nop 0
	global_load_dwordx4 v[74:77], v74, s[50:51] offset:128
	s_waitcnt lgkmcnt(1)
	v_lshl_or_b32 v49, v90, 8, v250
	s_waitcnt lgkmcnt(0)
	v_lshl_or_b32 v98, v91, 8, v250
	global_load_dwordx4 v[90:93], v49, s[50:51] offset:128
	s_nop 0
	global_load_dwordx4 v[98:101], v98, s[50:51] offset:128
	v_pk_mul_f32 v[186:187], v[162:163], v[206:207] op_sel_hi:[0,1]
	v_pk_mul_f32 v[188:189], v[162:163], v[208:209] op_sel_hi:[0,1]
	v_cvt_pk_bf16_f32 v186, v186, v187
	v_cvt_pk_bf16_f32 v187, v188, v189
	v_pk_mul_f32 v[188:189], v[162:163], v[214:215] op_sel_hi:[0,1]
	v_pk_mul_f32 v[190:191], v[162:163], v[216:217] op_sel_hi:[0,1]
	v_cvt_pk_bf16_f32 v188, v188, v189
	v_cvt_pk_bf16_f32 v189, v190, v191
	s_waitcnt lgkmcnt(0)
	ds_read_b64_tr_b16 v[192:193], v249 offset:6912
	ds_read_b64_tr_b16 v[190:191], v249 offset:4608
	ds_read_b64_tr_b16 v[198:199], v249 offset:4640
	s_waitcnt lgkmcnt(1)
	v_mfma_f32_16x16x32_bf16 v[142:145], v[186:189], v[190:193], v[142:145]
	ds_read_b64_tr_b16 v[200:201], v249 offset:6944
	ds_read_b64_tr_b16 v[190:191], v249 offset:4672
	ds_read_b64_tr_b16 v[192:193], v249 offset:6976
	s_waitcnt lgkmcnt(0)
	v_mfma_f32_16x16x32_bf16 v[134:137], v[186:189], v[190:193], v[134:137]
	ds_read_b64_tr_b16 v[190:191], v249 offset:4704
	ds_read_b64_tr_b16 v[192:193], v249 offset:7008
	v_mfma_f32_16x16x32_bf16 v[138:141], v[186:189], v[198:201], v[138:141]
	s_waitcnt lgkmcnt(0)
	v_mfma_f32_16x16x32_bf16 v[44:47], v[186:189], v[190:193], v[44:47]
	v_pk_mul_f32 v[182:183], v[162:163], v[182:183] op_sel_hi:[0,1]
	v_pk_mul_f32 v[180:181], v[162:163], v[180:181] op_sel_hi:[0,1]
	v_cvt_pk_bf16_f32 v182, v182, v183
	v_cvt_pk_bf16_f32 v183, v180, v181
	v_pk_mul_f32 v[180:181], v[162:163], v[184:185] op_sel_hi:[0,1]
	s_waitcnt vmcnt(15)
	ds_write_b128 v252, v[102:105]
	s_waitcnt vmcnt(14)
	ds_write_b128 v252, v[110:113] offset:1152
	s_waitcnt vmcnt(13)
	ds_write_b128 v252, v[126:129] offset:2304
	s_waitcnt vmcnt(12)
	ds_write_b128 v252, v[130:133] offset:3456
	v_cvt_pk_bf16_f32 v184, v180, v181
	v_pk_mul_f32 v[180:181], v[162:163], v[196:197] op_sel_hi:[0,1]
	v_cvt_pk_bf16_f32 v185, v180, v181
	s_waitcnt lgkmcnt(0)
	ds_read_b64_tr_b16 v[188:189], v249 offset:2304
	ds_read_b64_tr_b16 v[186:187], v249
	ds_read_b64_tr_b16 v[190:191], v249 offset:32
	s_waitcnt lgkmcnt(1)
	v_mfma_f32_16x16x32_bf16 v[142:145], v[182:185], v[186:189], v[142:145]
	ds_read_b64_tr_b16 v[192:193], v249 offset:2336
	ds_read_b64_tr_b16 v[186:187], v249 offset:64
	ds_read_b64_tr_b16 v[188:189], v249 offset:2368
	s_waitcnt lgkmcnt(0)
	v_mfma_f32_16x16x32_bf16 v[134:137], v[182:185], v[186:189], v[134:137]
	ds_read_b64_tr_b16 v[186:187], v249 offset:96
	ds_read_b64_tr_b16 v[188:189], v249 offset:2400
	v_mfma_f32_16x16x32_bf16 v[138:141], v[182:185], v[190:193], v[138:141]
	s_waitcnt lgkmcnt(0)
	v_mfma_f32_16x16x32_bf16 v[44:47], v[182:185], v[186:189], v[44:47]
	v_pk_mul_f32 v[172:173], v[162:163], v[172:173] op_sel_hi:[0,1]
	v_pk_mul_f32 v[174:175], v[162:163], v[174:175] op_sel_hi:[0,1]
	s_waitcnt vmcnt(11)
	ds_write_b128 v252, v[86:89] offset:4608
	s_waitcnt vmcnt(10)
	ds_write_b128 v252, v[94:97] offset:5760
	s_waitcnt vmcnt(9)
	ds_write_b128 v252, v[118:121] offset:6912
	s_waitcnt vmcnt(8)
	ds_write_b128 v252, v[122:125] offset:8064
	v_cvt_pk_bf16_f32 v172, v172, v173
	v_cvt_pk_bf16_f32 v173, v174, v175
	v_pk_mul_f32 v[174:175], v[162:163], v[176:177] op_sel_hi:[0,1]
	v_pk_mul_f32 v[176:177], v[162:163], v[178:179] op_sel_hi:[0,1]
	v_cvt_pk_bf16_f32 v174, v174, v175
	v_cvt_pk_bf16_f32 v175, v176, v177
	s_waitcnt lgkmcnt(0)
	ds_read_b64_tr_b16 v[178:179], v249 offset:6912
	ds_read_b64_tr_b16 v[176:177], v249 offset:4608
	ds_read_b64_tr_b16 v[180:181], v249 offset:4640
	s_waitcnt lgkmcnt(1)
	v_mfma_f32_16x16x32_bf16 v[142:145], v[172:175], v[176:179], v[142:145]
	ds_read_b64_tr_b16 v[182:183], v249 offset:6944
	ds_read_b64_tr_b16 v[176:177], v249 offset:4672
	ds_read_b64_tr_b16 v[178:179], v249 offset:6976
	s_waitcnt lgkmcnt(0)
	v_mfma_f32_16x16x32_bf16 v[134:137], v[172:175], v[176:179], v[134:137]
	ds_read_b64_tr_b16 v[176:177], v249 offset:4704
	ds_read_b64_tr_b16 v[178:179], v249 offset:7008
	v_mfma_f32_16x16x32_bf16 v[138:141], v[172:175], v[180:183], v[138:141]
	s_waitcnt lgkmcnt(0)
	v_mfma_f32_16x16x32_bf16 v[44:47], v[172:175], v[176:179], v[44:47]
	v_pk_mul_f32 v[164:165], v[162:163], v[164:165] op_sel_hi:[0,1]
	v_pk_mul_f32 v[166:167], v[162:163], v[166:167] op_sel_hi:[0,1]
	s_waitcnt vmcnt(7)
	ds_write_b128 v252, v[78:81]
	s_waitcnt vmcnt(6)
	ds_write_b128 v252, v[82:85] offset:1152
	s_waitcnt vmcnt(5)
	ds_write_b128 v252, v[106:109] offset:2304
	s_waitcnt vmcnt(4)
	ds_write_b128 v252, v[114:117] offset:3456
	v_cvt_pk_bf16_f32 v164, v164, v165
	v_cvt_pk_bf16_f32 v165, v166, v167
	v_pk_mul_f32 v[166:167], v[162:163], v[168:169] op_sel_hi:[0,1]
	v_pk_mul_f32 v[168:169], v[162:163], v[170:171] op_sel_hi:[0,1]
	v_cvt_pk_bf16_f32 v166, v166, v167
	v_cvt_pk_bf16_f32 v167, v168, v169
	s_waitcnt lgkmcnt(0)
	ds_read_b64_tr_b16 v[170:171], v249 offset:2304
	ds_read_b64_tr_b16 v[168:169], v249
	ds_read_b64_tr_b16 v[172:173], v249 offset:32
	s_waitcnt lgkmcnt(1)
	v_mfma_f32_16x16x32_bf16 v[142:145], v[164:167], v[168:171], v[142:145]
	ds_read_b64_tr_b16 v[174:175], v249 offset:2336
	ds_read_b64_tr_b16 v[168:169], v249 offset:64
	ds_read_b64_tr_b16 v[170:171], v249 offset:2368
	s_waitcnt lgkmcnt(0)
	v_mfma_f32_16x16x32_bf16 v[134:137], v[164:167], v[168:171], v[134:137]
	ds_read_b64_tr_b16 v[168:169], v249 offset:96
	ds_read_b64_tr_b16 v[170:171], v249 offset:2400
	v_mfma_f32_16x16x32_bf16 v[138:141], v[164:167], v[172:175], v[138:141]
	s_waitcnt lgkmcnt(0)
	v_mfma_f32_16x16x32_bf16 v[44:47], v[164:167], v[168:171], v[44:47]
	v_pk_mul_f32 v[154:155], v[162:163], v[154:155] op_sel_hi:[0,1]
	v_pk_mul_f32 v[156:157], v[162:163], v[156:157] op_sel_hi:[0,1]
	s_waitcnt vmcnt(3)
	ds_write_b128 v252, v[70:73] offset:4608
	s_waitcnt vmcnt(2)
	ds_write_b128 v252, v[74:77] offset:5760
	s_waitcnt vmcnt(1)
	ds_write_b128 v252, v[90:93] offset:6912
	s_waitcnt vmcnt(0)
	ds_write_b128 v252, v[98:101] offset:8064
	v_cvt_pk_bf16_f32 v154, v154, v155
	v_cvt_pk_bf16_f32 v155, v156, v157
	v_pk_mul_f32 v[156:157], v[162:163], v[158:159] op_sel_hi:[0,1]
	v_pk_mul_f32 v[158:159], v[162:163], v[160:161] op_sel_hi:[0,1]
	v_cvt_pk_bf16_f32 v156, v156, v157
	v_cvt_pk_bf16_f32 v157, v158, v159
	s_waitcnt lgkmcnt(0)
	ds_read_b64_tr_b16 v[160:161], v249 offset:6912
	ds_read_b64_tr_b16 v[158:159], v249 offset:4608
	ds_read_b64_tr_b16 v[162:163], v249 offset:4640
	s_waitcnt lgkmcnt(1)
	v_mfma_f32_16x16x32_bf16 v[142:145], v[154:157], v[158:161], v[142:145]
	ds_read_b64_tr_b16 v[164:165], v249 offset:6944
	ds_read_b64_tr_b16 v[158:159], v249 offset:4672
	ds_read_b64_tr_b16 v[160:161], v249 offset:6976
	s_waitcnt lgkmcnt(0)
	v_mfma_f32_16x16x32_bf16 v[134:137], v[154:157], v[158:161], v[134:137]
	ds_read_b64_tr_b16 v[158:159], v249 offset:4704
	ds_read_b64_tr_b16 v[160:161], v249 offset:7008
	v_mfma_f32_16x16x32_bf16 v[138:141], v[154:157], v[162:165], v[138:141]
	s_waitcnt lgkmcnt(0)
	v_mfma_f32_16x16x32_bf16 v[44:47], v[154:157], v[158:161], v[44:47]
	s_waitcnt lgkmcnt(0)
	s_and_saveexec_b64 s[8:9], s[40:41]
	s_cbranch_execz .LBB0_784
	s_lshl_b64 s[18:19], s[52:53], 10
	v_bfe_u32 v49, v142, 16, 1
	v_add3_u32 v49, v142, v49, s75
	v_lshl_add_u64 v[154:155], v[148:149], 0, s[18:19]
	global_store_short_d16_hi v[154:155], v49, off
	v_bfe_u32 v49, v143, 16, 1
	v_add3_u32 v49, v143, v49, s75
	global_store_short_d16_hi v[154:155], v49, off offset:128
	v_bfe_u32 v49, v144, 16, 1
	v_add3_u32 v49, v144, v49, s75
	global_store_short_d16_hi v[154:155], v49, off offset:256
	v_bfe_u32 v49, v145, 16, 1
	v_add3_u32 v49, v145, v49, s75
	global_store_short_d16_hi v[154:155], v49, off offset:384
	v_bfe_u32 v49, v138, 16, 1
	v_add3_u32 v49, v138, v49, s75
	global_store_short_d16_hi v[154:155], v49, off offset:32
	v_bfe_u32 v49, v139, 16, 1
	v_add3_u32 v49, v139, v49, s75
	global_store_short_d16_hi v[154:155], v49, off offset:160
	v_bfe_u32 v49, v140, 16, 1
	v_add3_u32 v49, v140, v49, s75
	global_store_short_d16_hi v[154:155], v49, off offset:288
	v_bfe_u32 v49, v141, 16, 1
	v_add3_u32 v49, v141, v49, s75
	global_store_short_d16_hi v[154:155], v49, off offset:416
	v_bfe_u32 v49, v134, 16, 1
	v_add3_u32 v49, v134, v49, s75
	global_store_short_d16_hi v[154:155], v49, off offset:64
	v_bfe_u32 v49, v135, 16, 1
	v_add3_u32 v49, v135, v49, s75
	global_store_short_d16_hi v[154:155], v49, off offset:192
	v_bfe_u32 v49, v136, 16, 1
	v_add3_u32 v49, v136, v49, s75
	global_store_short_d16_hi v[154:155], v49, off offset:320
	v_bfe_u32 v49, v137, 16, 1
	v_add3_u32 v49, v137, v49, s75
	global_store_short_d16_hi v[154:155], v49, off offset:448
	v_bfe_u32 v49, v44, 16, 1
	v_add3_u32 v44, v44, v49, s75
	global_store_short_d16_hi v[154:155], v44, off offset:96
	v_bfe_u32 v44, v45, 16, 1
	v_add3_u32 v44, v45, v44, s75
	global_store_short_d16_hi v[154:155], v44, off offset:224
	v_bfe_u32 v44, v46, 16, 1
	v_add3_u32 v44, v46, v44, s75
	global_store_short_d16_hi v[154:155], v44, off offset:352
	v_bfe_u32 v44, v47, 16, 1
	v_add3_u32 v44, v47, v44, s75
	global_store_short_d16_hi v[154:155], v44, off offset:480
	s_branch .LBB0_784

.Lmy_z_1:
	s_add_u32 s6, s6, 0x80
	s_addc_u32 s7, s7, 0
	s_add_u32 s25, s8, 0x100
	s_addc_u32 s28, s9, 0
	s_mov_b32 s8, 0
	s_add_i32 s29, s8, 2
	s_add_u32 s30, s6, 0x80
	s_addc_u32 s9, s7, 0
	s_add_i32 s42, 0, 0x10000
	s_cmp_eq_u32 s66, s8
	s_cselect_b32 s9, s59, s9
	s_cselect_b32 s8, s58, s30
	s_cselect_b32 s41, s61, s28
	s_cselect_b32 s40, s60, s25
	s_add_i32 s30, 0, 0x14000
	v_add_u32_e32 v94, s42, v216
	v_add_u32_e32 v134, s30, v216
	ds_read_b128 v[66:69], v94
	ds_read_b128 v[70:73], v94 offset:1024
	ds_read_b128 v[82:85], v94 offset:2048
	ds_read_b128 v[94:97], v94 offset:3072
	ds_read_b128 v[106:109], v134
	ds_read_b128 v[118:121], v134 offset:1024
	ds_read_b128 v[122:125], v134 offset:2048
	ds_read_b128 v[134:137], v134 offset:3072
	v_lshl_add_u64 v[210:211], s[6:7], 0, v[206:207]
	s_add_i32 m0, s21, 0xc000
	ds_read_b128 v[162:165], v218
	ds_read_b128 v[166:169], v218 offset:1024
	ds_read_b128 v[170:173], v218 offset:2048
	ds_read_b128 v[174:177], v218 offset:3072
	ds_read_b128 v[178:181], v218 offset:4096
	ds_read_b128 v[182:185], v218 offset:5120
	ds_read_b128 v[186:189], v218 offset:6144
	ds_read_b128 v[190:193], v218 offset:7168
	global_load_lds_dwordx4 v[210:211], off
	v_lshl_add_u64 v[210:211], s[6:7], 0, v[208:209]
	s_add_i32 m0, s21, 0xe000
	s_nop 0
	global_load_lds_dwordx4 v[210:211], off
	s_waitcnt vmcnt(8)
	s_waitcnt lgkmcnt(0)
	s_barrier
	s_setprio 1
	s_waitcnt lgkmcnt(0)
	v_mfma_f32_16x16x32_bf16 v[158:161], v[66:69], v[162:165], 0
	v_mfma_f32_16x16x32_bf16 v[154:157], v[82:85], v[162:165], 0
	v_mfma_f32_16x16x32_bf16 v[142:145], v[66:69], v[170:173], 0
	v_mfma_f32_16x16x32_bf16 v[138:141], v[82:85], v[170:173], 0
	v_mfma_f32_16x16x32_bf16 v[114:117], v[66:69], v[178:181], 0
	v_mfma_f32_16x16x32_bf16 v[110:113], v[82:85], v[178:181], 0
	v_mfma_f32_16x16x32_bf16 v[90:93], v[66:69], v[186:189], 0
	v_mfma_f32_16x16x32_bf16 v[86:89], v[82:85], v[186:189], 0
	v_mfma_f32_16x16x32_bf16 v[158:161], v[70:73], v[166:169], v[158:161]
	v_mfma_f32_16x16x32_bf16 v[154:157], v[94:97], v[166:169], v[154:157]
	v_mfma_f32_16x16x32_bf16 v[142:145], v[70:73], v[174:177], v[142:145]
	v_mfma_f32_16x16x32_bf16 v[138:141], v[94:97], v[174:177], v[138:141]
	v_mfma_f32_16x16x32_bf16 v[114:117], v[70:73], v[182:185], v[114:117]
	v_mfma_f32_16x16x32_bf16 v[110:113], v[94:97], v[182:185], v[110:113]
	v_mfma_f32_16x16x32_bf16 v[90:93], v[70:73], v[190:193], v[90:93]
	v_mfma_f32_16x16x32_bf16 v[86:89], v[94:97], v[190:193], v[86:89]
	s_setprio 0
	s_setprio 1
	v_mfma_f32_16x16x32_bf16 v[150:153], v[106:109], v[162:165], 0
	v_mfma_f32_16x16x32_bf16 v[146:149], v[122:125], v[162:165], 0
	v_mfma_f32_16x16x32_bf16 v[130:133], v[106:109], v[170:173], 0
	v_mfma_f32_16x16x32_bf16 v[126:129], v[122:125], v[170:173], 0
	v_mfma_f32_16x16x32_bf16 v[102:105], v[106:109], v[178:181], 0
	v_mfma_f32_16x16x32_bf16 v[98:101], v[122:125], v[178:181], 0
	v_mfma_f32_16x16x32_bf16 v[78:81], v[106:109], v[186:189], 0
	v_mfma_f32_16x16x32_bf16 v[74:77], v[122:125], v[186:189], 0
	v_mfma_f32_16x16x32_bf16 v[150:153], v[118:121], v[166:169], v[150:153]
	v_mfma_f32_16x16x32_bf16 v[146:149], v[134:137], v[166:169], v[146:149]
	v_mfma_f32_16x16x32_bf16 v[130:133], v[118:121], v[174:177], v[130:133]
	v_mfma_f32_16x16x32_bf16 v[126:129], v[134:137], v[174:177], v[126:129]
	v_mfma_f32_16x16x32_bf16 v[102:105], v[118:121], v[182:185], v[102:105]
	v_mfma_f32_16x16x32_bf16 v[98:101], v[134:137], v[182:185], v[98:101]
	v_mfma_f32_16x16x32_bf16 v[78:81], v[118:121], v[190:193], v[78:81]
	v_mfma_f32_16x16x32_bf16 v[74:77], v[134:137], v[190:193], v[74:77]
	s_setprio 0
	s_barrier
	s_add_i32 s42, s42, s20
	v_lshl_add_u64 v[210:211], s[40:41], 0, v[196:197]
	s_mov_b32 m0, s42
	ds_read_b128 v[162:165], v218 offset:16384
	ds_read_b128 v[166:169], v218 offset:17408
	ds_read_b128 v[170:173], v218 offset:18432
	ds_read_b128 v[174:177], v218 offset:19456
	ds_read_b128 v[178:181], v218 offset:20480
	ds_read_b128 v[182:185], v218 offset:21504
	ds_read_b128 v[186:189], v218 offset:22528
	ds_read_b128 v[190:193], v218 offset:23552
	global_load_lds_dwordx4 v[210:211], off
	s_add_i32 m0, s42, 0x2000
	v_lshl_add_u64 v[212:213], s[40:41], 0, v[200:201]
	s_add_u32 s40, s40, s46
	s_addc_u32 s41, s41, s47
	s_add_i32 s30, s30, s20
	global_load_lds_dwordx4 v[212:213], off
	v_lshl_add_u64 v[214:215], s[40:41], 0, v[196:197]
	s_mov_b32 m0, s30
	v_lshl_add_u64 v[220:221], s[40:41], 0, v[200:201]
	global_load_lds_dwordx4 v[214:215], off
	s_add_i32 m0, s30, 0x2000
	v_lshl_add_u64 v[222:223], s[8:9], 0, v[194:195]
	global_load_lds_dwordx4 v[220:221], off
	s_mov_b32 m0, s21
	v_lshl_add_u64 v[224:225], s[8:9], 0, v[198:199]
	global_load_lds_dwordx4 v[222:223], off
	s_mov_b32 m0, s24
	s_nop 0
	global_load_lds_dwordx4 v[224:225], off
	s_waitcnt vmcnt(8)
	s_waitcnt lgkmcnt(0)
	s_barrier
	s_setprio 1
	s_waitcnt lgkmcnt(0)
	v_mfma_f32_16x16x32_bf16 v[62:65], v[66:69], v[162:165], 0
	v_mfma_f32_16x16x32_bf16 v[58:61], v[82:85], v[162:165], 0
	v_mfma_f32_16x16x32_bf16 v[44:47], v[66:69], v[170:173], 0
	v_mfma_f32_16x16x32_bf16 v[40:43], v[82:85], v[170:173], 0
	v_mfma_f32_16x16x32_bf16 v[28:31], v[66:69], v[178:181], 0
	v_mfma_f32_16x16x32_bf16 v[24:27], v[82:85], v[178:181], 0
	v_mfma_f32_16x16x32_bf16 v[12:15], v[66:69], v[186:189], 0
	v_mfma_f32_16x16x32_bf16 v[8:11], v[82:85], v[186:189], 0
	v_mfma_f32_16x16x32_bf16 v[62:65], v[70:73], v[166:169], v[62:65]
	v_mfma_f32_16x16x32_bf16 v[58:61], v[94:97], v[166:169], v[58:61]
	v_mfma_f32_16x16x32_bf16 v[44:47], v[70:73], v[174:177], v[44:47]
	v_mfma_f32_16x16x32_bf16 v[40:43], v[94:97], v[174:177], v[40:43]
	v_mfma_f32_16x16x32_bf16 v[28:31], v[70:73], v[182:185], v[28:31]
	v_mfma_f32_16x16x32_bf16 v[24:27], v[94:97], v[182:185], v[24:27]
	v_mfma_f32_16x16x32_bf16 v[12:15], v[70:73], v[190:193], v[12:15]
	v_mfma_f32_16x16x32_bf16 v[8:11], v[94:97], v[190:193], v[8:11]
	s_setprio 0
	s_setprio 1
	v_mfma_f32_16x16x32_bf16 v[54:57], v[106:109], v[162:165], 0
	v_mfma_f32_16x16x32_bf16 v[50:53], v[122:125], v[162:165], 0
	v_mfma_f32_16x16x32_bf16 v[36:39], v[106:109], v[170:173], 0
	v_mfma_f32_16x16x32_bf16 v[32:35], v[122:125], v[170:173], 0
	v_mfma_f32_16x16x32_bf16 v[20:23], v[106:109], v[178:181], 0
	v_mfma_f32_16x16x32_bf16 v[16:19], v[122:125], v[178:181], 0
	v_mfma_f32_16x16x32_bf16 v[4:7], v[106:109], v[186:189], 0
	v_mfma_f32_16x16x32_bf16 v[0:3], v[122:125], v[186:189], 0
	v_mfma_f32_16x16x32_bf16 v[54:57], v[118:121], v[166:169], v[54:57]
	v_mfma_f32_16x16x32_bf16 v[50:53], v[134:137], v[166:169], v[50:53]
	v_mfma_f32_16x16x32_bf16 v[36:39], v[118:121], v[174:177], v[36:39]
	v_mfma_f32_16x16x32_bf16 v[32:35], v[134:137], v[174:177], v[32:35]
	v_mfma_f32_16x16x32_bf16 v[20:23], v[118:121], v[182:185], v[20:23]
	v_mfma_f32_16x16x32_bf16 v[16:19], v[134:137], v[182:185], v[16:19]
	v_mfma_f32_16x16x32_bf16 v[4:7], v[118:121], v[190:193], v[4:7]
	v_mfma_f32_16x16x32_bf16 v[0:3], v[134:137], v[190:193], v[0:3]
	s_setprio 0
	s_barrier
	s_add_i32 s30, 0, 0x18000
	s_add_i32 s40, 0, 0x1c000
	v_add_u32_e32 v94, s30, v216
	v_add_u32_e32 v134, s40, v216
	ds_read_b128 v[66:69], v94
	ds_read_b128 v[70:73], v94 offset:1024
	ds_read_b128 v[82:85], v94 offset:2048
	ds_read_b128 v[94:97], v94 offset:3072
	ds_read_b128 v[106:109], v134
	ds_read_b128 v[118:121], v134 offset:1024
	ds_read_b128 v[122:125], v134 offset:2048
	ds_read_b128 v[134:137], v134 offset:3072
	s_add_u32 s8, s8, s46
	s_addc_u32 s9, s9, s47
	s_mov_b32 m0, s26
	v_lshl_add_u64 v[226:227], s[8:9], 0, v[194:195]
	ds_read_b128 v[162:165], v218 offset:32768
	ds_read_b128 v[166:169], v218 offset:33792
	ds_read_b128 v[170:173], v218 offset:34816
	ds_read_b128 v[174:177], v218 offset:35840
	ds_read_b128 v[178:181], v218 offset:36864
	ds_read_b128 v[182:185], v218 offset:37888
	ds_read_b128 v[186:189], v218 offset:38912
	ds_read_b128 v[190:193], v218 offset:39936
	global_load_lds_dwordx4 v[226:227], off
	v_lshl_add_u64 v[226:227], s[8:9], 0, v[198:199]
	s_mov_b32 m0, s62
	s_nop 0
	global_load_lds_dwordx4 v[226:227], off
	s_waitcnt vmcnt(8)
	s_waitcnt lgkmcnt(0)
	s_barrier
	s_setprio 1
	s_waitcnt lgkmcnt(0)
	v_mfma_f32_16x16x32_bf16 v[158:161], v[66:69], v[162:165], v[158:161]
	v_mfma_f32_16x16x32_bf16 v[154:157], v[82:85], v[162:165], v[154:157]
	v_mfma_f32_16x16x32_bf16 v[142:145], v[66:69], v[170:173], v[142:145]
	v_mfma_f32_16x16x32_bf16 v[138:141], v[82:85], v[170:173], v[138:141]
	v_mfma_f32_16x16x32_bf16 v[114:117], v[66:69], v[178:181], v[114:117]
	v_mfma_f32_16x16x32_bf16 v[110:113], v[82:85], v[178:181], v[110:113]
	v_mfma_f32_16x16x32_bf16 v[90:93], v[66:69], v[186:189], v[90:93]
	v_mfma_f32_16x16x32_bf16 v[86:89], v[82:85], v[186:189], v[86:89]
	v_mfma_f32_16x16x32_bf16 v[158:161], v[70:73], v[166:169], v[158:161]
	v_mfma_f32_16x16x32_bf16 v[154:157], v[94:97], v[166:169], v[154:157]
	v_mfma_f32_16x16x32_bf16 v[142:145], v[70:73], v[174:177], v[142:145]
	v_mfma_f32_16x16x32_bf16 v[138:141], v[94:97], v[174:177], v[138:141]
	v_mfma_f32_16x16x32_bf16 v[114:117], v[70:73], v[182:185], v[114:117]
	v_mfma_f32_16x16x32_bf16 v[110:113], v[94:97], v[182:185], v[110:113]
	v_mfma_f32_16x16x32_bf16 v[90:93], v[70:73], v[190:193], v[90:93]
	v_mfma_f32_16x16x32_bf16 v[86:89], v[94:97], v[190:193], v[86:89]
	s_setprio 0
	s_setprio 1
	v_mfma_f32_16x16x32_bf16 v[150:153], v[106:109], v[162:165], v[150:153]
	v_mfma_f32_16x16x32_bf16 v[146:149], v[122:125], v[162:165], v[146:149]
	v_mfma_f32_16x16x32_bf16 v[130:133], v[106:109], v[170:173], v[130:133]
	v_mfma_f32_16x16x32_bf16 v[126:129], v[122:125], v[170:173], v[126:129]
	v_mfma_f32_16x16x32_bf16 v[102:105], v[106:109], v[178:181], v[102:105]
	v_mfma_f32_16x16x32_bf16 v[98:101], v[122:125], v[178:181], v[98:101]
	v_mfma_f32_16x16x32_bf16 v[78:81], v[106:109], v[186:189], v[78:81]
	v_mfma_f32_16x16x32_bf16 v[74:77], v[122:125], v[186:189], v[74:77]
	v_mfma_f32_16x16x32_bf16 v[150:153], v[118:121], v[166:169], v[150:153]
	v_mfma_f32_16x16x32_bf16 v[146:149], v[134:137], v[166:169], v[146:149]
	v_mfma_f32_16x16x32_bf16 v[130:133], v[118:121], v[174:177], v[130:133]
	v_mfma_f32_16x16x32_bf16 v[126:129], v[134:137], v[174:177], v[126:129]
	v_mfma_f32_16x16x32_bf16 v[102:105], v[118:121], v[182:185], v[102:105]
	v_mfma_f32_16x16x32_bf16 v[98:101], v[134:137], v[182:185], v[98:101]
	v_mfma_f32_16x16x32_bf16 v[78:81], v[118:121], v[190:193], v[78:81]
	v_mfma_f32_16x16x32_bf16 v[74:77], v[134:137], v[190:193], v[74:77]
	s_setprio 0
	s_barrier
	s_add_i32 s8, s30, s20
	v_lshl_add_u64 v[210:211], v[210:211], 0, s[34:35]
	s_mov_b32 m0, s8
	ds_read_b128 v[162:165], v218 offset:49152
	ds_read_b128 v[166:169], v218 offset:50176
	ds_read_b128 v[170:173], v218 offset:51200
	ds_read_b128 v[174:177], v218 offset:52224
	ds_read_b128 v[178:181], v218 offset:53248
	ds_read_b128 v[182:185], v218 offset:54272
	ds_read_b128 v[186:189], v218 offset:55296
	ds_read_b128 v[190:193], v218 offset:56320
	global_load_lds_dwordx4 v[210:211], off
	v_lshl_add_u64 v[210:211], v[212:213], 0, s[34:35]
	s_add_i32 m0, s8, 0x2000
	s_add_i32 s8, s40, s20
	global_load_lds_dwordx4 v[210:211], off
	v_lshl_add_u64 v[210:211], v[214:215], 0, s[34:35]
	s_mov_b32 m0, s8
	s_nop 0
	global_load_lds_dwordx4 v[210:211], off
	v_lshl_add_u64 v[210:211], v[220:221], 0, s[34:35]
	s_add_i32 m0, s8, 0x2000
	s_nop 0
	global_load_lds_dwordx4 v[210:211], off
	v_lshl_add_u64 v[210:211], v[222:223], 0, s[34:35]
	s_mov_b32 m0, s64
	s_nop 0
	global_load_lds_dwordx4 v[210:211], off
	v_lshl_add_u64 v[210:211], v[224:225], 0, s[34:35]
	s_mov_b32 m0, s65
	s_nop 0
	global_load_lds_dwordx4 v[210:211], off
	s_waitcnt vmcnt(8)
	s_waitcnt lgkmcnt(0)
	s_barrier
	s_setprio 1
	s_waitcnt lgkmcnt(0)
	v_mfma_f32_16x16x32_bf16 v[62:65], v[66:69], v[162:165], v[62:65]
	v_mfma_f32_16x16x32_bf16 v[58:61], v[82:85], v[162:165], v[58:61]
	v_mfma_f32_16x16x32_bf16 v[44:47], v[66:69], v[170:173], v[44:47]
	v_mfma_f32_16x16x32_bf16 v[40:43], v[82:85], v[170:173], v[40:43]
	v_mfma_f32_16x16x32_bf16 v[28:31], v[66:69], v[178:181], v[28:31]
	v_mfma_f32_16x16x32_bf16 v[24:27], v[82:85], v[178:181], v[24:27]
	v_mfma_f32_16x16x32_bf16 v[12:15], v[66:69], v[186:189], v[12:15]
	v_mfma_f32_16x16x32_bf16 v[8:11], v[82:85], v[186:189], v[8:11]
	v_mfma_f32_16x16x32_bf16 v[62:65], v[70:73], v[166:169], v[62:65]
	v_mfma_f32_16x16x32_bf16 v[58:61], v[94:97], v[166:169], v[58:61]
	v_mfma_f32_16x16x32_bf16 v[44:47], v[70:73], v[174:177], v[44:47]
	v_mfma_f32_16x16x32_bf16 v[40:43], v[94:97], v[174:177], v[40:43]
	v_mfma_f32_16x16x32_bf16 v[28:31], v[70:73], v[182:185], v[28:31]
	v_mfma_f32_16x16x32_bf16 v[24:27], v[94:97], v[182:185], v[24:27]
	v_mfma_f32_16x16x32_bf16 v[12:15], v[70:73], v[190:193], v[12:15]
	v_mfma_f32_16x16x32_bf16 v[8:11], v[94:97], v[190:193], v[8:11]
	s_setprio 0
	s_setprio 1
	v_mfma_f32_16x16x32_bf16 v[54:57], v[106:109], v[162:165], v[54:57]
	v_mfma_f32_16x16x32_bf16 v[50:53], v[122:125], v[162:165], v[50:53]
	v_mfma_f32_16x16x32_bf16 v[36:39], v[106:109], v[170:173], v[36:39]
	v_mfma_f32_16x16x32_bf16 v[32:35], v[122:125], v[170:173], v[32:35]
	v_mfma_f32_16x16x32_bf16 v[20:23], v[106:109], v[178:181], v[20:23]
	v_mfma_f32_16x16x32_bf16 v[16:19], v[122:125], v[178:181], v[16:19]
	v_mfma_f32_16x16x32_bf16 v[4:7], v[106:109], v[186:189], v[4:7]
	v_mfma_f32_16x16x32_bf16 v[0:3], v[122:125], v[186:189], v[0:3]
	v_mfma_f32_16x16x32_bf16 v[54:57], v[118:121], v[166:169], v[54:57]
	v_mfma_f32_16x16x32_bf16 v[50:53], v[134:137], v[166:169], v[50:53]
	v_mfma_f32_16x16x32_bf16 v[36:39], v[118:121], v[174:177], v[36:39]
	v_mfma_f32_16x16x32_bf16 v[32:35], v[134:137], v[174:177], v[32:35]
	v_mfma_f32_16x16x32_bf16 v[20:23], v[118:121], v[182:185], v[20:23]
	v_mfma_f32_16x16x32_bf16 v[16:19], v[134:137], v[182:185], v[16:19]
	v_mfma_f32_16x16x32_bf16 v[4:7], v[118:121], v[190:193], v[4:7]
	v_mfma_f32_16x16x32_bf16 v[0:3], v[134:137], v[190:193], v[0:3]
	s_setprio 0
	s_barrier
	s_add_u32 s6, s6, 0x100
	s_addc_u32 s7, s7, 0
	s_add_u32 s25, s25, 0x100
	s_addc_u32 s28, s28, 0
	s_cmp_ge_i32 s29, s63
	s_mov_b32 s8, s29

.Lmy_z_2:
	s_add_u32 s6, s6, 0x80
	s_addc_u32 s7, s7, 0
	s_add_u32 s29, s8, 0x100
	s_addc_u32 s57, s9, 0
	s_mov_b32 s8, 0
	s_add_i32 s72, s8, 2
	s_add_u32 s82, s6, 0x80
	s_addc_u32 s9, s7, 0
	s_add_i32 s84, 0, 0x10000
	s_cmp_eq_u32 s89, s8
	s_cselect_b32 s9, s45, s9
	s_cselect_b32 s8, s44, s82
	s_cselect_b32 s83, s67, s57
	s_cselect_b32 s82, s66, s29
	s_add_i32 s85, 0, 0x14000
	v_add_u32_e32 v142, s84, v179
	v_add_u32_e32 v170, s85, v179
	ds_read_b128 v[130:133], v142
	ds_read_b128 v[134:137], v142 offset:1024
	ds_read_b128 v[138:141], v142 offset:2048
	ds_read_b128 v[142:145], v142 offset:3072
	ds_read_b128 v[146:149], v170
	ds_read_b128 v[150:153], v170 offset:1024
	ds_read_b128 v[154:157], v170 offset:2048
	ds_read_b128 v[170:173], v170 offset:3072
	v_lshl_add_u64 v[218:219], s[6:7], 0, v[166:167]
	s_add_i32 m0, s69, 0xc000
	ds_read_b128 v[174:177], v186
	ds_read_b128 v[190:193], v186 offset:1024
	ds_read_b128 v[194:197], v186 offset:2048
	ds_read_b128 v[198:201], v186 offset:3072
	ds_read_b128 v[202:205], v186 offset:4096
	ds_read_b128 v[206:209], v186 offset:5120
	ds_read_b128 v[210:213], v186 offset:6144
	ds_read_b128 v[214:217], v186 offset:7168
	global_load_lds_dwordx4 v[218:219], off
	v_lshl_add_u64 v[218:219], s[6:7], 0, v[168:169]
	s_add_i32 m0, s69, 0xe000
	s_nop 0
	global_load_lds_dwordx4 v[218:219], off
	s_waitcnt vmcnt(8)
	s_waitcnt lgkmcnt(0)
	s_barrier
	s_setprio 1
	s_waitcnt lgkmcnt(0)
	v_mfma_f32_16x16x32_bf16 v[122:125], v[130:133], v[174:177], 0
	v_mfma_f32_16x16x32_bf16 v[126:129], v[138:141], v[174:177], 0
	v_mfma_f32_16x16x32_bf16 v[110:113], v[130:133], v[194:197], 0
	v_mfma_f32_16x16x32_bf16 v[106:109], v[138:141], v[194:197], 0
	v_mfma_f32_16x16x32_bf16 v[94:97], v[130:133], v[202:205], 0
	v_mfma_f32_16x16x32_bf16 v[90:93], v[138:141], v[202:205], 0
	v_mfma_f32_16x16x32_bf16 v[78:81], v[130:133], v[210:213], 0
	v_mfma_f32_16x16x32_bf16 v[74:77], v[138:141], v[210:213], 0
	v_mfma_f32_16x16x32_bf16 v[122:125], v[134:137], v[190:193], v[122:125]
	v_mfma_f32_16x16x32_bf16 v[126:129], v[142:145], v[190:193], v[126:129]
	v_mfma_f32_16x16x32_bf16 v[110:113], v[134:137], v[198:201], v[110:113]
	v_mfma_f32_16x16x32_bf16 v[106:109], v[142:145], v[198:201], v[106:109]
	v_mfma_f32_16x16x32_bf16 v[94:97], v[134:137], v[206:209], v[94:97]
	v_mfma_f32_16x16x32_bf16 v[90:93], v[142:145], v[206:209], v[90:93]
	v_mfma_f32_16x16x32_bf16 v[78:81], v[134:137], v[214:217], v[78:81]
	v_mfma_f32_16x16x32_bf16 v[74:77], v[142:145], v[214:217], v[74:77]
	s_setprio 0
	s_setprio 1
	v_mfma_f32_16x16x32_bf16 v[118:121], v[146:149], v[174:177], 0
	v_mfma_f32_16x16x32_bf16 v[114:117], v[154:157], v[174:177], 0
	v_mfma_f32_16x16x32_bf16 v[102:105], v[146:149], v[194:197], 0
	v_mfma_f32_16x16x32_bf16 v[98:101], v[154:157], v[194:197], 0
	v_mfma_f32_16x16x32_bf16 v[86:89], v[146:149], v[202:205], 0
	v_mfma_f32_16x16x32_bf16 v[82:85], v[154:157], v[202:205], 0
	v_mfma_f32_16x16x32_bf16 v[70:73], v[146:149], v[210:213], 0
	v_mfma_f32_16x16x32_bf16 v[66:69], v[154:157], v[210:213], 0
	v_mfma_f32_16x16x32_bf16 v[118:121], v[150:153], v[190:193], v[118:121]
	v_mfma_f32_16x16x32_bf16 v[114:117], v[170:173], v[190:193], v[114:117]
	v_mfma_f32_16x16x32_bf16 v[102:105], v[150:153], v[198:201], v[102:105]
	v_mfma_f32_16x16x32_bf16 v[98:101], v[170:173], v[198:201], v[98:101]
	v_mfma_f32_16x16x32_bf16 v[86:89], v[150:153], v[206:209], v[86:89]
	v_mfma_f32_16x16x32_bf16 v[82:85], v[170:173], v[206:209], v[82:85]
	v_mfma_f32_16x16x32_bf16 v[70:73], v[150:153], v[214:217], v[70:73]
	v_mfma_f32_16x16x32_bf16 v[66:69], v[170:173], v[214:217], v[66:69]
	s_setprio 0
	s_barrier
	s_add_i32 s84, s84, s68
	v_lshl_add_u64 v[218:219], s[82:83], 0, v[160:161]
	s_mov_b32 m0, s84
	ds_read_b128 v[174:177], v186 offset:16384
	ds_read_b128 v[190:193], v186 offset:17408
	ds_read_b128 v[194:197], v186 offset:18432
	ds_read_b128 v[198:201], v186 offset:19456
	ds_read_b128 v[202:205], v186 offset:20480
	ds_read_b128 v[206:209], v186 offset:21504
	ds_read_b128 v[210:213], v186 offset:22528
	ds_read_b128 v[214:217], v186 offset:23552
	global_load_lds_dwordx4 v[218:219], off
	s_add_i32 m0, s84, 0x2000
	v_lshl_add_u64 v[220:221], s[82:83], 0, v[164:165]
	s_add_u32 s82, s82, s52
	s_addc_u32 s83, s83, s53
	s_add_i32 s84, s85, s68
	global_load_lds_dwordx4 v[220:221], off
	v_lshl_add_u64 v[222:223], s[82:83], 0, v[160:161]
	s_mov_b32 m0, s84
	v_lshl_add_u64 v[224:225], s[82:83], 0, v[164:165]
	global_load_lds_dwordx4 v[222:223], off
	s_add_i32 m0, s84, 0x2000
	v_lshl_add_u64 v[226:227], s[8:9], 0, v[158:159]
	global_load_lds_dwordx4 v[224:225], off
	s_mov_b32 m0, s69
	v_lshl_add_u64 v[228:229], s[8:9], 0, v[162:163]
	global_load_lds_dwordx4 v[226:227], off
	s_mov_b32 m0, s12
	s_nop 0
	global_load_lds_dwordx4 v[228:229], off
	s_waitcnt vmcnt(8)
	s_waitcnt lgkmcnt(0)
	s_barrier
	s_setprio 1
	s_waitcnt lgkmcnt(0)
	v_mfma_f32_16x16x32_bf16 v[62:65], v[130:133], v[174:177], 0
	v_mfma_f32_16x16x32_bf16 v[58:61], v[138:141], v[174:177], 0
	v_mfma_f32_16x16x32_bf16 v[44:47], v[130:133], v[194:197], 0
	v_mfma_f32_16x16x32_bf16 v[40:43], v[138:141], v[194:197], 0
	v_mfma_f32_16x16x32_bf16 v[28:31], v[130:133], v[202:205], 0
	v_mfma_f32_16x16x32_bf16 v[24:27], v[138:141], v[202:205], 0
	v_mfma_f32_16x16x32_bf16 v[12:15], v[130:133], v[210:213], 0
	v_mfma_f32_16x16x32_bf16 v[8:11], v[138:141], v[210:213], 0
	v_mfma_f32_16x16x32_bf16 v[62:65], v[134:137], v[190:193], v[62:65]
	v_mfma_f32_16x16x32_bf16 v[58:61], v[142:145], v[190:193], v[58:61]
	v_mfma_f32_16x16x32_bf16 v[44:47], v[134:137], v[198:201], v[44:47]
	v_mfma_f32_16x16x32_bf16 v[40:43], v[142:145], v[198:201], v[40:43]
	v_mfma_f32_16x16x32_bf16 v[28:31], v[134:137], v[206:209], v[28:31]
	v_mfma_f32_16x16x32_bf16 v[24:27], v[142:145], v[206:209], v[24:27]
	v_mfma_f32_16x16x32_bf16 v[12:15], v[134:137], v[214:217], v[12:15]
	v_mfma_f32_16x16x32_bf16 v[8:11], v[142:145], v[214:217], v[8:11]
	s_setprio 0
	s_setprio 1
	v_mfma_f32_16x16x32_bf16 v[54:57], v[146:149], v[174:177], 0
	v_mfma_f32_16x16x32_bf16 v[50:53], v[154:157], v[174:177], 0
	v_mfma_f32_16x16x32_bf16 v[36:39], v[146:149], v[194:197], 0
	v_mfma_f32_16x16x32_bf16 v[32:35], v[154:157], v[194:197], 0
	v_mfma_f32_16x16x32_bf16 v[20:23], v[146:149], v[202:205], 0
	v_mfma_f32_16x16x32_bf16 v[16:19], v[154:157], v[202:205], 0
	v_mfma_f32_16x16x32_bf16 v[4:7], v[146:149], v[210:213], 0
	v_mfma_f32_16x16x32_bf16 v[0:3], v[154:157], v[210:213], 0
	v_mfma_f32_16x16x32_bf16 v[54:57], v[150:153], v[190:193], v[54:57]
	v_mfma_f32_16x16x32_bf16 v[50:53], v[170:173], v[190:193], v[50:53]
	v_mfma_f32_16x16x32_bf16 v[36:39], v[150:153], v[198:201], v[36:39]
	v_mfma_f32_16x16x32_bf16 v[32:35], v[170:173], v[198:201], v[32:35]
	v_mfma_f32_16x16x32_bf16 v[20:23], v[150:153], v[206:209], v[20:23]
	v_mfma_f32_16x16x32_bf16 v[16:19], v[170:173], v[206:209], v[16:19]
	v_mfma_f32_16x16x32_bf16 v[4:7], v[150:153], v[214:217], v[4:7]
	v_mfma_f32_16x16x32_bf16 v[0:3], v[170:173], v[214:217], v[0:3]
	s_setprio 0
	s_barrier
	s_add_i32 s82, 0, 0x18000
	s_add_i32 s83, 0, 0x1c000
	v_add_u32_e32 v142, s82, v179
	v_add_u32_e32 v170, s83, v179
	ds_read_b128 v[130:133], v142
	ds_read_b128 v[134:137], v142 offset:1024
	ds_read_b128 v[138:141], v142 offset:2048
	ds_read_b128 v[142:145], v142 offset:3072
	ds_read_b128 v[146:149], v170
	ds_read_b128 v[150:153], v170 offset:1024
	ds_read_b128 v[154:157], v170 offset:2048
	ds_read_b128 v[170:173], v170 offset:3072
	s_add_u32 s8, s8, s52
	s_addc_u32 s9, s9, s53
	s_mov_b32 m0, s19
	v_lshl_add_u64 v[230:231], s[8:9], 0, v[158:159]
	ds_read_b128 v[174:177], v186 offset:32768
	ds_read_b128 v[190:193], v186 offset:33792
	ds_read_b128 v[194:197], v186 offset:34816
	ds_read_b128 v[198:201], v186 offset:35840
	ds_read_b128 v[202:205], v186 offset:36864
	ds_read_b128 v[206:209], v186 offset:37888
	ds_read_b128 v[210:213], v186 offset:38912
	ds_read_b128 v[214:217], v186 offset:39936
	global_load_lds_dwordx4 v[230:231], off
	v_lshl_add_u64 v[230:231], s[8:9], 0, v[162:163]
	s_mov_b32 m0, s25
	s_nop 0
	global_load_lds_dwordx4 v[230:231], off
	s_waitcnt vmcnt(8)
	s_waitcnt lgkmcnt(0)
	s_barrier
	s_setprio 1
	s_waitcnt lgkmcnt(0)
	v_mfma_f32_16x16x32_bf16 v[122:125], v[130:133], v[174:177], v[122:125]
	v_mfma_f32_16x16x32_bf16 v[126:129], v[138:141], v[174:177], v[126:129]
	v_mfma_f32_16x16x32_bf16 v[110:113], v[130:133], v[194:197], v[110:113]
	v_mfma_f32_16x16x32_bf16 v[106:109], v[138:141], v[194:197], v[106:109]
	v_mfma_f32_16x16x32_bf16 v[94:97], v[130:133], v[202:205], v[94:97]
	v_mfma_f32_16x16x32_bf16 v[90:93], v[138:141], v[202:205], v[90:93]
	v_mfma_f32_16x16x32_bf16 v[78:81], v[130:133], v[210:213], v[78:81]
	v_mfma_f32_16x16x32_bf16 v[74:77], v[138:141], v[210:213], v[74:77]
	v_mfma_f32_16x16x32_bf16 v[122:125], v[134:137], v[190:193], v[122:125]
	v_mfma_f32_16x16x32_bf16 v[126:129], v[142:145], v[190:193], v[126:129]
	v_mfma_f32_16x16x32_bf16 v[110:113], v[134:137], v[198:201], v[110:113]
	v_mfma_f32_16x16x32_bf16 v[106:109], v[142:145], v[198:201], v[106:109]
	v_mfma_f32_16x16x32_bf16 v[94:97], v[134:137], v[206:209], v[94:97]
	v_mfma_f32_16x16x32_bf16 v[90:93], v[142:145], v[206:209], v[90:93]
	v_mfma_f32_16x16x32_bf16 v[78:81], v[134:137], v[214:217], v[78:81]
	v_mfma_f32_16x16x32_bf16 v[74:77], v[142:145], v[214:217], v[74:77]
	s_setprio 0
	s_setprio 1
	v_mfma_f32_16x16x32_bf16 v[118:121], v[146:149], v[174:177], v[118:121]
	v_mfma_f32_16x16x32_bf16 v[114:117], v[154:157], v[174:177], v[114:117]
	v_mfma_f32_16x16x32_bf16 v[102:105], v[146:149], v[194:197], v[102:105]
	v_mfma_f32_16x16x32_bf16 v[98:101], v[154:157], v[194:197], v[98:101]
	v_mfma_f32_16x16x32_bf16 v[86:89], v[146:149], v[202:205], v[86:89]
	v_mfma_f32_16x16x32_bf16 v[82:85], v[154:157], v[202:205], v[82:85]
	v_mfma_f32_16x16x32_bf16 v[70:73], v[146:149], v[210:213], v[70:73]
	v_mfma_f32_16x16x32_bf16 v[66:69], v[154:157], v[210:213], v[66:69]
	v_mfma_f32_16x16x32_bf16 v[118:121], v[150:153], v[190:193], v[118:121]
	v_mfma_f32_16x16x32_bf16 v[114:117], v[170:173], v[190:193], v[114:117]
	v_mfma_f32_16x16x32_bf16 v[102:105], v[150:153], v[198:201], v[102:105]
	v_mfma_f32_16x16x32_bf16 v[98:101], v[170:173], v[198:201], v[98:101]
	v_mfma_f32_16x16x32_bf16 v[86:89], v[150:153], v[206:209], v[86:89]
	v_mfma_f32_16x16x32_bf16 v[82:85], v[170:173], v[206:209], v[82:85]
	v_mfma_f32_16x16x32_bf16 v[70:73], v[150:153], v[214:217], v[70:73]
	v_mfma_f32_16x16x32_bf16 v[66:69], v[170:173], v[214:217], v[66:69]
	s_setprio 0
	s_barrier
	s_add_i32 s8, s82, s68
	v_lshl_add_u64 v[218:219], v[218:219], 0, s[34:35]
	s_mov_b32 m0, s8
	ds_read_b128 v[174:177], v186 offset:49152
	ds_read_b128 v[190:193], v186 offset:50176
	ds_read_b128 v[194:197], v186 offset:51200
	ds_read_b128 v[198:201], v186 offset:52224
	ds_read_b128 v[202:205], v186 offset:53248
	ds_read_b128 v[206:209], v186 offset:54272
	ds_read_b128 v[210:213], v186 offset:55296
	ds_read_b128 v[214:217], v186 offset:56320
	global_load_lds_dwordx4 v[218:219], off
	v_lshl_add_u64 v[218:219], v[220:221], 0, s[34:35]
	s_add_i32 m0, s8, 0x2000
	s_add_i32 s8, s83, s68
	global_load_lds_dwordx4 v[218:219], off
	v_lshl_add_u64 v[218:219], v[222:223], 0, s[34:35]
	s_mov_b32 m0, s8
	s_nop 0
	global_load_lds_dwordx4 v[218:219], off
	v_lshl_add_u64 v[218:219], v[224:225], 0, s[34:35]
	s_add_i32 m0, s8, 0x2000
	s_nop 0
	global_load_lds_dwordx4 v[218:219], off
	v_lshl_add_u64 v[218:219], v[226:227], 0, s[34:35]
	s_mov_b32 m0, s79
	s_nop 0
	global_load_lds_dwordx4 v[218:219], off
	v_lshl_add_u64 v[218:219], v[228:229], 0, s[34:35]
	s_mov_b32 m0, s88
	s_nop 0
	global_load_lds_dwordx4 v[218:219], off
	s_waitcnt vmcnt(8)
	s_waitcnt lgkmcnt(0)
	s_barrier
	s_setprio 1
	s_waitcnt lgkmcnt(0)
	v_mfma_f32_16x16x32_bf16 v[62:65], v[130:133], v[174:177], v[62:65]
	v_mfma_f32_16x16x32_bf16 v[58:61], v[138:141], v[174:177], v[58:61]
	v_mfma_f32_16x16x32_bf16 v[44:47], v[130:133], v[194:197], v[44:47]
	v_mfma_f32_16x16x32_bf16 v[40:43], v[138:141], v[194:197], v[40:43]
	v_mfma_f32_16x16x32_bf16 v[28:31], v[130:133], v[202:205], v[28:31]
	v_mfma_f32_16x16x32_bf16 v[24:27], v[138:141], v[202:205], v[24:27]
	v_mfma_f32_16x16x32_bf16 v[12:15], v[130:133], v[210:213], v[12:15]
	v_mfma_f32_16x16x32_bf16 v[8:11], v[138:141], v[210:213], v[8:11]
	v_mfma_f32_16x16x32_bf16 v[62:65], v[134:137], v[190:193], v[62:65]
	v_mfma_f32_16x16x32_bf16 v[58:61], v[142:145], v[190:193], v[58:61]
	v_mfma_f32_16x16x32_bf16 v[44:47], v[134:137], v[198:201], v[44:47]
	v_mfma_f32_16x16x32_bf16 v[40:43], v[142:145], v[198:201], v[40:43]
	v_mfma_f32_16x16x32_bf16 v[28:31], v[134:137], v[206:209], v[28:31]
	v_mfma_f32_16x16x32_bf16 v[24:27], v[142:145], v[206:209], v[24:27]
	v_mfma_f32_16x16x32_bf16 v[12:15], v[134:137], v[214:217], v[12:15]
	v_mfma_f32_16x16x32_bf16 v[8:11], v[142:145], v[214:217], v[8:11]
	s_setprio 0
	s_setprio 1
	v_mfma_f32_16x16x32_bf16 v[54:57], v[146:149], v[174:177], v[54:57]
	v_mfma_f32_16x16x32_bf16 v[50:53], v[154:157], v[174:177], v[50:53]
	v_mfma_f32_16x16x32_bf16 v[36:39], v[146:149], v[194:197], v[36:39]
	v_mfma_f32_16x16x32_bf16 v[32:35], v[154:157], v[194:197], v[32:35]
	v_mfma_f32_16x16x32_bf16 v[20:23], v[146:149], v[202:205], v[20:23]
	v_mfma_f32_16x16x32_bf16 v[16:19], v[154:157], v[202:205], v[16:19]
	v_mfma_f32_16x16x32_bf16 v[4:7], v[146:149], v[210:213], v[4:7]
	v_mfma_f32_16x16x32_bf16 v[0:3], v[154:157], v[210:213], v[0:3]
	v_mfma_f32_16x16x32_bf16 v[54:57], v[150:153], v[190:193], v[54:57]
	v_mfma_f32_16x16x32_bf16 v[50:53], v[170:173], v[190:193], v[50:53]
	v_mfma_f32_16x16x32_bf16 v[36:39], v[150:153], v[198:201], v[36:39]
	v_mfma_f32_16x16x32_bf16 v[32:35], v[170:173], v[198:201], v[32:35]
	v_mfma_f32_16x16x32_bf16 v[20:23], v[150:153], v[206:209], v[20:23]
	v_mfma_f32_16x16x32_bf16 v[16:19], v[170:173], v[206:209], v[16:19]
	v_mfma_f32_16x16x32_bf16 v[4:7], v[150:153], v[214:217], v[4:7]
	v_mfma_f32_16x16x32_bf16 v[0:3], v[170:173], v[214:217], v[0:3]
	s_setprio 0
	s_barrier
	s_add_u32 s6, s6, 0x100
	s_addc_u32 s7, s7, 0
	s_add_u32 s29, s29, 0x100
	s_addc_u32 s57, s57, 0
	s_cmp_ge_i32 s72, s70
	s_mov_b32 s8, s72

.LBB0_1360:
	s_and_b64 vcc, exec, s[40:41]
	s_cbranch_vccnz .LBB0_1362
	v_lshlrev_b32_e32 v2, 8, v167
	v_add_u32_e32 v0, v2, v49
	v_ashrrev_i32_e32 v1, 31, v0
	v_lshl_add_u64 v[0:1], v[0:1], 2, s[50:51]
	global_load_dword v162, v[0:1], off
	v_add_u32_e32 v0, v2, v151
	v_ashrrev_i32_e32 v1, 31, v0
	v_lshl_add_u64 v[0:1], v[0:1], 2, s[50:51]
	global_load_dword v163, v[0:1], off
	v_or_b32_e32 v2, 0x80, v2
	v_add_u32_e32 v0, v2, v49
	v_ashrrev_i32_e32 v1, 31, v0
	v_lshl_add_u64 v[0:1], v[0:1], 2, s[50:51]
	global_load_dword v164, v[0:1], off
	v_add_u32_e32 v0, v2, v151
	v_ashrrev_i32_e32 v1, 31, v0
	v_lshl_add_u64 v[0:1], v[0:1], 2, s[50:51]
	global_load_dword v165, v[0:1], off
	s_waitcnt vmcnt(0)
	v_max_i32_e32 v162, 0, v162
	v_mul_lo_u32 v162, v162, s4
	v_add_lshl_u32 v162, v162, v147, 1
	v_max_i32_e32 v163, 0, v163
	v_mul_lo_u32 v163, v163, s4
	v_add_lshl_u32 v163, v163, v155, 1
	v_max_i32_e32 v164, 0, v164
	v_mul_lo_u32 v164, v164, s4
	v_add_lshl_u32 v164, v164, v147, 1
	v_max_i32_e32 v165, 0, v165
	v_mul_lo_u32 v165, v165, s4
	v_add_lshl_u32 v165, v165, v155, 1

.Lmy_z_3:
	v_mov_b32_e32 v143, v48
	v_mov_b32_e32 v141, v48
	s_mov_b32 s28, 0
	s_mov_b64 s[6:7], 0x100
	s_mov_b64 s[8:9], s[66:67]
	s_cmp_eq_u32 s5, s28
	s_cselect_b64 vcc, -1, 0
	s_add_i32 s28, s28, 2
	s_and_b64 s[78:79], vcc, exec
	s_cselect_b32 s29, 0, s7
	s_cselect_b32 s30, 0, s6
	s_add_i32 s72, 0, 0x10000
	s_add_u32 s78, s46, s30
	v_add_u32_e32 v150, s72, v161
	s_addc_u32 s79, s47, s29
	s_add_i32 s29, 0, 0x14000
	ds_read_b128 v[170:173], v150
	ds_read_b128 v[174:177], v150 offset:1024
	ds_read_b128 v[178:181], v150 offset:2048
	ds_read_b128 v[182:185], v150 offset:3072
	v_add_u32_e32 v150, s29, v161
	ds_read_b128 v[186:189], v150
	ds_read_b128 v[190:193], v150 offset:1024
	ds_read_b128 v[194:197], v150 offset:2048
	ds_read_b128 v[198:201], v150 offset:3072
	v_lshl_add_u64 v[148:149], v[144:145], 0, s[6:7]
	v_cndmask_b32_e32 v149, v149, v135, vcc
	v_cndmask_b32_e32 v148, v148, v134, vcc
	v_lshl_add_u64 v[152:153], s[8:9], 0, v[140:141]
	s_add_i32 m0, s38, 0xc000
	ds_read_b128 v[202:205], v139
	ds_read_b128 v[206:209], v139 offset:1024
	ds_read_b128 v[210:213], v139 offset:2048
	ds_read_b128 v[214:217], v139 offset:3072
	ds_read_b128 v[218:221], v139 offset:4096
	ds_read_b128 v[222:225], v139 offset:5120
	ds_read_b128 v[226:229], v139 offset:6144
	ds_read_b128 v[230:233], v139 offset:7168
	global_load_lds_dwordx4 v[152:153], off
	v_lshl_add_u64 v[152:153], s[8:9], 0, v[142:143]
	s_add_i32 m0, s38, 0xe000
	s_nop 0
	global_load_lds_dwordx4 v[152:153], off
	s_waitcnt vmcnt(8)
	s_waitcnt lgkmcnt(0)
	s_barrier
	s_setprio 1
	s_waitcnt lgkmcnt(0)
	v_mfma_f32_16x16x32_bf16 v[126:129], v[170:173], v[202:205], 0
	v_mfma_f32_16x16x32_bf16 v[118:121], v[178:181], v[202:205], 0
	v_mfma_f32_16x16x32_bf16 v[110:113], v[170:173], v[210:213], 0
	v_mfma_f32_16x16x32_bf16 v[102:105], v[178:181], v[210:213], 0
	v_mfma_f32_16x16x32_bf16 v[94:97], v[170:173], v[218:221], 0
	v_mfma_f32_16x16x32_bf16 v[86:89], v[178:181], v[218:221], 0
	v_mfma_f32_16x16x32_bf16 v[78:81], v[170:173], v[226:229], 0
	v_mfma_f32_16x16x32_bf16 v[70:73], v[178:181], v[226:229], 0
	v_mfma_f32_16x16x32_bf16 v[126:129], v[174:177], v[206:209], v[126:129]
	v_mfma_f32_16x16x32_bf16 v[118:121], v[182:185], v[206:209], v[118:121]
	v_mfma_f32_16x16x32_bf16 v[110:113], v[174:177], v[214:217], v[110:113]
	v_mfma_f32_16x16x32_bf16 v[102:105], v[182:185], v[214:217], v[102:105]
	v_mfma_f32_16x16x32_bf16 v[94:97], v[174:177], v[222:225], v[94:97]
	v_mfma_f32_16x16x32_bf16 v[86:89], v[182:185], v[222:225], v[86:89]
	v_mfma_f32_16x16x32_bf16 v[78:81], v[174:177], v[230:233], v[78:81]
	v_mfma_f32_16x16x32_bf16 v[70:73], v[182:185], v[230:233], v[70:73]
	s_setprio 0
	s_setprio 1
	v_mfma_f32_16x16x32_bf16 v[122:125], v[186:189], v[202:205], 0
	v_mfma_f32_16x16x32_bf16 v[114:117], v[194:197], v[202:205], 0
	v_mfma_f32_16x16x32_bf16 v[106:109], v[186:189], v[210:213], 0
	v_mfma_f32_16x16x32_bf16 v[98:101], v[194:197], v[210:213], 0
	v_mfma_f32_16x16x32_bf16 v[90:93], v[186:189], v[218:221], 0
	v_mfma_f32_16x16x32_bf16 v[82:85], v[194:197], v[218:221], 0
	v_mfma_f32_16x16x32_bf16 v[74:77], v[186:189], v[226:229], 0
	v_mfma_f32_16x16x32_bf16 v[66:69], v[194:197], v[226:229], 0
	v_mfma_f32_16x16x32_bf16 v[122:125], v[190:193], v[206:209], v[122:125]
	v_mfma_f32_16x16x32_bf16 v[114:117], v[198:201], v[206:209], v[114:117]
	v_mfma_f32_16x16x32_bf16 v[106:109], v[190:193], v[214:217], v[106:109]
	v_mfma_f32_16x16x32_bf16 v[98:101], v[198:201], v[214:217], v[98:101]
	v_mfma_f32_16x16x32_bf16 v[90:93], v[190:193], v[222:225], v[90:93]
	v_mfma_f32_16x16x32_bf16 v[82:85], v[198:201], v[222:225], v[82:85]
	v_mfma_f32_16x16x32_bf16 v[74:77], v[190:193], v[230:233], v[74:77]
	v_mfma_f32_16x16x32_bf16 v[66:69], v[198:201], v[230:233], v[66:69]
	s_setprio 0
	s_barrier
	s_add_i32 s30, s72, s63
	v_lshl_add_u64 v[152:153], v[148:149], 0, v[130:131]
	s_mov_b32 m0, s30
	ds_read_b128 v[202:205], v139 offset:16384
	ds_read_b128 v[206:209], v139 offset:17408
	ds_read_b128 v[210:213], v139 offset:18432
	ds_read_b128 v[214:217], v139 offset:19456
	ds_read_b128 v[218:221], v139 offset:20480
	ds_read_b128 v[222:225], v139 offset:21504
	ds_read_b128 v[226:229], v139 offset:22528
	ds_read_b128 v[230:233], v139 offset:23552
	global_load_lds_dwordx4 v[152:153], off
	v_lshl_add_u64 v[156:157], v[148:149], 0, v[132:133]
	s_add_i32 m0, s30, 0x2000
	v_lshl_add_u64 v[148:149], v[148:149], 0, s[52:53]
	s_add_i32 s29, s29, s63
	global_load_lds_dwordx4 v[156:157], off
	v_lshl_add_u64 v[246:247], v[148:149], 0, v[130:131]
	s_mov_b32 m0, s29
	v_lshl_add_u64 v[148:149], v[148:149], 0, v[132:133]
	global_load_lds_dwordx4 v[246:247], off
	s_add_i32 m0, s29, 0x2000
	s_and_b64 vcc, s[42:43], vcc
	global_load_lds_dwordx4 v[148:149], off
	v_cndmask_b32_e32 v248, v136, v162, vcc
	s_mov_b32 m0, s38
	v_cndmask_b32_e32 v250, v138, v163, vcc
	global_load_lds_dwordx4 v248, s[78:79]
	s_mov_b32 m0, s39
	v_mov_b32_e32 v249, v48
	global_load_lds_dwordx4 v250, s[78:79]
	s_waitcnt vmcnt(8)
	s_waitcnt lgkmcnt(0)
	v_mov_b32_e32 v251, v48
	v_lshl_add_u64 v[248:249], s[78:79], 0, v[248:249]
	v_lshl_add_u64 v[250:251], s[78:79], 0, v[250:251]
	s_barrier
	s_setprio 1
	s_waitcnt lgkmcnt(0)
	v_mfma_f32_16x16x32_bf16 v[62:65], v[170:173], v[202:205], 0
	v_mfma_f32_16x16x32_bf16 v[54:57], v[178:181], v[202:205], 0
	v_mfma_f32_16x16x32_bf16 v[44:47], v[170:173], v[210:213], 0
	v_mfma_f32_16x16x32_bf16 v[36:39], v[178:181], v[210:213], 0
	v_mfma_f32_16x16x32_bf16 v[28:31], v[170:173], v[218:221], 0
	v_mfma_f32_16x16x32_bf16 v[20:23], v[178:181], v[218:221], 0
	v_mfma_f32_16x16x32_bf16 v[12:15], v[170:173], v[226:229], 0
	v_mfma_f32_16x16x32_bf16 v[4:7], v[178:181], v[226:229], 0
	v_mfma_f32_16x16x32_bf16 v[62:65], v[174:177], v[206:209], v[62:65]
	v_mfma_f32_16x16x32_bf16 v[54:57], v[182:185], v[206:209], v[54:57]
	v_mfma_f32_16x16x32_bf16 v[44:47], v[174:177], v[214:217], v[44:47]
	v_mfma_f32_16x16x32_bf16 v[36:39], v[182:185], v[214:217], v[36:39]
	v_mfma_f32_16x16x32_bf16 v[28:31], v[174:177], v[222:225], v[28:31]
	v_mfma_f32_16x16x32_bf16 v[20:23], v[182:185], v[222:225], v[20:23]
	v_mfma_f32_16x16x32_bf16 v[12:15], v[174:177], v[230:233], v[12:15]
	v_mfma_f32_16x16x32_bf16 v[4:7], v[182:185], v[230:233], v[4:7]
	s_setprio 0
	s_setprio 1
	v_mfma_f32_16x16x32_bf16 v[58:61], v[186:189], v[202:205], 0
	v_mfma_f32_16x16x32_bf16 v[50:53], v[194:197], v[202:205], 0
	v_mfma_f32_16x16x32_bf16 v[40:43], v[186:189], v[210:213], 0
	v_mfma_f32_16x16x32_bf16 v[32:35], v[194:197], v[210:213], 0
	v_mfma_f32_16x16x32_bf16 v[24:27], v[186:189], v[218:221], 0
	v_mfma_f32_16x16x32_bf16 v[16:19], v[194:197], v[218:221], 0
	v_mfma_f32_16x16x32_bf16 v[8:11], v[186:189], v[226:229], 0
	v_mfma_f32_16x16x32_bf16 v[0:3], v[194:197], v[226:229], 0
	v_mfma_f32_16x16x32_bf16 v[58:61], v[190:193], v[206:209], v[58:61]
	v_mfma_f32_16x16x32_bf16 v[50:53], v[198:201], v[206:209], v[50:53]
	v_mfma_f32_16x16x32_bf16 v[40:43], v[190:193], v[214:217], v[40:43]
	v_mfma_f32_16x16x32_bf16 v[32:35], v[198:201], v[214:217], v[32:35]
	v_mfma_f32_16x16x32_bf16 v[24:27], v[190:193], v[222:225], v[24:27]
	v_mfma_f32_16x16x32_bf16 v[16:19], v[198:201], v[222:225], v[16:19]
	v_mfma_f32_16x16x32_bf16 v[8:11], v[190:193], v[230:233], v[8:11]
	v_mfma_f32_16x16x32_bf16 v[0:3], v[198:201], v[230:233], v[0:3]
	s_setprio 0
	s_barrier
	s_add_i32 s29, 0, 0x18000
	v_add_u32_e32 v150, s29, v161
	s_add_i32 s30, 0, 0x1c000
	ds_read_b128 v[170:173], v150
	ds_read_b128 v[174:177], v150 offset:1024
	ds_read_b128 v[178:181], v150 offset:2048
	ds_read_b128 v[182:185], v150 offset:3072
	v_add_u32_e32 v150, s30, v161
	ds_read_b128 v[186:189], v150
	ds_read_b128 v[190:193], v150 offset:1024
	ds_read_b128 v[194:197], v150 offset:2048
	ds_read_b128 v[198:201], v150 offset:3072
	s_mov_b32 m0, s62
	v_cndmask_b32_e32 v150, v140, v164, vcc
	ds_read_b128 v[202:205], v139 offset:32768
	ds_read_b128 v[206:209], v139 offset:33792
	ds_read_b128 v[210:213], v139 offset:34816
	ds_read_b128 v[214:217], v139 offset:35840
	ds_read_b128 v[218:221], v139 offset:36864
	ds_read_b128 v[222:225], v139 offset:37888
	ds_read_b128 v[226:229], v139 offset:38912
	ds_read_b128 v[230:233], v139 offset:39936
	v_cndmask_b32_e32 v154, v142, v165, vcc
	global_load_lds_dwordx4 v150, s[78:79]
	s_mov_b32 m0, s97
	s_nop 0
	global_load_lds_dwordx4 v154, s[78:79]
	s_waitcnt vmcnt(8)
	s_waitcnt lgkmcnt(0)
	s_barrier
	s_setprio 1
	s_waitcnt lgkmcnt(0)
	v_mfma_f32_16x16x32_bf16 v[126:129], v[170:173], v[202:205], v[126:129]
	v_mfma_f32_16x16x32_bf16 v[118:121], v[178:181], v[202:205], v[118:121]
	v_mfma_f32_16x16x32_bf16 v[110:113], v[170:173], v[210:213], v[110:113]
	v_mfma_f32_16x16x32_bf16 v[102:105], v[178:181], v[210:213], v[102:105]
	v_mfma_f32_16x16x32_bf16 v[94:97], v[170:173], v[218:221], v[94:97]
	v_mfma_f32_16x16x32_bf16 v[86:89], v[178:181], v[218:221], v[86:89]
	v_mfma_f32_16x16x32_bf16 v[78:81], v[170:173], v[226:229], v[78:81]
	v_mfma_f32_16x16x32_bf16 v[70:73], v[178:181], v[226:229], v[70:73]
	v_mfma_f32_16x16x32_bf16 v[126:129], v[174:177], v[206:209], v[126:129]
	v_mfma_f32_16x16x32_bf16 v[118:121], v[182:185], v[206:209], v[118:121]
	v_mfma_f32_16x16x32_bf16 v[110:113], v[174:177], v[214:217], v[110:113]
	v_mfma_f32_16x16x32_bf16 v[102:105], v[182:185], v[214:217], v[102:105]
	v_mfma_f32_16x16x32_bf16 v[94:97], v[174:177], v[222:225], v[94:97]
	v_mfma_f32_16x16x32_bf16 v[86:89], v[182:185], v[222:225], v[86:89]
	v_mfma_f32_16x16x32_bf16 v[78:81], v[174:177], v[230:233], v[78:81]
	v_mfma_f32_16x16x32_bf16 v[70:73], v[182:185], v[230:233], v[70:73]
	s_setprio 0
	s_setprio 1
	v_mfma_f32_16x16x32_bf16 v[122:125], v[186:189], v[202:205], v[122:125]
	v_mfma_f32_16x16x32_bf16 v[114:117], v[194:197], v[202:205], v[114:117]
	v_mfma_f32_16x16x32_bf16 v[106:109], v[186:189], v[210:213], v[106:109]
	v_mfma_f32_16x16x32_bf16 v[98:101], v[194:197], v[210:213], v[98:101]
	v_mfma_f32_16x16x32_bf16 v[90:93], v[186:189], v[218:221], v[90:93]
	v_mfma_f32_16x16x32_bf16 v[82:85], v[194:197], v[218:221], v[82:85]
	v_mfma_f32_16x16x32_bf16 v[74:77], v[186:189], v[226:229], v[74:77]
	v_mfma_f32_16x16x32_bf16 v[66:69], v[194:197], v[226:229], v[66:69]
	v_mfma_f32_16x16x32_bf16 v[122:125], v[190:193], v[206:209], v[122:125]
	v_mfma_f32_16x16x32_bf16 v[114:117], v[198:201], v[206:209], v[114:117]
	v_mfma_f32_16x16x32_bf16 v[106:109], v[190:193], v[214:217], v[106:109]
	v_mfma_f32_16x16x32_bf16 v[98:101], v[198:201], v[214:217], v[98:101]
	v_mfma_f32_16x16x32_bf16 v[90:93], v[190:193], v[222:225], v[90:93]
	v_mfma_f32_16x16x32_bf16 v[82:85], v[198:201], v[222:225], v[82:85]
	v_mfma_f32_16x16x32_bf16 v[74:77], v[190:193], v[230:233], v[74:77]
	v_mfma_f32_16x16x32_bf16 v[66:69], v[198:201], v[230:233], v[66:69]
	s_setprio 0
	s_barrier
	s_add_i32 s29, s29, s63
	v_lshl_add_u64 v[152:153], v[152:153], 0, s[34:35]
	s_mov_b32 m0, s29
	ds_read_b128 v[202:205], v139 offset:49152
	ds_read_b128 v[206:209], v139 offset:50176
	ds_read_b128 v[210:213], v139 offset:51200
	ds_read_b128 v[214:217], v139 offset:52224
	ds_read_b128 v[218:221], v139 offset:53248
	ds_read_b128 v[222:225], v139 offset:54272
	ds_read_b128 v[226:229], v139 offset:55296
	ds_read_b128 v[230:233], v139 offset:56320
	global_load_lds_dwordx4 v[152:153], off
	v_lshl_add_u64 v[152:153], v[156:157], 0, s[34:35]
	s_add_i32 m0, s29, 0x2000
	s_add_i32 s29, s30, s63
	global_load_lds_dwordx4 v[152:153], off
	v_lshl_add_u64 v[152:153], v[246:247], 0, s[34:35]
	s_mov_b32 m0, s29
	v_lshl_add_u64 v[148:149], v[148:149], 0, s[34:35]
	global_load_lds_dwordx4 v[152:153], off
	s_add_i32 m0, s29, 0x2000
	s_nop 0
	global_load_lds_dwordx4 v[148:149], off
	v_lshl_add_u64 v[148:149], v[248:249], 0, s[34:35]
	s_mov_b32 m0, s61
	s_nop 0
	global_load_lds_dwordx4 v[148:149], off
	v_lshl_add_u64 v[148:149], v[250:251], 0, s[34:35]
	s_mov_b32 m0, s25
	s_nop 0
	global_load_lds_dwordx4 v[148:149], off
	s_waitcnt vmcnt(8)
	s_waitcnt lgkmcnt(0)
	s_barrier
	s_setprio 1
	s_waitcnt lgkmcnt(0)
	v_mfma_f32_16x16x32_bf16 v[62:65], v[170:173], v[202:205], v[62:65]
	v_mfma_f32_16x16x32_bf16 v[54:57], v[178:181], v[202:205], v[54:57]
	v_mfma_f32_16x16x32_bf16 v[44:47], v[170:173], v[210:213], v[44:47]
	v_mfma_f32_16x16x32_bf16 v[36:39], v[178:181], v[210:213], v[36:39]
	v_mfma_f32_16x16x32_bf16 v[28:31], v[170:173], v[218:221], v[28:31]
	v_mfma_f32_16x16x32_bf16 v[20:23], v[178:181], v[218:221], v[20:23]
	v_mfma_f32_16x16x32_bf16 v[12:15], v[170:173], v[226:229], v[12:15]
	v_mfma_f32_16x16x32_bf16 v[4:7], v[178:181], v[226:229], v[4:7]
	v_mfma_f32_16x16x32_bf16 v[62:65], v[174:177], v[206:209], v[62:65]
	v_mfma_f32_16x16x32_bf16 v[54:57], v[182:185], v[206:209], v[54:57]
	v_mfma_f32_16x16x32_bf16 v[44:47], v[174:177], v[214:217], v[44:47]
	v_mfma_f32_16x16x32_bf16 v[36:39], v[182:185], v[214:217], v[36:39]
	v_mfma_f32_16x16x32_bf16 v[28:31], v[174:177], v[222:225], v[28:31]
	v_mfma_f32_16x16x32_bf16 v[20:23], v[182:185], v[222:225], v[20:23]
	v_mfma_f32_16x16x32_bf16 v[12:15], v[174:177], v[230:233], v[12:15]
	v_mfma_f32_16x16x32_bf16 v[4:7], v[182:185], v[230:233], v[4:7]
	s_setprio 0
	s_setprio 1
	v_mfma_f32_16x16x32_bf16 v[58:61], v[186:189], v[202:205], v[58:61]
	v_mfma_f32_16x16x32_bf16 v[50:53], v[194:197], v[202:205], v[50:53]
	v_mfma_f32_16x16x32_bf16 v[40:43], v[186:189], v[210:213], v[40:43]
	v_mfma_f32_16x16x32_bf16 v[32:35], v[194:197], v[210:213], v[32:35]
	v_mfma_f32_16x16x32_bf16 v[24:27], v[186:189], v[218:221], v[24:27]
	v_mfma_f32_16x16x32_bf16 v[16:19], v[194:197], v[218:221], v[16:19]
	v_mfma_f32_16x16x32_bf16 v[8:11], v[186:189], v[226:229], v[8:11]
	v_mfma_f32_16x16x32_bf16 v[0:3], v[194:197], v[226:229], v[0:3]
	v_mfma_f32_16x16x32_bf16 v[58:61], v[190:193], v[206:209], v[58:61]
	v_mfma_f32_16x16x32_bf16 v[50:53], v[198:201], v[206:209], v[50:53]
	v_mfma_f32_16x16x32_bf16 v[40:43], v[190:193], v[214:217], v[40:43]
	v_mfma_f32_16x16x32_bf16 v[32:35], v[198:201], v[214:217], v[32:35]
	v_mfma_f32_16x16x32_bf16 v[24:27], v[190:193], v[222:225], v[24:27]
	v_mfma_f32_16x16x32_bf16 v[16:19], v[198:201], v[222:225], v[16:19]
	v_mfma_f32_16x16x32_bf16 v[8:11], v[190:193], v[230:233], v[8:11]
	v_mfma_f32_16x16x32_bf16 v[0:3], v[198:201], v[230:233], v[0:3]
	s_setprio 0
	s_barrier
	s_add_u32 s6, s6, 0x100
	s_addc_u32 s7, s7, 0
	s_add_u32 s8, s8, 0x100
	s_addc_u32 s9, s9, 0
	s_cmp_ge_i32 s28, s19

.Lmy_z_4:
	s_add_u32 s6, s78, 0x80
	s_addc_u32 s7, s79, 0
	v_lshl_add_u64 v[130:131], v[130:131], 0, s[36:37]
	s_mov_b32 s8, 0
	s_add_i32 s78, s8, 2
	s_add_u32 s79, s6, 0x80
	s_addc_u32 s9, s7, 0
	s_add_i32 s86, 0, 0x10000
	s_cmp_eq_u32 s93, s8
	s_cselect_b32 s9, s43, s9
	s_cselect_b32 s8, s42, s79
	s_cselect_b64 vcc, -1, 0
	s_add_i32 s79, 0, 0x14000
	v_add_u32_e32 v144, s86, v203
	v_add_u32_e32 v176, s79, v203
	ds_read_b128 v[132:135], v144
	ds_read_b128 v[136:139], v144 offset:1024
	ds_read_b128 v[140:143], v144 offset:2048
	ds_read_b128 v[144:147], v144 offset:3072
	ds_read_b128 v[148:151], v176
	ds_read_b128 v[168:171], v176 offset:1024
	ds_read_b128 v[172:175], v176 offset:2048
	ds_read_b128 v[176:179], v176 offset:3072
	v_cndmask_b32_e32 v153, v131, v167, vcc
	v_cndmask_b32_e32 v152, v130, v166, vcc
	v_lshl_add_u64 v[222:223], s[6:7], 0, v[162:163]
	s_add_i32 m0, s25, 0xc000
	ds_read_b128 v[180:183], v208
	ds_read_b128 v[184:187], v208 offset:1024
	ds_read_b128 v[188:191], v208 offset:2048
	ds_read_b128 v[192:195], v208 offset:3072
	ds_read_b128 v[196:199], v208 offset:4096
	ds_read_b128 v[210:213], v208 offset:5120
	ds_read_b128 v[214:217], v208 offset:6144
	ds_read_b128 v[218:221], v208 offset:7168
	global_load_lds_dwordx4 v[222:223], off
	v_lshl_add_u64 v[222:223], s[6:7], 0, v[164:165]
	s_add_i32 m0, s25, 0xe000
	s_nop 0
	global_load_lds_dwordx4 v[222:223], off
	s_waitcnt vmcnt(8)
	s_waitcnt lgkmcnt(0)
	s_barrier
	s_setprio 1
	s_waitcnt lgkmcnt(0)
	v_mfma_f32_16x16x32_bf16 v[122:125], v[132:135], v[180:183], 0
	v_mfma_f32_16x16x32_bf16 v[126:129], v[140:143], v[180:183], 0
	v_mfma_f32_16x16x32_bf16 v[110:113], v[132:135], v[188:191], 0
	v_mfma_f32_16x16x32_bf16 v[106:109], v[140:143], v[188:191], 0
	v_mfma_f32_16x16x32_bf16 v[94:97], v[132:135], v[196:199], 0
	v_mfma_f32_16x16x32_bf16 v[90:93], v[140:143], v[196:199], 0
	v_mfma_f32_16x16x32_bf16 v[78:81], v[132:135], v[214:217], 0
	v_mfma_f32_16x16x32_bf16 v[74:77], v[140:143], v[214:217], 0
	v_mfma_f32_16x16x32_bf16 v[122:125], v[136:139], v[184:187], v[122:125]
	v_mfma_f32_16x16x32_bf16 v[126:129], v[144:147], v[184:187], v[126:129]
	v_mfma_f32_16x16x32_bf16 v[110:113], v[136:139], v[192:195], v[110:113]
	v_mfma_f32_16x16x32_bf16 v[106:109], v[144:147], v[192:195], v[106:109]
	v_mfma_f32_16x16x32_bf16 v[94:97], v[136:139], v[210:213], v[94:97]
	v_mfma_f32_16x16x32_bf16 v[90:93], v[144:147], v[210:213], v[90:93]
	v_mfma_f32_16x16x32_bf16 v[78:81], v[136:139], v[218:221], v[78:81]
	v_mfma_f32_16x16x32_bf16 v[74:77], v[144:147], v[218:221], v[74:77]
	s_setprio 0
	s_setprio 1
	v_mfma_f32_16x16x32_bf16 v[118:121], v[148:151], v[180:183], 0
	v_mfma_f32_16x16x32_bf16 v[114:117], v[172:175], v[180:183], 0
	v_mfma_f32_16x16x32_bf16 v[102:105], v[148:151], v[188:191], 0
	v_mfma_f32_16x16x32_bf16 v[98:101], v[172:175], v[188:191], 0
	v_mfma_f32_16x16x32_bf16 v[86:89], v[148:151], v[196:199], 0
	v_mfma_f32_16x16x32_bf16 v[82:85], v[172:175], v[196:199], 0
	v_mfma_f32_16x16x32_bf16 v[70:73], v[148:151], v[214:217], 0
	v_mfma_f32_16x16x32_bf16 v[66:69], v[172:175], v[214:217], 0
	v_mfma_f32_16x16x32_bf16 v[118:121], v[168:171], v[184:187], v[118:121]
	v_mfma_f32_16x16x32_bf16 v[114:117], v[176:179], v[184:187], v[114:117]
	v_mfma_f32_16x16x32_bf16 v[102:105], v[168:171], v[192:195], v[102:105]
	v_mfma_f32_16x16x32_bf16 v[98:101], v[176:179], v[192:195], v[98:101]
	v_mfma_f32_16x16x32_bf16 v[86:89], v[168:171], v[210:213], v[86:89]
	v_mfma_f32_16x16x32_bf16 v[82:85], v[176:179], v[210:213], v[82:85]
	v_mfma_f32_16x16x32_bf16 v[70:73], v[168:171], v[218:221], v[70:73]
	v_mfma_f32_16x16x32_bf16 v[66:69], v[176:179], v[218:221], v[66:69]
	s_setprio 0
	s_barrier
	s_add_i32 s86, s86, s19
	v_lshl_add_u64 v[222:223], v[152:153], 0, v[156:157]
	s_mov_b32 m0, s86
	ds_read_b128 v[180:183], v208 offset:16384
	ds_read_b128 v[184:187], v208 offset:17408
	ds_read_b128 v[188:191], v208 offset:18432
	ds_read_b128 v[192:195], v208 offset:19456
	ds_read_b128 v[196:199], v208 offset:20480
	ds_read_b128 v[210:213], v208 offset:21504
	ds_read_b128 v[214:217], v208 offset:22528
	ds_read_b128 v[218:221], v208 offset:23552
	global_load_lds_dwordx4 v[222:223], off
	v_lshl_add_u64 v[224:225], v[152:153], 0, v[160:161]
	s_add_i32 m0, s86, 0x2000
	v_lshl_add_u64 v[152:153], v[152:153], 0, s[50:51]
	s_add_i32 s79, s79, s19
	global_load_lds_dwordx4 v[224:225], off
	v_lshl_add_u64 v[226:227], v[152:153], 0, v[156:157]
	s_mov_b32 m0, s79
	v_lshl_add_u64 v[152:153], v[152:153], 0, v[160:161]
	global_load_lds_dwordx4 v[226:227], off
	s_add_i32 m0, s79, 0x2000
	v_lshl_add_u64 v[228:229], s[8:9], 0, v[154:155]
	global_load_lds_dwordx4 v[152:153], off
	s_mov_b32 m0, s25
	v_lshl_add_u64 v[230:231], s[8:9], 0, v[158:159]
	global_load_lds_dwordx4 v[228:229], off
	s_mov_b32 m0, s38
	s_nop 0
	global_load_lds_dwordx4 v[230:231], off
	s_waitcnt vmcnt(8)
	s_waitcnt lgkmcnt(0)
	s_barrier
	s_setprio 1
	s_waitcnt lgkmcnt(0)
	v_mfma_f32_16x16x32_bf16 v[62:65], v[132:135], v[180:183], 0
	v_mfma_f32_16x16x32_bf16 v[58:61], v[140:143], v[180:183], 0
	v_mfma_f32_16x16x32_bf16 v[44:47], v[132:135], v[188:191], 0
	v_mfma_f32_16x16x32_bf16 v[40:43], v[140:143], v[188:191], 0
	v_mfma_f32_16x16x32_bf16 v[28:31], v[132:135], v[196:199], 0
	v_mfma_f32_16x16x32_bf16 v[24:27], v[140:143], v[196:199], 0
	v_mfma_f32_16x16x32_bf16 v[12:15], v[132:135], v[214:217], 0
	v_mfma_f32_16x16x32_bf16 v[8:11], v[140:143], v[214:217], 0
	v_mfma_f32_16x16x32_bf16 v[62:65], v[136:139], v[184:187], v[62:65]
	v_mfma_f32_16x16x32_bf16 v[58:61], v[144:147], v[184:187], v[58:61]
	v_mfma_f32_16x16x32_bf16 v[44:47], v[136:139], v[192:195], v[44:47]
	v_mfma_f32_16x16x32_bf16 v[40:43], v[144:147], v[192:195], v[40:43]
	v_mfma_f32_16x16x32_bf16 v[28:31], v[136:139], v[210:213], v[28:31]
	v_mfma_f32_16x16x32_bf16 v[24:27], v[144:147], v[210:213], v[24:27]
	v_mfma_f32_16x16x32_bf16 v[12:15], v[136:139], v[218:221], v[12:15]
	v_mfma_f32_16x16x32_bf16 v[8:11], v[144:147], v[218:221], v[8:11]
	s_setprio 0
	s_setprio 1
	v_mfma_f32_16x16x32_bf16 v[54:57], v[148:151], v[180:183], 0
	v_mfma_f32_16x16x32_bf16 v[50:53], v[172:175], v[180:183], 0
	v_mfma_f32_16x16x32_bf16 v[36:39], v[148:151], v[188:191], 0
	v_mfma_f32_16x16x32_bf16 v[32:35], v[172:175], v[188:191], 0
	v_mfma_f32_16x16x32_bf16 v[20:23], v[148:151], v[196:199], 0
	v_mfma_f32_16x16x32_bf16 v[16:19], v[172:175], v[196:199], 0
	v_mfma_f32_16x16x32_bf16 v[4:7], v[148:151], v[214:217], 0
	v_mfma_f32_16x16x32_bf16 v[0:3], v[172:175], v[214:217], 0
	v_mfma_f32_16x16x32_bf16 v[54:57], v[168:171], v[184:187], v[54:57]
	v_mfma_f32_16x16x32_bf16 v[50:53], v[176:179], v[184:187], v[50:53]
	v_mfma_f32_16x16x32_bf16 v[36:39], v[168:171], v[192:195], v[36:39]
	v_mfma_f32_16x16x32_bf16 v[32:35], v[176:179], v[192:195], v[32:35]
	v_mfma_f32_16x16x32_bf16 v[20:23], v[168:171], v[210:213], v[20:23]
	v_mfma_f32_16x16x32_bf16 v[16:19], v[176:179], v[210:213], v[16:19]
	v_mfma_f32_16x16x32_bf16 v[4:7], v[168:171], v[218:221], v[4:7]
	v_mfma_f32_16x16x32_bf16 v[0:3], v[176:179], v[218:221], v[0:3]
	s_setprio 0
	s_barrier
	s_add_i32 s79, 0, 0x18000
	s_add_i32 s86, 0, 0x1c000
	v_add_u32_e32 v144, s79, v203
	v_add_u32_e32 v176, s86, v203
	ds_read_b128 v[132:135], v144
	ds_read_b128 v[136:139], v144 offset:1024
	ds_read_b128 v[140:143], v144 offset:2048
	ds_read_b128 v[144:147], v144 offset:3072
	ds_read_b128 v[148:151], v176
	ds_read_b128 v[168:171], v176 offset:1024
	ds_read_b128 v[172:175], v176 offset:2048
	ds_read_b128 v[176:179], v176 offset:3072
	s_add_u32 s8, s8, s50
	s_addc_u32 s9, s9, s51
	s_mov_b32 m0, s39
	v_lshl_add_u64 v[232:233], s[8:9], 0, v[154:155]
	ds_read_b128 v[180:183], v208 offset:32768
	ds_read_b128 v[184:187], v208 offset:33792
	ds_read_b128 v[188:191], v208 offset:34816
	ds_read_b128 v[192:195], v208 offset:35840
	ds_read_b128 v[196:199], v208 offset:36864
	ds_read_b128 v[210:213], v208 offset:37888
	ds_read_b128 v[214:217], v208 offset:38912
	ds_read_b128 v[218:221], v208 offset:39936
	global_load_lds_dwordx4 v[232:233], off
	v_lshl_add_u64 v[232:233], s[8:9], 0, v[158:159]
	s_mov_b32 m0, s92
	s_nop 0
	global_load_lds_dwordx4 v[232:233], off
	s_waitcnt vmcnt(8)
	s_waitcnt lgkmcnt(0)
	s_barrier
	s_setprio 1
	s_waitcnt lgkmcnt(0)
	v_mfma_f32_16x16x32_bf16 v[122:125], v[132:135], v[180:183], v[122:125]
	v_mfma_f32_16x16x32_bf16 v[126:129], v[140:143], v[180:183], v[126:129]
	v_mfma_f32_16x16x32_bf16 v[110:113], v[132:135], v[188:191], v[110:113]
	v_mfma_f32_16x16x32_bf16 v[106:109], v[140:143], v[188:191], v[106:109]
	v_mfma_f32_16x16x32_bf16 v[94:97], v[132:135], v[196:199], v[94:97]
	v_mfma_f32_16x16x32_bf16 v[90:93], v[140:143], v[196:199], v[90:93]
	v_mfma_f32_16x16x32_bf16 v[78:81], v[132:135], v[214:217], v[78:81]
	v_mfma_f32_16x16x32_bf16 v[74:77], v[140:143], v[214:217], v[74:77]
	v_mfma_f32_16x16x32_bf16 v[122:125], v[136:139], v[184:187], v[122:125]
	v_mfma_f32_16x16x32_bf16 v[126:129], v[144:147], v[184:187], v[126:129]
	v_mfma_f32_16x16x32_bf16 v[110:113], v[136:139], v[192:195], v[110:113]
	v_mfma_f32_16x16x32_bf16 v[106:109], v[144:147], v[192:195], v[106:109]
	v_mfma_f32_16x16x32_bf16 v[94:97], v[136:139], v[210:213], v[94:97]
	v_mfma_f32_16x16x32_bf16 v[90:93], v[144:147], v[210:213], v[90:93]
	v_mfma_f32_16x16x32_bf16 v[78:81], v[136:139], v[218:221], v[78:81]
	v_mfma_f32_16x16x32_bf16 v[74:77], v[144:147], v[218:221], v[74:77]
	s_setprio 0
	s_setprio 1
	v_mfma_f32_16x16x32_bf16 v[118:121], v[148:151], v[180:183], v[118:121]
	v_mfma_f32_16x16x32_bf16 v[114:117], v[172:175], v[180:183], v[114:117]
	v_mfma_f32_16x16x32_bf16 v[102:105], v[148:151], v[188:191], v[102:105]
	v_mfma_f32_16x16x32_bf16 v[98:101], v[172:175], v[188:191], v[98:101]
	v_mfma_f32_16x16x32_bf16 v[86:89], v[148:151], v[196:199], v[86:89]
	v_mfma_f32_16x16x32_bf16 v[82:85], v[172:175], v[196:199], v[82:85]
	v_mfma_f32_16x16x32_bf16 v[70:73], v[148:151], v[214:217], v[70:73]
	v_mfma_f32_16x16x32_bf16 v[66:69], v[172:175], v[214:217], v[66:69]
	v_mfma_f32_16x16x32_bf16 v[118:121], v[168:171], v[184:187], v[118:121]
	v_mfma_f32_16x16x32_bf16 v[114:117], v[176:179], v[184:187], v[114:117]
	v_mfma_f32_16x16x32_bf16 v[102:105], v[168:171], v[192:195], v[102:105]
	v_mfma_f32_16x16x32_bf16 v[98:101], v[176:179], v[192:195], v[98:101]
	v_mfma_f32_16x16x32_bf16 v[86:89], v[168:171], v[210:213], v[86:89]
	v_mfma_f32_16x16x32_bf16 v[82:85], v[176:179], v[210:213], v[82:85]
	v_mfma_f32_16x16x32_bf16 v[70:73], v[168:171], v[218:221], v[70:73]
	v_mfma_f32_16x16x32_bf16 v[66:69], v[176:179], v[218:221], v[66:69]
	s_setprio 0
	s_barrier
	s_add_i32 s8, s79, s19
	v_lshl_add_u64 v[222:223], v[222:223], 0, s[34:35]
	s_mov_b32 m0, s8
	ds_read_b128 v[180:183], v208 offset:49152
	ds_read_b128 v[184:187], v208 offset:50176
	ds_read_b128 v[188:191], v208 offset:51200
	ds_read_b128 v[192:195], v208 offset:52224
	ds_read_b128 v[196:199], v208 offset:53248
	ds_read_b128 v[210:213], v208 offset:54272
	ds_read_b128 v[214:217], v208 offset:55296
	ds_read_b128 v[218:221], v208 offset:56320
	global_load_lds_dwordx4 v[222:223], off
	v_lshl_add_u64 v[222:223], v[224:225], 0, s[34:35]
	s_add_i32 m0, s8, 0x2000
	s_add_i32 s8, s86, s19
	global_load_lds_dwordx4 v[222:223], off
	v_lshl_add_u64 v[222:223], v[226:227], 0, s[34:35]
	s_mov_b32 m0, s8
	v_lshl_add_u64 v[152:153], v[152:153], 0, s[34:35]
	global_load_lds_dwordx4 v[222:223], off
	s_add_i32 m0, s8, 0x2000
	s_nop 0
	global_load_lds_dwordx4 v[152:153], off
	v_lshl_add_u64 v[152:153], v[228:229], 0, s[34:35]
	s_mov_b32 m0, s96
	s_nop 0
	global_load_lds_dwordx4 v[152:153], off
	v_lshl_add_u64 v[152:153], v[230:231], 0, s[34:35]
	s_mov_b32 m0, s97
	s_nop 0
	global_load_lds_dwordx4 v[152:153], off
	s_waitcnt vmcnt(8)
	s_waitcnt lgkmcnt(0)
	s_barrier
	s_setprio 1
	s_waitcnt lgkmcnt(0)
	v_mfma_f32_16x16x32_bf16 v[62:65], v[132:135], v[180:183], v[62:65]
	v_mfma_f32_16x16x32_bf16 v[58:61], v[140:143], v[180:183], v[58:61]
	v_mfma_f32_16x16x32_bf16 v[44:47], v[132:135], v[188:191], v[44:47]
	v_mfma_f32_16x16x32_bf16 v[40:43], v[140:143], v[188:191], v[40:43]
	v_mfma_f32_16x16x32_bf16 v[28:31], v[132:135], v[196:199], v[28:31]
	v_mfma_f32_16x16x32_bf16 v[24:27], v[140:143], v[196:199], v[24:27]
	v_mfma_f32_16x16x32_bf16 v[12:15], v[132:135], v[214:217], v[12:15]
	v_mfma_f32_16x16x32_bf16 v[8:11], v[140:143], v[214:217], v[8:11]
	v_mfma_f32_16x16x32_bf16 v[62:65], v[136:139], v[184:187], v[62:65]
	v_mfma_f32_16x16x32_bf16 v[58:61], v[144:147], v[184:187], v[58:61]
	v_mfma_f32_16x16x32_bf16 v[44:47], v[136:139], v[192:195], v[44:47]
	v_mfma_f32_16x16x32_bf16 v[40:43], v[144:147], v[192:195], v[40:43]
	v_mfma_f32_16x16x32_bf16 v[28:31], v[136:139], v[210:213], v[28:31]
	v_mfma_f32_16x16x32_bf16 v[24:27], v[144:147], v[210:213], v[24:27]
	v_mfma_f32_16x16x32_bf16 v[12:15], v[136:139], v[218:221], v[12:15]
	v_mfma_f32_16x16x32_bf16 v[8:11], v[144:147], v[218:221], v[8:11]
	s_setprio 0
	s_setprio 1
	v_mfma_f32_16x16x32_bf16 v[54:57], v[148:151], v[180:183], v[54:57]
	v_mfma_f32_16x16x32_bf16 v[50:53], v[172:175], v[180:183], v[50:53]
	v_mfma_f32_16x16x32_bf16 v[36:39], v[148:151], v[188:191], v[36:39]
	v_mfma_f32_16x16x32_bf16 v[32:35], v[172:175], v[188:191], v[32:35]
	v_mfma_f32_16x16x32_bf16 v[20:23], v[148:151], v[196:199], v[20:23]
	v_mfma_f32_16x16x32_bf16 v[16:19], v[172:175], v[196:199], v[16:19]
	v_mfma_f32_16x16x32_bf16 v[4:7], v[148:151], v[214:217], v[4:7]
	v_mfma_f32_16x16x32_bf16 v[0:3], v[172:175], v[214:217], v[0:3]
	v_mfma_f32_16x16x32_bf16 v[54:57], v[168:171], v[184:187], v[54:57]
	v_mfma_f32_16x16x32_bf16 v[50:53], v[176:179], v[184:187], v[50:53]
	v_mfma_f32_16x16x32_bf16 v[36:39], v[168:171], v[192:195], v[36:39]
	v_mfma_f32_16x16x32_bf16 v[32:35], v[176:179], v[192:195], v[32:35]
	v_mfma_f32_16x16x32_bf16 v[20:23], v[168:171], v[210:213], v[20:23]
	v_mfma_f32_16x16x32_bf16 v[16:19], v[176:179], v[210:213], v[16:19]
	v_mfma_f32_16x16x32_bf16 v[4:7], v[168:171], v[218:221], v[4:7]
	v_mfma_f32_16x16x32_bf16 v[0:3], v[176:179], v[218:221], v[0:3]
	s_setprio 0
	s_barrier
	s_add_u32 s6, s6, 0x100
	s_addc_u32 s7, s7, 0
	v_lshl_add_u64 v[130:131], v[130:131], 0, s[36:37]
	s_cmp_ge_i32 s78, s30
	s_mov_b32 s8, s78

.Lmy_z_5:
	s_add_u32 s6, s6, 0x80
	s_addc_u32 s7, s7, 0
	s_add_u32 s30, s8, 0x100
	s_addc_u32 s40, s9, 0
	s_mov_b32 s8, 0
	s_add_i32 s41, s8, 2
	s_add_u32 s72, s6, 0x80
	s_addc_u32 s9, s7, 0
	s_add_i32 s79, 0, 0x10000
	s_cmp_eq_u32 s69, s8
	s_cselect_b32 s9, s59, s9
	s_cselect_b32 s8, s58, s72
	s_cselect_b32 s83, s65, s40
	s_cselect_b32 s82, s64, s30
	s_add_i32 s72, 0, 0x14000
	v_add_u32_e32 v142, s79, v171
	v_add_u32_e32 v170, s72, v171
	ds_read_b128 v[130:133], v142
	ds_read_b128 v[134:137], v142 offset:1024
	ds_read_b128 v[138:141], v142 offset:2048
	ds_read_b128 v[142:145], v142 offset:3072
	ds_read_b128 v[158:161], v170
	ds_read_b128 v[162:165], v170 offset:1024
	ds_read_b128 v[166:169], v170 offset:2048
	ds_read_b128 v[178:181], v170 offset:3072
	v_lshl_add_u64 v[172:173], s[6:7], 0, v[154:155]
	s_add_i32 m0, s63, 0xc000
	ds_read_b128 v[182:185], v177
	ds_read_b128 v[186:189], v177 offset:1024
	ds_read_b128 v[190:193], v177 offset:2048
	ds_read_b128 v[194:197], v177 offset:3072
	ds_read_b128 v[198:201], v177 offset:4096
	ds_read_b128 v[202:205], v177 offset:5120
	ds_read_b128 v[206:209], v177 offset:6144
	ds_read_b128 v[210:213], v177 offset:7168
	global_load_lds_dwordx4 v[172:173], off
	v_lshl_add_u64 v[172:173], s[6:7], 0, v[156:157]
	s_add_i32 m0, s63, 0xe000
	s_nop 0
	global_load_lds_dwordx4 v[172:173], off
	s_waitcnt vmcnt(8)
	s_waitcnt lgkmcnt(0)
	s_barrier
	s_setprio 1
	s_waitcnt lgkmcnt(0)
	v_mfma_f32_16x16x32_bf16 v[126:129], v[130:133], v[182:185], 0
	v_mfma_f32_16x16x32_bf16 v[118:121], v[138:141], v[182:185], 0
	v_mfma_f32_16x16x32_bf16 v[110:113], v[130:133], v[190:193], 0
	v_mfma_f32_16x16x32_bf16 v[102:105], v[138:141], v[190:193], 0
	v_mfma_f32_16x16x32_bf16 v[94:97], v[130:133], v[198:201], 0
	v_mfma_f32_16x16x32_bf16 v[86:89], v[138:141], v[198:201], 0
	v_mfma_f32_16x16x32_bf16 v[78:81], v[130:133], v[206:209], 0
	v_mfma_f32_16x16x32_bf16 v[70:73], v[138:141], v[206:209], 0
	v_mfma_f32_16x16x32_bf16 v[126:129], v[134:137], v[186:189], v[126:129]
	v_mfma_f32_16x16x32_bf16 v[118:121], v[142:145], v[186:189], v[118:121]
	v_mfma_f32_16x16x32_bf16 v[110:113], v[134:137], v[194:197], v[110:113]
	v_mfma_f32_16x16x32_bf16 v[102:105], v[142:145], v[194:197], v[102:105]
	v_mfma_f32_16x16x32_bf16 v[94:97], v[134:137], v[202:205], v[94:97]
	v_mfma_f32_16x16x32_bf16 v[86:89], v[142:145], v[202:205], v[86:89]
	v_mfma_f32_16x16x32_bf16 v[78:81], v[134:137], v[210:213], v[78:81]
	v_mfma_f32_16x16x32_bf16 v[70:73], v[142:145], v[210:213], v[70:73]
	s_setprio 0
	s_setprio 1
	v_mfma_f32_16x16x32_bf16 v[122:125], v[158:161], v[182:185], 0
	v_mfma_f32_16x16x32_bf16 v[114:117], v[166:169], v[182:185], 0
	v_mfma_f32_16x16x32_bf16 v[106:109], v[158:161], v[190:193], 0
	v_mfma_f32_16x16x32_bf16 v[98:101], v[166:169], v[190:193], 0
	v_mfma_f32_16x16x32_bf16 v[90:93], v[158:161], v[198:201], 0
	v_mfma_f32_16x16x32_bf16 v[82:85], v[166:169], v[198:201], 0
	v_mfma_f32_16x16x32_bf16 v[74:77], v[158:161], v[206:209], 0
	v_mfma_f32_16x16x32_bf16 v[66:69], v[166:169], v[206:209], 0
	v_mfma_f32_16x16x32_bf16 v[122:125], v[162:165], v[186:189], v[122:125]
	v_mfma_f32_16x16x32_bf16 v[114:117], v[178:181], v[186:189], v[114:117]
	v_mfma_f32_16x16x32_bf16 v[106:109], v[162:165], v[194:197], v[106:109]
	v_mfma_f32_16x16x32_bf16 v[98:101], v[178:181], v[194:197], v[98:101]
	v_mfma_f32_16x16x32_bf16 v[90:93], v[162:165], v[202:205], v[90:93]
	v_mfma_f32_16x16x32_bf16 v[82:85], v[178:181], v[202:205], v[82:85]
	v_mfma_f32_16x16x32_bf16 v[74:77], v[162:165], v[210:213], v[74:77]
	v_mfma_f32_16x16x32_bf16 v[66:69], v[178:181], v[210:213], v[66:69]
	s_setprio 0
	s_barrier
	s_add_i32 s79, s79, s62
	v_lshl_add_u64 v[172:173], s[82:83], 0, v[148:149]
	s_mov_b32 m0, s79
	ds_read_b128 v[182:185], v177 offset:16384
	ds_read_b128 v[186:189], v177 offset:17408
	ds_read_b128 v[190:193], v177 offset:18432
	ds_read_b128 v[194:197], v177 offset:19456
	ds_read_b128 v[198:201], v177 offset:20480
	ds_read_b128 v[202:205], v177 offset:21504
	ds_read_b128 v[206:209], v177 offset:22528
	ds_read_b128 v[210:213], v177 offset:23552
	global_load_lds_dwordx4 v[172:173], off
	s_add_i32 m0, s79, 0x2000
	v_lshl_add_u64 v[214:215], s[82:83], 0, v[152:153]
	s_add_u32 s82, s82, s44
	s_addc_u32 s83, s83, s45
	s_add_i32 s72, s72, s62
	global_load_lds_dwordx4 v[214:215], off
	v_lshl_add_u64 v[216:217], s[82:83], 0, v[148:149]
	s_mov_b32 m0, s72
	v_lshl_add_u64 v[218:219], s[82:83], 0, v[152:153]
	global_load_lds_dwordx4 v[216:217], off
	s_add_i32 m0, s72, 0x2000
	v_lshl_add_u64 v[220:221], s[8:9], 0, v[146:147]
	global_load_lds_dwordx4 v[218:219], off
	s_mov_b32 m0, s63
	v_lshl_add_u64 v[222:223], s[8:9], 0, v[150:151]
	global_load_lds_dwordx4 v[220:221], off
	s_mov_b32 m0, s66
	s_nop 0
	global_load_lds_dwordx4 v[222:223], off
	s_waitcnt vmcnt(8)
	s_waitcnt lgkmcnt(0)
	s_barrier
	s_setprio 1
	s_waitcnt lgkmcnt(0)
	v_mfma_f32_16x16x32_bf16 v[62:65], v[130:133], v[182:185], 0
	v_mfma_f32_16x16x32_bf16 v[54:57], v[138:141], v[182:185], 0
	v_mfma_f32_16x16x32_bf16 v[44:47], v[130:133], v[190:193], 0
	v_mfma_f32_16x16x32_bf16 v[36:39], v[138:141], v[190:193], 0
	v_mfma_f32_16x16x32_bf16 v[28:31], v[130:133], v[198:201], 0
	v_mfma_f32_16x16x32_bf16 v[20:23], v[138:141], v[198:201], 0
	v_mfma_f32_16x16x32_bf16 v[12:15], v[130:133], v[206:209], 0
	v_mfma_f32_16x16x32_bf16 v[4:7], v[138:141], v[206:209], 0
	v_mfma_f32_16x16x32_bf16 v[62:65], v[134:137], v[186:189], v[62:65]
	v_mfma_f32_16x16x32_bf16 v[54:57], v[142:145], v[186:189], v[54:57]
	v_mfma_f32_16x16x32_bf16 v[44:47], v[134:137], v[194:197], v[44:47]
	v_mfma_f32_16x16x32_bf16 v[36:39], v[142:145], v[194:197], v[36:39]
	v_mfma_f32_16x16x32_bf16 v[28:31], v[134:137], v[202:205], v[28:31]
	v_mfma_f32_16x16x32_bf16 v[20:23], v[142:145], v[202:205], v[20:23]
	v_mfma_f32_16x16x32_bf16 v[12:15], v[134:137], v[210:213], v[12:15]
	v_mfma_f32_16x16x32_bf16 v[4:7], v[142:145], v[210:213], v[4:7]
	s_setprio 0
	s_setprio 1
	v_mfma_f32_16x16x32_bf16 v[58:61], v[158:161], v[182:185], 0
	v_mfma_f32_16x16x32_bf16 v[50:53], v[166:169], v[182:185], 0
	v_mfma_f32_16x16x32_bf16 v[40:43], v[158:161], v[190:193], 0
	v_mfma_f32_16x16x32_bf16 v[32:35], v[166:169], v[190:193], 0
	v_mfma_f32_16x16x32_bf16 v[24:27], v[158:161], v[198:201], 0
	v_mfma_f32_16x16x32_bf16 v[16:19], v[166:169], v[198:201], 0
	v_mfma_f32_16x16x32_bf16 v[8:11], v[158:161], v[206:209], 0
	v_mfma_f32_16x16x32_bf16 v[0:3], v[166:169], v[206:209], 0
	v_mfma_f32_16x16x32_bf16 v[58:61], v[162:165], v[186:189], v[58:61]
	v_mfma_f32_16x16x32_bf16 v[50:53], v[178:181], v[186:189], v[50:53]
	v_mfma_f32_16x16x32_bf16 v[40:43], v[162:165], v[194:197], v[40:43]
	v_mfma_f32_16x16x32_bf16 v[32:35], v[178:181], v[194:197], v[32:35]
	v_mfma_f32_16x16x32_bf16 v[24:27], v[162:165], v[202:205], v[24:27]
	v_mfma_f32_16x16x32_bf16 v[16:19], v[178:181], v[202:205], v[16:19]
	v_mfma_f32_16x16x32_bf16 v[8:11], v[162:165], v[210:213], v[8:11]
	v_mfma_f32_16x16x32_bf16 v[0:3], v[178:181], v[210:213], v[0:3]
	s_setprio 0
	s_barrier
	s_add_i32 s72, 0, 0x18000
	s_add_i32 s79, 0, 0x1c000
	v_add_u32_e32 v142, s72, v171
	v_add_u32_e32 v170, s79, v171
	ds_read_b128 v[130:133], v142
	ds_read_b128 v[134:137], v142 offset:1024
	ds_read_b128 v[138:141], v142 offset:2048
	ds_read_b128 v[142:145], v142 offset:3072
	ds_read_b128 v[158:161], v170
	ds_read_b128 v[162:165], v170 offset:1024
	ds_read_b128 v[166:169], v170 offset:2048
	ds_read_b128 v[178:181], v170 offset:3072
	s_add_u32 s8, s8, s44
	s_addc_u32 s9, s9, s45
	s_mov_b32 m0, s67
	v_lshl_add_u64 v[224:225], s[8:9], 0, v[146:147]
	ds_read_b128 v[182:185], v177 offset:32768
	ds_read_b128 v[186:189], v177 offset:33792
	ds_read_b128 v[190:193], v177 offset:34816
	ds_read_b128 v[194:197], v177 offset:35840
	ds_read_b128 v[198:201], v177 offset:36864
	ds_read_b128 v[202:205], v177 offset:37888
	ds_read_b128 v[206:209], v177 offset:38912
	ds_read_b128 v[210:213], v177 offset:39936
	global_load_lds_dwordx4 v[224:225], off
	v_lshl_add_u64 v[224:225], s[8:9], 0, v[150:151]
	s_mov_b32 m0, s68
	s_nop 0
	global_load_lds_dwordx4 v[224:225], off
	s_waitcnt vmcnt(8)
	s_waitcnt lgkmcnt(0)
	s_barrier
	s_setprio 1
	s_waitcnt lgkmcnt(0)
	v_mfma_f32_16x16x32_bf16 v[126:129], v[130:133], v[182:185], v[126:129]
	v_mfma_f32_16x16x32_bf16 v[118:121], v[138:141], v[182:185], v[118:121]
	v_mfma_f32_16x16x32_bf16 v[110:113], v[130:133], v[190:193], v[110:113]
	v_mfma_f32_16x16x32_bf16 v[102:105], v[138:141], v[190:193], v[102:105]
	v_mfma_f32_16x16x32_bf16 v[94:97], v[130:133], v[198:201], v[94:97]
	v_mfma_f32_16x16x32_bf16 v[86:89], v[138:141], v[198:201], v[86:89]
	v_mfma_f32_16x16x32_bf16 v[78:81], v[130:133], v[206:209], v[78:81]
	v_mfma_f32_16x16x32_bf16 v[70:73], v[138:141], v[206:209], v[70:73]
	v_mfma_f32_16x16x32_bf16 v[126:129], v[134:137], v[186:189], v[126:129]
	v_mfma_f32_16x16x32_bf16 v[118:121], v[142:145], v[186:189], v[118:121]
	v_mfma_f32_16x16x32_bf16 v[110:113], v[134:137], v[194:197], v[110:113]
	v_mfma_f32_16x16x32_bf16 v[102:105], v[142:145], v[194:197], v[102:105]
	v_mfma_f32_16x16x32_bf16 v[94:97], v[134:137], v[202:205], v[94:97]
	v_mfma_f32_16x16x32_bf16 v[86:89], v[142:145], v[202:205], v[86:89]
	v_mfma_f32_16x16x32_bf16 v[78:81], v[134:137], v[210:213], v[78:81]
	v_mfma_f32_16x16x32_bf16 v[70:73], v[142:145], v[210:213], v[70:73]
	s_setprio 0
	s_setprio 1
	v_mfma_f32_16x16x32_bf16 v[122:125], v[158:161], v[182:185], v[122:125]
	v_mfma_f32_16x16x32_bf16 v[114:117], v[166:169], v[182:185], v[114:117]
	v_mfma_f32_16x16x32_bf16 v[106:109], v[158:161], v[190:193], v[106:109]
	v_mfma_f32_16x16x32_bf16 v[98:101], v[166:169], v[190:193], v[98:101]
	v_mfma_f32_16x16x32_bf16 v[90:93], v[158:161], v[198:201], v[90:93]
	v_mfma_f32_16x16x32_bf16 v[82:85], v[166:169], v[198:201], v[82:85]
	v_mfma_f32_16x16x32_bf16 v[74:77], v[158:161], v[206:209], v[74:77]
	v_mfma_f32_16x16x32_bf16 v[66:69], v[166:169], v[206:209], v[66:69]
	v_mfma_f32_16x16x32_bf16 v[122:125], v[162:165], v[186:189], v[122:125]
	v_mfma_f32_16x16x32_bf16 v[114:117], v[178:181], v[186:189], v[114:117]
	v_mfma_f32_16x16x32_bf16 v[106:109], v[162:165], v[194:197], v[106:109]
	v_mfma_f32_16x16x32_bf16 v[98:101], v[178:181], v[194:197], v[98:101]
	v_mfma_f32_16x16x32_bf16 v[90:93], v[162:165], v[202:205], v[90:93]
	v_mfma_f32_16x16x32_bf16 v[82:85], v[178:181], v[202:205], v[82:85]
	v_mfma_f32_16x16x32_bf16 v[74:77], v[162:165], v[210:213], v[74:77]
	v_mfma_f32_16x16x32_bf16 v[66:69], v[178:181], v[210:213], v[66:69]
	s_setprio 0
	s_barrier
	s_add_i32 s8, s72, s62
	v_lshl_add_u64 v[172:173], v[172:173], 0, s[34:35]
	s_mov_b32 m0, s8
	ds_read_b128 v[182:185], v177 offset:49152
	ds_read_b128 v[186:189], v177 offset:50176
	ds_read_b128 v[190:193], v177 offset:51200
	ds_read_b128 v[194:197], v177 offset:52224
	ds_read_b128 v[198:201], v177 offset:53248
	ds_read_b128 v[202:205], v177 offset:54272
	ds_read_b128 v[206:209], v177 offset:55296
	ds_read_b128 v[210:213], v177 offset:56320
	global_load_lds_dwordx4 v[172:173], off
	v_lshl_add_u64 v[172:173], v[214:215], 0, s[34:35]
	s_add_i32 m0, s8, 0x2000
	s_add_i32 s8, s79, s62
	global_load_lds_dwordx4 v[172:173], off
	v_lshl_add_u64 v[172:173], v[216:217], 0, s[34:35]
	s_mov_b32 m0, s8
	s_nop 0
	global_load_lds_dwordx4 v[172:173], off
	v_lshl_add_u64 v[172:173], v[218:219], 0, s[34:35]
	s_add_i32 m0, s8, 0x2000
	s_nop 0
	global_load_lds_dwordx4 v[172:173], off
	v_lshl_add_u64 v[172:173], v[220:221], 0, s[34:35]
	s_mov_b32 m0, s12
	s_nop 0
	global_load_lds_dwordx4 v[172:173], off
	v_lshl_add_u64 v[172:173], v[222:223], 0, s[34:35]
	s_mov_b32 m0, s19
	s_nop 0
	global_load_lds_dwordx4 v[172:173], off
	s_waitcnt vmcnt(8)
	s_waitcnt lgkmcnt(0)
	s_barrier
	s_setprio 1
	s_waitcnt lgkmcnt(0)
	v_mfma_f32_16x16x32_bf16 v[62:65], v[130:133], v[182:185], v[62:65]
	v_mfma_f32_16x16x32_bf16 v[54:57], v[138:141], v[182:185], v[54:57]
	v_mfma_f32_16x16x32_bf16 v[44:47], v[130:133], v[190:193], v[44:47]
	v_mfma_f32_16x16x32_bf16 v[36:39], v[138:141], v[190:193], v[36:39]
	v_mfma_f32_16x16x32_bf16 v[28:31], v[130:133], v[198:201], v[28:31]
	v_mfma_f32_16x16x32_bf16 v[20:23], v[138:141], v[198:201], v[20:23]
	v_mfma_f32_16x16x32_bf16 v[12:15], v[130:133], v[206:209], v[12:15]
	v_mfma_f32_16x16x32_bf16 v[4:7], v[138:141], v[206:209], v[4:7]
	v_mfma_f32_16x16x32_bf16 v[62:65], v[134:137], v[186:189], v[62:65]
	v_mfma_f32_16x16x32_bf16 v[54:57], v[142:145], v[186:189], v[54:57]
	v_mfma_f32_16x16x32_bf16 v[44:47], v[134:137], v[194:197], v[44:47]
	v_mfma_f32_16x16x32_bf16 v[36:39], v[142:145], v[194:197], v[36:39]
	v_mfma_f32_16x16x32_bf16 v[28:31], v[134:137], v[202:205], v[28:31]
	v_mfma_f32_16x16x32_bf16 v[20:23], v[142:145], v[202:205], v[20:23]
	v_mfma_f32_16x16x32_bf16 v[12:15], v[134:137], v[210:213], v[12:15]
	v_mfma_f32_16x16x32_bf16 v[4:7], v[142:145], v[210:213], v[4:7]
	s_setprio 0
	s_setprio 1
	v_mfma_f32_16x16x32_bf16 v[58:61], v[158:161], v[182:185], v[58:61]
	v_mfma_f32_16x16x32_bf16 v[50:53], v[166:169], v[182:185], v[50:53]
	v_mfma_f32_16x16x32_bf16 v[40:43], v[158:161], v[190:193], v[40:43]
	v_mfma_f32_16x16x32_bf16 v[32:35], v[166:169], v[190:193], v[32:35]
	v_mfma_f32_16x16x32_bf16 v[24:27], v[158:161], v[198:201], v[24:27]
	v_mfma_f32_16x16x32_bf16 v[16:19], v[166:169], v[198:201], v[16:19]
	v_mfma_f32_16x16x32_bf16 v[8:11], v[158:161], v[206:209], v[8:11]
	v_mfma_f32_16x16x32_bf16 v[0:3], v[166:169], v[206:209], v[0:3]
	v_mfma_f32_16x16x32_bf16 v[58:61], v[162:165], v[186:189], v[58:61]
	v_mfma_f32_16x16x32_bf16 v[50:53], v[178:181], v[186:189], v[50:53]
	v_mfma_f32_16x16x32_bf16 v[40:43], v[162:165], v[194:197], v[40:43]
	v_mfma_f32_16x16x32_bf16 v[32:35], v[178:181], v[194:197], v[32:35]
	v_mfma_f32_16x16x32_bf16 v[24:27], v[162:165], v[202:205], v[24:27]
	v_mfma_f32_16x16x32_bf16 v[16:19], v[178:181], v[202:205], v[16:19]
	v_mfma_f32_16x16x32_bf16 v[8:11], v[162:165], v[210:213], v[8:11]
	v_mfma_f32_16x16x32_bf16 v[0:3], v[178:181], v[210:213], v[0:3]
	s_setprio 0
	s_barrier
	s_add_u32 s6, s6, 0x100
	s_addc_u32 s7, s7, 0
	s_add_u32 s30, s30, 0x100
	s_addc_u32 s40, s40, 0
	s_cmp_ge_i32 s41, s25
	s_mov_b32 s8, s41

.Lmy_z_6:
	s_add_u32 s6, s6, 0x80
	s_addc_u32 s7, s7, 0
	s_add_u32 s29, s8, 0x100
	s_addc_u32 s57, s9, 0
	s_mov_b32 s8, 0
	s_add_i32 s72, s8, 2
	s_add_u32 s82, s6, 0x80
	s_addc_u32 s9, s7, 0
	s_add_i32 s84, 0, 0x10000
	s_cmp_eq_u32 s89, s8
	s_cselect_b32 s9, s45, s9
	s_cselect_b32 s8, s44, s82
	s_cselect_b32 s83, s71, s57
	s_cselect_b32 s82, s70, s29
	s_add_i32 s85, 0, 0x14000
	v_add_u32_e32 v142, s84, v179
	v_add_u32_e32 v170, s85, v179
	ds_read_b128 v[130:133], v142
	ds_read_b128 v[134:137], v142 offset:1024
	ds_read_b128 v[138:141], v142 offset:2048
	ds_read_b128 v[142:145], v142 offset:3072
	ds_read_b128 v[146:149], v170
	ds_read_b128 v[150:153], v170 offset:1024
	ds_read_b128 v[154:157], v170 offset:2048
	ds_read_b128 v[170:173], v170 offset:3072
	v_lshl_add_u64 v[218:219], s[6:7], 0, v[166:167]
	s_add_i32 m0, s61, 0xc000
	ds_read_b128 v[174:177], v186
	ds_read_b128 v[190:193], v186 offset:1024
	ds_read_b128 v[194:197], v186 offset:2048
	ds_read_b128 v[198:201], v186 offset:3072
	ds_read_b128 v[202:205], v186 offset:4096
	ds_read_b128 v[206:209], v186 offset:5120
	ds_read_b128 v[210:213], v186 offset:6144
	ds_read_b128 v[214:217], v186 offset:7168
	global_load_lds_dwordx4 v[218:219], off
	v_lshl_add_u64 v[218:219], s[6:7], 0, v[168:169]
	s_add_i32 m0, s61, 0xe000
	s_nop 0
	global_load_lds_dwordx4 v[218:219], off
	s_waitcnt vmcnt(8)
	s_waitcnt lgkmcnt(0)
	s_barrier
	s_setprio 1
	s_waitcnt lgkmcnt(0)
	v_mfma_f32_16x16x32_bf16 v[122:125], v[130:133], v[174:177], 0
	v_mfma_f32_16x16x32_bf16 v[126:129], v[138:141], v[174:177], 0
	v_mfma_f32_16x16x32_bf16 v[110:113], v[130:133], v[194:197], 0
	v_mfma_f32_16x16x32_bf16 v[106:109], v[138:141], v[194:197], 0
	v_mfma_f32_16x16x32_bf16 v[94:97], v[130:133], v[202:205], 0
	v_mfma_f32_16x16x32_bf16 v[90:93], v[138:141], v[202:205], 0
	v_mfma_f32_16x16x32_bf16 v[78:81], v[130:133], v[210:213], 0
	v_mfma_f32_16x16x32_bf16 v[74:77], v[138:141], v[210:213], 0
	v_mfma_f32_16x16x32_bf16 v[122:125], v[134:137], v[190:193], v[122:125]
	v_mfma_f32_16x16x32_bf16 v[126:129], v[142:145], v[190:193], v[126:129]
	v_mfma_f32_16x16x32_bf16 v[110:113], v[134:137], v[198:201], v[110:113]
	v_mfma_f32_16x16x32_bf16 v[106:109], v[142:145], v[198:201], v[106:109]
	v_mfma_f32_16x16x32_bf16 v[94:97], v[134:137], v[206:209], v[94:97]
	v_mfma_f32_16x16x32_bf16 v[90:93], v[142:145], v[206:209], v[90:93]
	v_mfma_f32_16x16x32_bf16 v[78:81], v[134:137], v[214:217], v[78:81]
	v_mfma_f32_16x16x32_bf16 v[74:77], v[142:145], v[214:217], v[74:77]
	s_setprio 0
	s_setprio 1
	v_mfma_f32_16x16x32_bf16 v[118:121], v[146:149], v[174:177], 0
	v_mfma_f32_16x16x32_bf16 v[114:117], v[154:157], v[174:177], 0
	v_mfma_f32_16x16x32_bf16 v[102:105], v[146:149], v[194:197], 0
	v_mfma_f32_16x16x32_bf16 v[98:101], v[154:157], v[194:197], 0
	v_mfma_f32_16x16x32_bf16 v[86:89], v[146:149], v[202:205], 0
	v_mfma_f32_16x16x32_bf16 v[82:85], v[154:157], v[202:205], 0
	v_mfma_f32_16x16x32_bf16 v[70:73], v[146:149], v[210:213], 0
	v_mfma_f32_16x16x32_bf16 v[66:69], v[154:157], v[210:213], 0
	v_mfma_f32_16x16x32_bf16 v[118:121], v[150:153], v[190:193], v[118:121]
	v_mfma_f32_16x16x32_bf16 v[114:117], v[170:173], v[190:193], v[114:117]
	v_mfma_f32_16x16x32_bf16 v[102:105], v[150:153], v[198:201], v[102:105]
	v_mfma_f32_16x16x32_bf16 v[98:101], v[170:173], v[198:201], v[98:101]
	v_mfma_f32_16x16x32_bf16 v[86:89], v[150:153], v[206:209], v[86:89]
	v_mfma_f32_16x16x32_bf16 v[82:85], v[170:173], v[206:209], v[82:85]
	v_mfma_f32_16x16x32_bf16 v[70:73], v[150:153], v[214:217], v[70:73]
	v_mfma_f32_16x16x32_bf16 v[66:69], v[170:173], v[214:217], v[66:69]
	s_setprio 0
	s_barrier
	s_add_i32 s84, s84, s60
	v_lshl_add_u64 v[218:219], s[82:83], 0, v[160:161]
	s_mov_b32 m0, s84
	ds_read_b128 v[174:177], v186 offset:16384
	ds_read_b128 v[190:193], v186 offset:17408
	ds_read_b128 v[194:197], v186 offset:18432
	ds_read_b128 v[198:201], v186 offset:19456
	ds_read_b128 v[202:205], v186 offset:20480
	ds_read_b128 v[206:209], v186 offset:21504
	ds_read_b128 v[210:213], v186 offset:22528
	ds_read_b128 v[214:217], v186 offset:23552
	global_load_lds_dwordx4 v[218:219], off
	s_add_i32 m0, s84, 0x2000
	v_lshl_add_u64 v[220:221], s[82:83], 0, v[164:165]
	s_add_u32 s82, s82, s52
	s_addc_u32 s83, s83, s53
	s_add_i32 s84, s85, s60
	global_load_lds_dwordx4 v[220:221], off
	v_lshl_add_u64 v[222:223], s[82:83], 0, v[160:161]
	s_mov_b32 m0, s84
	v_lshl_add_u64 v[224:225], s[82:83], 0, v[164:165]
	global_load_lds_dwordx4 v[222:223], off
	s_add_i32 m0, s84, 0x2000
	v_lshl_add_u64 v[226:227], s[8:9], 0, v[158:159]
	global_load_lds_dwordx4 v[224:225], off
	s_mov_b32 m0, s61
	v_lshl_add_u64 v[228:229], s[8:9], 0, v[162:163]
	global_load_lds_dwordx4 v[226:227], off
	s_mov_b32 m0, s12
	s_nop 0
	global_load_lds_dwordx4 v[228:229], off
	s_waitcnt vmcnt(8)
	s_waitcnt lgkmcnt(0)
	s_barrier
	s_setprio 1
	s_waitcnt lgkmcnt(0)
	v_mfma_f32_16x16x32_bf16 v[62:65], v[130:133], v[174:177], 0
	v_mfma_f32_16x16x32_bf16 v[58:61], v[138:141], v[174:177], 0
	v_mfma_f32_16x16x32_bf16 v[44:47], v[130:133], v[194:197], 0
	v_mfma_f32_16x16x32_bf16 v[40:43], v[138:141], v[194:197], 0
	v_mfma_f32_16x16x32_bf16 v[28:31], v[130:133], v[202:205], 0
	v_mfma_f32_16x16x32_bf16 v[24:27], v[138:141], v[202:205], 0
	v_mfma_f32_16x16x32_bf16 v[12:15], v[130:133], v[210:213], 0
	v_mfma_f32_16x16x32_bf16 v[8:11], v[138:141], v[210:213], 0
	v_mfma_f32_16x16x32_bf16 v[62:65], v[134:137], v[190:193], v[62:65]
	v_mfma_f32_16x16x32_bf16 v[58:61], v[142:145], v[190:193], v[58:61]
	v_mfma_f32_16x16x32_bf16 v[44:47], v[134:137], v[198:201], v[44:47]
	v_mfma_f32_16x16x32_bf16 v[40:43], v[142:145], v[198:201], v[40:43]
	v_mfma_f32_16x16x32_bf16 v[28:31], v[134:137], v[206:209], v[28:31]
	v_mfma_f32_16x16x32_bf16 v[24:27], v[142:145], v[206:209], v[24:27]
	v_mfma_f32_16x16x32_bf16 v[12:15], v[134:137], v[214:217], v[12:15]
	v_mfma_f32_16x16x32_bf16 v[8:11], v[142:145], v[214:217], v[8:11]
	s_setprio 0
	s_setprio 1
	v_mfma_f32_16x16x32_bf16 v[54:57], v[146:149], v[174:177], 0
	v_mfma_f32_16x16x32_bf16 v[50:53], v[154:157], v[174:177], 0
	v_mfma_f32_16x16x32_bf16 v[36:39], v[146:149], v[194:197], 0
	v_mfma_f32_16x16x32_bf16 v[32:35], v[154:157], v[194:197], 0
	v_mfma_f32_16x16x32_bf16 v[20:23], v[146:149], v[202:205], 0
	v_mfma_f32_16x16x32_bf16 v[16:19], v[154:157], v[202:205], 0
	v_mfma_f32_16x16x32_bf16 v[4:7], v[146:149], v[210:213], 0
	v_mfma_f32_16x16x32_bf16 v[0:3], v[154:157], v[210:213], 0
	v_mfma_f32_16x16x32_bf16 v[54:57], v[150:153], v[190:193], v[54:57]
	v_mfma_f32_16x16x32_bf16 v[50:53], v[170:173], v[190:193], v[50:53]
	v_mfma_f32_16x16x32_bf16 v[36:39], v[150:153], v[198:201], v[36:39]
	v_mfma_f32_16x16x32_bf16 v[32:35], v[170:173], v[198:201], v[32:35]
	v_mfma_f32_16x16x32_bf16 v[20:23], v[150:153], v[206:209], v[20:23]
	v_mfma_f32_16x16x32_bf16 v[16:19], v[170:173], v[206:209], v[16:19]
	v_mfma_f32_16x16x32_bf16 v[4:7], v[150:153], v[214:217], v[4:7]
	v_mfma_f32_16x16x32_bf16 v[0:3], v[170:173], v[214:217], v[0:3]
	s_setprio 0
	s_barrier
	s_add_i32 s82, 0, 0x18000
	s_add_i32 s83, 0, 0x1c000
	v_add_u32_e32 v142, s82, v179
	v_add_u32_e32 v170, s83, v179
	ds_read_b128 v[130:133], v142
	ds_read_b128 v[134:137], v142 offset:1024
	ds_read_b128 v[138:141], v142 offset:2048
	ds_read_b128 v[142:145], v142 offset:3072
	ds_read_b128 v[146:149], v170
	ds_read_b128 v[150:153], v170 offset:1024
	ds_read_b128 v[154:157], v170 offset:2048
	ds_read_b128 v[170:173], v170 offset:3072
	s_add_u32 s8, s8, s52
	s_addc_u32 s9, s9, s53
	s_mov_b32 m0, s19
	v_lshl_add_u64 v[230:231], s[8:9], 0, v[158:159]
	ds_read_b128 v[174:177], v186 offset:32768
	ds_read_b128 v[190:193], v186 offset:33792
	ds_read_b128 v[194:197], v186 offset:34816
	ds_read_b128 v[198:201], v186 offset:35840
	ds_read_b128 v[202:205], v186 offset:36864
	ds_read_b128 v[206:209], v186 offset:37888
	ds_read_b128 v[210:213], v186 offset:38912
	ds_read_b128 v[214:217], v186 offset:39936
	global_load_lds_dwordx4 v[230:231], off
	v_lshl_add_u64 v[230:231], s[8:9], 0, v[162:163]
	s_mov_b32 m0, s25
	s_nop 0
	global_load_lds_dwordx4 v[230:231], off
	s_waitcnt vmcnt(8)
	s_waitcnt lgkmcnt(0)
	s_barrier
	s_setprio 1
	s_waitcnt lgkmcnt(0)
	v_mfma_f32_16x16x32_bf16 v[122:125], v[130:133], v[174:177], v[122:125]
	v_mfma_f32_16x16x32_bf16 v[126:129], v[138:141], v[174:177], v[126:129]
	v_mfma_f32_16x16x32_bf16 v[110:113], v[130:133], v[194:197], v[110:113]
	v_mfma_f32_16x16x32_bf16 v[106:109], v[138:141], v[194:197], v[106:109]
	v_mfma_f32_16x16x32_bf16 v[94:97], v[130:133], v[202:205], v[94:97]
	v_mfma_f32_16x16x32_bf16 v[90:93], v[138:141], v[202:205], v[90:93]
	v_mfma_f32_16x16x32_bf16 v[78:81], v[130:133], v[210:213], v[78:81]
	v_mfma_f32_16x16x32_bf16 v[74:77], v[138:141], v[210:213], v[74:77]
	v_mfma_f32_16x16x32_bf16 v[122:125], v[134:137], v[190:193], v[122:125]
	v_mfma_f32_16x16x32_bf16 v[126:129], v[142:145], v[190:193], v[126:129]
	v_mfma_f32_16x16x32_bf16 v[110:113], v[134:137], v[198:201], v[110:113]
	v_mfma_f32_16x16x32_bf16 v[106:109], v[142:145], v[198:201], v[106:109]
	v_mfma_f32_16x16x32_bf16 v[94:97], v[134:137], v[206:209], v[94:97]
	v_mfma_f32_16x16x32_bf16 v[90:93], v[142:145], v[206:209], v[90:93]
	v_mfma_f32_16x16x32_bf16 v[78:81], v[134:137], v[214:217], v[78:81]
	v_mfma_f32_16x16x32_bf16 v[74:77], v[142:145], v[214:217], v[74:77]
	s_setprio 0
	s_setprio 1
	v_mfma_f32_16x16x32_bf16 v[118:121], v[146:149], v[174:177], v[118:121]
	v_mfma_f32_16x16x32_bf16 v[114:117], v[154:157], v[174:177], v[114:117]
	v_mfma_f32_16x16x32_bf16 v[102:105], v[146:149], v[194:197], v[102:105]
	v_mfma_f32_16x16x32_bf16 v[98:101], v[154:157], v[194:197], v[98:101]
	v_mfma_f32_16x16x32_bf16 v[86:89], v[146:149], v[202:205], v[86:89]
	v_mfma_f32_16x16x32_bf16 v[82:85], v[154:157], v[202:205], v[82:85]
	v_mfma_f32_16x16x32_bf16 v[70:73], v[146:149], v[210:213], v[70:73]
	v_mfma_f32_16x16x32_bf16 v[66:69], v[154:157], v[210:213], v[66:69]
	v_mfma_f32_16x16x32_bf16 v[118:121], v[150:153], v[190:193], v[118:121]
	v_mfma_f32_16x16x32_bf16 v[114:117], v[170:173], v[190:193], v[114:117]
	v_mfma_f32_16x16x32_bf16 v[102:105], v[150:153], v[198:201], v[102:105]
	v_mfma_f32_16x16x32_bf16 v[98:101], v[170:173], v[198:201], v[98:101]
	v_mfma_f32_16x16x32_bf16 v[86:89], v[150:153], v[206:209], v[86:89]
	v_mfma_f32_16x16x32_bf16 v[82:85], v[170:173], v[206:209], v[82:85]
	v_mfma_f32_16x16x32_bf16 v[70:73], v[150:153], v[214:217], v[70:73]
	v_mfma_f32_16x16x32_bf16 v[66:69], v[170:173], v[214:217], v[66:69]
	s_setprio 0
	s_barrier
	s_add_i32 s8, s82, s60
	v_lshl_add_u64 v[218:219], v[218:219], 0, s[34:35]
	s_mov_b32 m0, s8
	ds_read_b128 v[174:177], v186 offset:49152
	ds_read_b128 v[190:193], v186 offset:50176
	ds_read_b128 v[194:197], v186 offset:51200
	ds_read_b128 v[198:201], v186 offset:52224
	ds_read_b128 v[202:205], v186 offset:53248
	ds_read_b128 v[206:209], v186 offset:54272
	ds_read_b128 v[210:213], v186 offset:55296
	ds_read_b128 v[214:217], v186 offset:56320
	global_load_lds_dwordx4 v[218:219], off
	v_lshl_add_u64 v[218:219], v[220:221], 0, s[34:35]
	s_add_i32 m0, s8, 0x2000
	s_add_i32 s8, s83, s60
	global_load_lds_dwordx4 v[218:219], off
	v_lshl_add_u64 v[218:219], v[222:223], 0, s[34:35]
	s_mov_b32 m0, s8
	s_nop 0
	global_load_lds_dwordx4 v[218:219], off
	v_lshl_add_u64 v[218:219], v[224:225], 0, s[34:35]
	s_add_i32 m0, s8, 0x2000
	s_nop 0
	global_load_lds_dwordx4 v[218:219], off
	v_lshl_add_u64 v[218:219], v[226:227], 0, s[34:35]
	s_mov_b32 m0, s79
	s_nop 0
	global_load_lds_dwordx4 v[218:219], off
	v_lshl_add_u64 v[218:219], v[228:229], 0, s[34:35]
	s_mov_b32 m0, s88
	s_nop 0
	global_load_lds_dwordx4 v[218:219], off
	s_waitcnt vmcnt(8)
	s_waitcnt lgkmcnt(0)
	s_barrier
	s_setprio 1
	s_waitcnt lgkmcnt(0)
	v_mfma_f32_16x16x32_bf16 v[62:65], v[130:133], v[174:177], v[62:65]
	v_mfma_f32_16x16x32_bf16 v[58:61], v[138:141], v[174:177], v[58:61]
	v_mfma_f32_16x16x32_bf16 v[44:47], v[130:133], v[194:197], v[44:47]
	v_mfma_f32_16x16x32_bf16 v[40:43], v[138:141], v[194:197], v[40:43]
	v_mfma_f32_16x16x32_bf16 v[28:31], v[130:133], v[202:205], v[28:31]
	v_mfma_f32_16x16x32_bf16 v[24:27], v[138:141], v[202:205], v[24:27]
	v_mfma_f32_16x16x32_bf16 v[12:15], v[130:133], v[210:213], v[12:15]
	v_mfma_f32_16x16x32_bf16 v[8:11], v[138:141], v[210:213], v[8:11]
	v_mfma_f32_16x16x32_bf16 v[62:65], v[134:137], v[190:193], v[62:65]
	v_mfma_f32_16x16x32_bf16 v[58:61], v[142:145], v[190:193], v[58:61]
	v_mfma_f32_16x16x32_bf16 v[44:47], v[134:137], v[198:201], v[44:47]
	v_mfma_f32_16x16x32_bf16 v[40:43], v[142:145], v[198:201], v[40:43]
	v_mfma_f32_16x16x32_bf16 v[28:31], v[134:137], v[206:209], v[28:31]
	v_mfma_f32_16x16x32_bf16 v[24:27], v[142:145], v[206:209], v[24:27]
	v_mfma_f32_16x16x32_bf16 v[12:15], v[134:137], v[214:217], v[12:15]
	v_mfma_f32_16x16x32_bf16 v[8:11], v[142:145], v[214:217], v[8:11]
	s_setprio 0
	s_setprio 1
	v_mfma_f32_16x16x32_bf16 v[54:57], v[146:149], v[174:177], v[54:57]
	v_mfma_f32_16x16x32_bf16 v[50:53], v[154:157], v[174:177], v[50:53]
	v_mfma_f32_16x16x32_bf16 v[36:39], v[146:149], v[194:197], v[36:39]
	v_mfma_f32_16x16x32_bf16 v[32:35], v[154:157], v[194:197], v[32:35]
	v_mfma_f32_16x16x32_bf16 v[20:23], v[146:149], v[202:205], v[20:23]
	v_mfma_f32_16x16x32_bf16 v[16:19], v[154:157], v[202:205], v[16:19]
	v_mfma_f32_16x16x32_bf16 v[4:7], v[146:149], v[210:213], v[4:7]
	v_mfma_f32_16x16x32_bf16 v[0:3], v[154:157], v[210:213], v[0:3]
	v_mfma_f32_16x16x32_bf16 v[54:57], v[150:153], v[190:193], v[54:57]
	v_mfma_f32_16x16x32_bf16 v[50:53], v[170:173], v[190:193], v[50:53]
	v_mfma_f32_16x16x32_bf16 v[36:39], v[150:153], v[198:201], v[36:39]
	v_mfma_f32_16x16x32_bf16 v[32:35], v[170:173], v[198:201], v[32:35]
	v_mfma_f32_16x16x32_bf16 v[20:23], v[150:153], v[206:209], v[20:23]
	v_mfma_f32_16x16x32_bf16 v[16:19], v[170:173], v[206:209], v[16:19]
	v_mfma_f32_16x16x32_bf16 v[4:7], v[150:153], v[214:217], v[4:7]
	v_mfma_f32_16x16x32_bf16 v[0:3], v[170:173], v[214:217], v[0:3]
	s_setprio 0
	s_barrier
	s_add_u32 s6, s6, 0x100
	s_addc_u32 s7, s7, 0
	s_add_u32 s29, s29, 0x100
	s_addc_u32 s57, s57, 0
	s_cmp_ge_i32 s72, s62
	s_mov_b32 s8, s72

.Lmy_z_7:
	s_add_u32 s6, s6, 0x80
	s_addc_u32 s7, s7, 0
	s_add_u32 s83, s8, 0x100
	s_addc_u32 s84, s9, 0
	s_mov_b32 s8, 0
	s_add_i32 s85, s8, 2
	s_add_u32 s86, s6, 0x80
	s_addc_u32 s9, s7, 0
	s_add_i32 s90, 0, 0x10000
	s_cmp_eq_u32 s72, s8
	s_cselect_b32 s9, s45, s9
	s_cselect_b32 s8, s44, s86
	s_cselect_b32 s89, s69, s84
	s_cselect_b32 s88, s68, s83
	s_add_i32 s86, 0, 0x14000
	v_add_u32_e32 v142, s90, v189
	v_add_u32_e32 v158, s86, v189
	ds_read_b128 v[130:133], v142
	ds_read_b128 v[134:137], v142 offset:1024
	ds_read_b128 v[138:141], v142 offset:2048
	ds_read_b128 v[142:145], v142 offset:3072
	ds_read_b128 v[146:149], v158
	ds_read_b128 v[150:153], v158 offset:1024
	ds_read_b128 v[154:157], v158 offset:2048
	ds_read_b128 v[158:161], v158 offset:3072
	v_lshl_add_u64 v[220:221], s[6:7], 0, v[172:173]
	s_add_i32 m0, s25, 0xc000
	ds_read_b128 v[176:179], v196
	ds_read_b128 v[180:183], v196 offset:1024
	ds_read_b128 v[184:187], v196 offset:2048
	ds_read_b128 v[200:203], v196 offset:3072
	ds_read_b128 v[204:207], v196 offset:4096
	ds_read_b128 v[208:211], v196 offset:5120
	ds_read_b128 v[212:215], v196 offset:6144
	ds_read_b128 v[216:219], v196 offset:7168
	global_load_lds_dwordx4 v[220:221], off
	v_lshl_add_u64 v[220:221], s[6:7], 0, v[174:175]
	s_add_i32 m0, s25, 0xe000
	s_nop 0
	global_load_lds_dwordx4 v[220:221], off
	s_waitcnt vmcnt(8)
	s_waitcnt lgkmcnt(0)
	s_barrier
	s_setprio 1
	s_waitcnt lgkmcnt(0)
	v_mfma_f32_16x16x32_bf16 v[122:125], v[130:133], v[176:179], 0
	v_mfma_f32_16x16x32_bf16 v[126:129], v[138:141], v[176:179], 0
	v_mfma_f32_16x16x32_bf16 v[110:113], v[130:133], v[184:187], 0
	v_mfma_f32_16x16x32_bf16 v[106:109], v[138:141], v[184:187], 0
	v_mfma_f32_16x16x32_bf16 v[94:97], v[130:133], v[204:207], 0
	v_mfma_f32_16x16x32_bf16 v[90:93], v[138:141], v[204:207], 0
	v_mfma_f32_16x16x32_bf16 v[78:81], v[130:133], v[212:215], 0
	v_mfma_f32_16x16x32_bf16 v[74:77], v[138:141], v[212:215], 0
	v_mfma_f32_16x16x32_bf16 v[122:125], v[134:137], v[180:183], v[122:125]
	v_mfma_f32_16x16x32_bf16 v[126:129], v[142:145], v[180:183], v[126:129]
	v_mfma_f32_16x16x32_bf16 v[110:113], v[134:137], v[200:203], v[110:113]
	v_mfma_f32_16x16x32_bf16 v[106:109], v[142:145], v[200:203], v[106:109]
	v_mfma_f32_16x16x32_bf16 v[94:97], v[134:137], v[208:211], v[94:97]
	v_mfma_f32_16x16x32_bf16 v[90:93], v[142:145], v[208:211], v[90:93]
	v_mfma_f32_16x16x32_bf16 v[78:81], v[134:137], v[216:219], v[78:81]
	v_mfma_f32_16x16x32_bf16 v[74:77], v[142:145], v[216:219], v[74:77]
	s_setprio 0
	s_setprio 1
	v_mfma_f32_16x16x32_bf16 v[118:121], v[146:149], v[176:179], 0
	v_mfma_f32_16x16x32_bf16 v[114:117], v[154:157], v[176:179], 0
	v_mfma_f32_16x16x32_bf16 v[102:105], v[146:149], v[184:187], 0
	v_mfma_f32_16x16x32_bf16 v[98:101], v[154:157], v[184:187], 0
	v_mfma_f32_16x16x32_bf16 v[86:89], v[146:149], v[204:207], 0
	v_mfma_f32_16x16x32_bf16 v[82:85], v[154:157], v[204:207], 0
	v_mfma_f32_16x16x32_bf16 v[70:73], v[146:149], v[212:215], 0
	v_mfma_f32_16x16x32_bf16 v[66:69], v[154:157], v[212:215], 0
	v_mfma_f32_16x16x32_bf16 v[118:121], v[150:153], v[180:183], v[118:121]
	v_mfma_f32_16x16x32_bf16 v[114:117], v[158:161], v[180:183], v[114:117]
	v_mfma_f32_16x16x32_bf16 v[102:105], v[150:153], v[200:203], v[102:105]
	v_mfma_f32_16x16x32_bf16 v[98:101], v[158:161], v[200:203], v[98:101]
	v_mfma_f32_16x16x32_bf16 v[86:89], v[150:153], v[208:211], v[86:89]
	v_mfma_f32_16x16x32_bf16 v[82:85], v[158:161], v[208:211], v[82:85]
	v_mfma_f32_16x16x32_bf16 v[70:73], v[150:153], v[216:219], v[70:73]
	v_mfma_f32_16x16x32_bf16 v[66:69], v[158:161], v[216:219], v[66:69]
	s_setprio 0
	s_barrier
	s_add_i32 s90, s90, s24
	v_lshl_add_u64 v[220:221], s[88:89], 0, v[164:165]
	s_mov_b32 m0, s90
	ds_read_b128 v[176:179], v196 offset:16384
	ds_read_b128 v[180:183], v196 offset:17408
	ds_read_b128 v[184:187], v196 offset:18432
	ds_read_b128 v[200:203], v196 offset:19456
	ds_read_b128 v[204:207], v196 offset:20480
	ds_read_b128 v[208:211], v196 offset:21504
	ds_read_b128 v[212:215], v196 offset:22528
	ds_read_b128 v[216:219], v196 offset:23552
	global_load_lds_dwordx4 v[220:221], off
	s_add_i32 m0, s90, 0x2000
	v_lshl_add_u64 v[222:223], s[88:89], 0, v[168:169]
	s_add_u32 s88, s88, s50
	s_addc_u32 s89, s89, s51
	s_add_i32 s86, s86, s24
	global_load_lds_dwordx4 v[222:223], off
	v_lshl_add_u64 v[224:225], s[88:89], 0, v[164:165]
	s_mov_b32 m0, s86
	v_lshl_add_u64 v[226:227], s[88:89], 0, v[168:169]
	global_load_lds_dwordx4 v[224:225], off
	s_add_i32 m0, s86, 0x2000
	v_lshl_add_u64 v[228:229], s[8:9], 0, v[162:163]
	global_load_lds_dwordx4 v[226:227], off
	s_mov_b32 m0, s25
	v_lshl_add_u64 v[230:231], s[8:9], 0, v[166:167]
	global_load_lds_dwordx4 v[228:229], off
	s_mov_b32 m0, s26
	s_nop 0
	global_load_lds_dwordx4 v[230:231], off
	s_waitcnt vmcnt(8)
	s_waitcnt lgkmcnt(0)
	s_barrier
	s_setprio 1
	s_waitcnt lgkmcnt(0)
	v_mfma_f32_16x16x32_bf16 v[62:65], v[130:133], v[176:179], 0
	v_mfma_f32_16x16x32_bf16 v[58:61], v[138:141], v[176:179], 0
	v_mfma_f32_16x16x32_bf16 v[44:47], v[130:133], v[184:187], 0
	v_mfma_f32_16x16x32_bf16 v[40:43], v[138:141], v[184:187], 0
	v_mfma_f32_16x16x32_bf16 v[28:31], v[130:133], v[204:207], 0
	v_mfma_f32_16x16x32_bf16 v[24:27], v[138:141], v[204:207], 0
	v_mfma_f32_16x16x32_bf16 v[12:15], v[130:133], v[212:215], 0
	v_mfma_f32_16x16x32_bf16 v[8:11], v[138:141], v[212:215], 0
	v_mfma_f32_16x16x32_bf16 v[62:65], v[134:137], v[180:183], v[62:65]
	v_mfma_f32_16x16x32_bf16 v[58:61], v[142:145], v[180:183], v[58:61]
	v_mfma_f32_16x16x32_bf16 v[44:47], v[134:137], v[200:203], v[44:47]
	v_mfma_f32_16x16x32_bf16 v[40:43], v[142:145], v[200:203], v[40:43]
	v_mfma_f32_16x16x32_bf16 v[28:31], v[134:137], v[208:211], v[28:31]
	v_mfma_f32_16x16x32_bf16 v[24:27], v[142:145], v[208:211], v[24:27]
	v_mfma_f32_16x16x32_bf16 v[12:15], v[134:137], v[216:219], v[12:15]
	v_mfma_f32_16x16x32_bf16 v[8:11], v[142:145], v[216:219], v[8:11]
	s_setprio 0
	s_setprio 1
	v_mfma_f32_16x16x32_bf16 v[54:57], v[146:149], v[176:179], 0
	v_mfma_f32_16x16x32_bf16 v[50:53], v[154:157], v[176:179], 0
	v_mfma_f32_16x16x32_bf16 v[36:39], v[146:149], v[184:187], 0
	v_mfma_f32_16x16x32_bf16 v[32:35], v[154:157], v[184:187], 0
	v_mfma_f32_16x16x32_bf16 v[20:23], v[146:149], v[204:207], 0
	v_mfma_f32_16x16x32_bf16 v[16:19], v[154:157], v[204:207], 0
	v_mfma_f32_16x16x32_bf16 v[4:7], v[146:149], v[212:215], 0
	v_mfma_f32_16x16x32_bf16 v[0:3], v[154:157], v[212:215], 0
	v_mfma_f32_16x16x32_bf16 v[54:57], v[150:153], v[180:183], v[54:57]
	v_mfma_f32_16x16x32_bf16 v[50:53], v[158:161], v[180:183], v[50:53]
	v_mfma_f32_16x16x32_bf16 v[36:39], v[150:153], v[200:203], v[36:39]
	v_mfma_f32_16x16x32_bf16 v[32:35], v[158:161], v[200:203], v[32:35]
	v_mfma_f32_16x16x32_bf16 v[20:23], v[150:153], v[208:211], v[20:23]
	v_mfma_f32_16x16x32_bf16 v[16:19], v[158:161], v[208:211], v[16:19]
	v_mfma_f32_16x16x32_bf16 v[4:7], v[150:153], v[216:219], v[4:7]
	v_mfma_f32_16x16x32_bf16 v[0:3], v[158:161], v[216:219], v[0:3]
	s_setprio 0
	s_barrier
	s_add_i32 s86, 0, 0x18000
	s_add_i32 s88, 0, 0x1c000
	v_add_u32_e32 v142, s86, v189
	v_add_u32_e32 v158, s88, v189
	ds_read_b128 v[130:133], v142
	ds_read_b128 v[134:137], v142 offset:1024
	ds_read_b128 v[138:141], v142 offset:2048
	ds_read_b128 v[142:145], v142 offset:3072
	ds_read_b128 v[146:149], v158
	ds_read_b128 v[150:153], v158 offset:1024
	ds_read_b128 v[154:157], v158 offset:2048
	ds_read_b128 v[158:161], v158 offset:3072
	s_add_u32 s8, s8, s50
	s_addc_u32 s9, s9, s51
	s_mov_b32 m0, s28
	v_lshl_add_u64 v[232:233], s[8:9], 0, v[162:163]
	ds_read_b128 v[176:179], v196 offset:32768
	ds_read_b128 v[180:183], v196 offset:33792
	ds_read_b128 v[184:187], v196 offset:34816
	ds_read_b128 v[200:203], v196 offset:35840
	ds_read_b128 v[204:207], v196 offset:36864
	ds_read_b128 v[208:211], v196 offset:37888
	ds_read_b128 v[212:215], v196 offset:38912
	ds_read_b128 v[216:219], v196 offset:39936
	global_load_lds_dwordx4 v[232:233], off
	v_lshl_add_u64 v[232:233], s[8:9], 0, v[166:167]
	s_mov_b32 m0, s29
	s_nop 0
	global_load_lds_dwordx4 v[232:233], off
	s_waitcnt vmcnt(8)
	s_waitcnt lgkmcnt(0)
	s_barrier
	s_setprio 1
	s_waitcnt lgkmcnt(0)
	v_mfma_f32_16x16x32_bf16 v[122:125], v[130:133], v[176:179], v[122:125]
	v_mfma_f32_16x16x32_bf16 v[126:129], v[138:141], v[176:179], v[126:129]
	v_mfma_f32_16x16x32_bf16 v[110:113], v[130:133], v[184:187], v[110:113]
	v_mfma_f32_16x16x32_bf16 v[106:109], v[138:141], v[184:187], v[106:109]
	v_mfma_f32_16x16x32_bf16 v[94:97], v[130:133], v[204:207], v[94:97]
	v_mfma_f32_16x16x32_bf16 v[90:93], v[138:141], v[204:207], v[90:93]
	v_mfma_f32_16x16x32_bf16 v[78:81], v[130:133], v[212:215], v[78:81]
	v_mfma_f32_16x16x32_bf16 v[74:77], v[138:141], v[212:215], v[74:77]
	v_mfma_f32_16x16x32_bf16 v[122:125], v[134:137], v[180:183], v[122:125]
	v_mfma_f32_16x16x32_bf16 v[126:129], v[142:145], v[180:183], v[126:129]
	v_mfma_f32_16x16x32_bf16 v[110:113], v[134:137], v[200:203], v[110:113]
	v_mfma_f32_16x16x32_bf16 v[106:109], v[142:145], v[200:203], v[106:109]
	v_mfma_f32_16x16x32_bf16 v[94:97], v[134:137], v[208:211], v[94:97]
	v_mfma_f32_16x16x32_bf16 v[90:93], v[142:145], v[208:211], v[90:93]
	v_mfma_f32_16x16x32_bf16 v[78:81], v[134:137], v[216:219], v[78:81]
	v_mfma_f32_16x16x32_bf16 v[74:77], v[142:145], v[216:219], v[74:77]
	s_setprio 0
	s_setprio 1
	v_mfma_f32_16x16x32_bf16 v[118:121], v[146:149], v[176:179], v[118:121]
	v_mfma_f32_16x16x32_bf16 v[114:117], v[154:157], v[176:179], v[114:117]
	v_mfma_f32_16x16x32_bf16 v[102:105], v[146:149], v[184:187], v[102:105]
	v_mfma_f32_16x16x32_bf16 v[98:101], v[154:157], v[184:187], v[98:101]
	v_mfma_f32_16x16x32_bf16 v[86:89], v[146:149], v[204:207], v[86:89]
	v_mfma_f32_16x16x32_bf16 v[82:85], v[154:157], v[204:207], v[82:85]
	v_mfma_f32_16x16x32_bf16 v[70:73], v[146:149], v[212:215], v[70:73]
	v_mfma_f32_16x16x32_bf16 v[66:69], v[154:157], v[212:215], v[66:69]
	v_mfma_f32_16x16x32_bf16 v[118:121], v[150:153], v[180:183], v[118:121]
	v_mfma_f32_16x16x32_bf16 v[114:117], v[158:161], v[180:183], v[114:117]
	v_mfma_f32_16x16x32_bf16 v[102:105], v[150:153], v[200:203], v[102:105]
	v_mfma_f32_16x16x32_bf16 v[98:101], v[158:161], v[200:203], v[98:101]
	v_mfma_f32_16x16x32_bf16 v[86:89], v[150:153], v[208:211], v[86:89]
	v_mfma_f32_16x16x32_bf16 v[82:85], v[158:161], v[208:211], v[82:85]
	v_mfma_f32_16x16x32_bf16 v[70:73], v[150:153], v[216:219], v[70:73]
	v_mfma_f32_16x16x32_bf16 v[66:69], v[158:161], v[216:219], v[66:69]
	s_setprio 0
	s_barrier
	s_add_i32 s8, s86, s24
	v_lshl_add_u64 v[220:221], v[220:221], 0, s[34:35]
	s_mov_b32 m0, s8
	ds_read_b128 v[176:179], v196 offset:49152
	ds_read_b128 v[180:183], v196 offset:50176
	ds_read_b128 v[184:187], v196 offset:51200
	ds_read_b128 v[200:203], v196 offset:52224
	ds_read_b128 v[204:207], v196 offset:53248
	ds_read_b128 v[208:211], v196 offset:54272
	ds_read_b128 v[212:215], v196 offset:55296
	ds_read_b128 v[216:219], v196 offset:56320
	global_load_lds_dwordx4 v[220:221], off
	v_lshl_add_u64 v[220:221], v[222:223], 0, s[34:35]
	s_add_i32 m0, s8, 0x2000
	s_add_i32 s8, s88, s24
	global_load_lds_dwordx4 v[220:221], off
	v_lshl_add_u64 v[220:221], v[224:225], 0, s[34:35]
	s_mov_b32 m0, s8
	s_nop 0
	global_load_lds_dwordx4 v[220:221], off
	v_lshl_add_u64 v[220:221], v[226:227], 0, s[34:35]
	s_add_i32 m0, s8, 0x2000
	s_nop 0
	global_load_lds_dwordx4 v[220:221], off
	v_lshl_add_u64 v[220:221], v[228:229], 0, s[34:35]
	s_mov_b32 m0, s70
	s_nop 0
	global_load_lds_dwordx4 v[220:221], off
	v_lshl_add_u64 v[220:221], v[230:231], 0, s[34:35]
	s_mov_b32 m0, s71
	s_nop 0
	global_load_lds_dwordx4 v[220:221], off
	s_waitcnt vmcnt(8)
	s_waitcnt lgkmcnt(0)
	s_barrier
	s_setprio 1
	s_waitcnt lgkmcnt(0)
	v_mfma_f32_16x16x32_bf16 v[62:65], v[130:133], v[176:179], v[62:65]
	v_mfma_f32_16x16x32_bf16 v[58:61], v[138:141], v[176:179], v[58:61]
	v_mfma_f32_16x16x32_bf16 v[44:47], v[130:133], v[184:187], v[44:47]
	v_mfma_f32_16x16x32_bf16 v[40:43], v[138:141], v[184:187], v[40:43]
	v_mfma_f32_16x16x32_bf16 v[28:31], v[130:133], v[204:207], v[28:31]
	v_mfma_f32_16x16x32_bf16 v[24:27], v[138:141], v[204:207], v[24:27]
	v_mfma_f32_16x16x32_bf16 v[12:15], v[130:133], v[212:215], v[12:15]
	v_mfma_f32_16x16x32_bf16 v[8:11], v[138:141], v[212:215], v[8:11]
	v_mfma_f32_16x16x32_bf16 v[62:65], v[134:137], v[180:183], v[62:65]
	v_mfma_f32_16x16x32_bf16 v[58:61], v[142:145], v[180:183], v[58:61]
	v_mfma_f32_16x16x32_bf16 v[44:47], v[134:137], v[200:203], v[44:47]
	v_mfma_f32_16x16x32_bf16 v[40:43], v[142:145], v[200:203], v[40:43]
	v_mfma_f32_16x16x32_bf16 v[28:31], v[134:137], v[208:211], v[28:31]
	v_mfma_f32_16x16x32_bf16 v[24:27], v[142:145], v[208:211], v[24:27]
	v_mfma_f32_16x16x32_bf16 v[12:15], v[134:137], v[216:219], v[12:15]
	v_mfma_f32_16x16x32_bf16 v[8:11], v[142:145], v[216:219], v[8:11]
	s_setprio 0
	s_setprio 1
	v_mfma_f32_16x16x32_bf16 v[54:57], v[146:149], v[176:179], v[54:57]
	v_mfma_f32_16x16x32_bf16 v[50:53], v[154:157], v[176:179], v[50:53]
	v_mfma_f32_16x16x32_bf16 v[36:39], v[146:149], v[184:187], v[36:39]
	v_mfma_f32_16x16x32_bf16 v[32:35], v[154:157], v[184:187], v[32:35]
	v_mfma_f32_16x16x32_bf16 v[20:23], v[146:149], v[204:207], v[20:23]
	v_mfma_f32_16x16x32_bf16 v[16:19], v[154:157], v[204:207], v[16:19]
	v_mfma_f32_16x16x32_bf16 v[4:7], v[146:149], v[212:215], v[4:7]
	v_mfma_f32_16x16x32_bf16 v[0:3], v[154:157], v[212:215], v[0:3]
	v_mfma_f32_16x16x32_bf16 v[54:57], v[150:153], v[180:183], v[54:57]
	v_mfma_f32_16x16x32_bf16 v[50:53], v[158:161], v[180:183], v[50:53]
	v_mfma_f32_16x16x32_bf16 v[36:39], v[150:153], v[200:203], v[36:39]
	v_mfma_f32_16x16x32_bf16 v[32:35], v[158:161], v[200:203], v[32:35]
	v_mfma_f32_16x16x32_bf16 v[20:23], v[150:153], v[208:211], v[20:23]
	v_mfma_f32_16x16x32_bf16 v[16:19], v[158:161], v[208:211], v[16:19]
	v_mfma_f32_16x16x32_bf16 v[4:7], v[150:153], v[216:219], v[4:7]
	v_mfma_f32_16x16x32_bf16 v[0:3], v[158:161], v[216:219], v[0:3]
	s_setprio 0
	s_barrier
	s_add_u32 s6, s6, 0x100
	s_addc_u32 s7, s7, 0
	s_add_u32 s83, s83, 0x100
	s_addc_u32 s84, s84, 0
	s_cmp_ge_i32 s85, s30
	s_mov_b32 s8, s85

.Lmy_z_8:
	s_add_u32 s52, s52, 0x80
	s_addc_u32 s53, s53, 0
	s_add_u32 s64, s54, 0x100
	s_addc_u32 s65, s55, 0
	s_mov_b32 s54, 0
	s_add_i32 s66, s54, 2
	s_add_u32 s67, s52, 0x80
	s_addc_u32 s55, s53, 0
	s_add_i32 s70, 0, 0x10000
	s_cmp_eq_u32 s60, s54
	s_cselect_b32 s55, s41, s55
	s_cselect_b32 s54, s40, s67
	v_add_u32_e32 v145, s70, v49
	s_cselect_b32 s69, s51, s65
	s_cselect_b32 s68, s50, s64
	s_add_i32 s67, 0, 0x14000
	ds_read_b128 v[146:149], v145
	ds_read_b128 v[150:153], v145 offset:1024
	ds_read_b128 v[154:157], v145 offset:2048
	ds_read_b128 v[158:161], v145 offset:3072
	v_add_u32_e32 v145, s67, v49
	ds_read_b128 v[162:165], v145
	ds_read_b128 v[166:169], v145 offset:1024
	ds_read_b128 v[170:173], v145 offset:2048
	ds_read_b128 v[174:177], v145 offset:3072
	v_lshl_add_u64 v[210:211], s[52:53], 0, v[140:141]
	s_add_i32 m0, s25, 0xc000
	ds_read_b128 v[178:181], v144
	ds_read_b128 v[182:185], v144 offset:1024
	ds_read_b128 v[186:189], v144 offset:2048
	ds_read_b128 v[190:193], v144 offset:3072
	ds_read_b128 v[194:197], v144 offset:4096
	ds_read_b128 v[198:201], v144 offset:5120
	ds_read_b128 v[202:205], v144 offset:6144
	ds_read_b128 v[206:209], v144 offset:7168
	global_load_lds_dwordx4 v[210:211], off
	v_lshl_add_u64 v[210:211], s[52:53], 0, v[142:143]
	s_add_i32 m0, s25, 0xe000
	s_nop 0
	global_load_lds_dwordx4 v[210:211], off
	s_waitcnt vmcnt(8)
	s_waitcnt lgkmcnt(0)
	s_barrier
	s_setprio 1
	s_waitcnt lgkmcnt(0)
	v_mfma_f32_16x16x32_bf16 v[122:125], v[146:149], v[178:181], 0
	v_mfma_f32_16x16x32_bf16 v[126:129], v[154:157], v[178:181], 0
	v_mfma_f32_16x16x32_bf16 v[110:113], v[146:149], v[186:189], 0
	v_mfma_f32_16x16x32_bf16 v[106:109], v[154:157], v[186:189], 0
	v_mfma_f32_16x16x32_bf16 v[94:97], v[146:149], v[194:197], 0
	v_mfma_f32_16x16x32_bf16 v[90:93], v[154:157], v[194:197], 0
	v_mfma_f32_16x16x32_bf16 v[78:81], v[146:149], v[202:205], 0
	v_mfma_f32_16x16x32_bf16 v[74:77], v[154:157], v[202:205], 0
	v_mfma_f32_16x16x32_bf16 v[122:125], v[150:153], v[182:185], v[122:125]
	v_mfma_f32_16x16x32_bf16 v[126:129], v[158:161], v[182:185], v[126:129]
	v_mfma_f32_16x16x32_bf16 v[110:113], v[150:153], v[190:193], v[110:113]
	v_mfma_f32_16x16x32_bf16 v[106:109], v[158:161], v[190:193], v[106:109]
	v_mfma_f32_16x16x32_bf16 v[94:97], v[150:153], v[198:201], v[94:97]
	v_mfma_f32_16x16x32_bf16 v[90:93], v[158:161], v[198:201], v[90:93]
	v_mfma_f32_16x16x32_bf16 v[78:81], v[150:153], v[206:209], v[78:81]
	v_mfma_f32_16x16x32_bf16 v[74:77], v[158:161], v[206:209], v[74:77]
	s_setprio 0
	s_setprio 1
	v_mfma_f32_16x16x32_bf16 v[118:121], v[162:165], v[178:181], 0
	v_mfma_f32_16x16x32_bf16 v[114:117], v[170:173], v[178:181], 0
	v_mfma_f32_16x16x32_bf16 v[102:105], v[162:165], v[186:189], 0
	v_mfma_f32_16x16x32_bf16 v[98:101], v[170:173], v[186:189], 0
	v_mfma_f32_16x16x32_bf16 v[86:89], v[162:165], v[194:197], 0
	v_mfma_f32_16x16x32_bf16 v[82:85], v[170:173], v[194:197], 0
	v_mfma_f32_16x16x32_bf16 v[70:73], v[162:165], v[202:205], 0
	v_mfma_f32_16x16x32_bf16 v[66:69], v[170:173], v[202:205], 0
	v_mfma_f32_16x16x32_bf16 v[118:121], v[166:169], v[182:185], v[118:121]
	v_mfma_f32_16x16x32_bf16 v[114:117], v[174:177], v[182:185], v[114:117]
	v_mfma_f32_16x16x32_bf16 v[102:105], v[166:169], v[190:193], v[102:105]
	v_mfma_f32_16x16x32_bf16 v[98:101], v[174:177], v[190:193], v[98:101]
	v_mfma_f32_16x16x32_bf16 v[86:89], v[166:169], v[198:201], v[86:89]
	v_mfma_f32_16x16x32_bf16 v[82:85], v[174:177], v[198:201], v[82:85]
	v_mfma_f32_16x16x32_bf16 v[70:73], v[166:169], v[206:209], v[70:73]
	v_mfma_f32_16x16x32_bf16 v[66:69], v[174:177], v[206:209], v[66:69]
	s_setprio 0
	s_barrier
	s_add_i32 s70, s70, s24
	v_lshl_add_u64 v[210:211], s[68:69], 0, v[132:133]
	s_mov_b32 m0, s70
	ds_read_b128 v[178:181], v144 offset:16384
	ds_read_b128 v[182:185], v144 offset:17408
	ds_read_b128 v[186:189], v144 offset:18432
	ds_read_b128 v[190:193], v144 offset:19456
	ds_read_b128 v[194:197], v144 offset:20480
	ds_read_b128 v[198:201], v144 offset:21504
	ds_read_b128 v[202:205], v144 offset:22528
	ds_read_b128 v[206:209], v144 offset:23552
	global_load_lds_dwordx4 v[210:211], off
	s_add_i32 m0, s70, 0x2000
	v_lshl_add_u64 v[212:213], s[68:69], 0, v[136:137]
	s_add_u32 s68, s68, s8
	s_addc_u32 s69, s69, s9
	s_add_i32 s67, s67, s24
	global_load_lds_dwordx4 v[212:213], off
	v_lshl_add_u64 v[214:215], s[68:69], 0, v[132:133]
	s_mov_b32 m0, s67
	v_lshl_add_u64 v[216:217], s[68:69], 0, v[136:137]
	global_load_lds_dwordx4 v[214:215], off
	s_add_i32 m0, s67, 0x2000
	v_lshl_add_u64 v[218:219], s[54:55], 0, v[130:131]
	global_load_lds_dwordx4 v[216:217], off
	s_mov_b32 m0, s25
	v_lshl_add_u64 v[220:221], s[54:55], 0, v[134:135]
	global_load_lds_dwordx4 v[218:219], off
	s_mov_b32 m0, s26
	s_nop 0
	global_load_lds_dwordx4 v[220:221], off
	s_waitcnt vmcnt(8)
	s_waitcnt lgkmcnt(0)
	s_barrier
	s_setprio 1
	s_waitcnt lgkmcnt(0)
	v_mfma_f32_16x16x32_bf16 v[62:65], v[146:149], v[178:181], 0
	v_mfma_f32_16x16x32_bf16 v[58:61], v[154:157], v[178:181], 0
	v_mfma_f32_16x16x32_bf16 v[44:47], v[146:149], v[186:189], 0
	v_mfma_f32_16x16x32_bf16 v[40:43], v[154:157], v[186:189], 0
	v_mfma_f32_16x16x32_bf16 v[28:31], v[146:149], v[194:197], 0
	v_mfma_f32_16x16x32_bf16 v[24:27], v[154:157], v[194:197], 0
	v_mfma_f32_16x16x32_bf16 v[12:15], v[146:149], v[202:205], 0
	v_mfma_f32_16x16x32_bf16 v[8:11], v[154:157], v[202:205], 0
	v_mfma_f32_16x16x32_bf16 v[62:65], v[150:153], v[182:185], v[62:65]
	v_mfma_f32_16x16x32_bf16 v[58:61], v[158:161], v[182:185], v[58:61]
	v_mfma_f32_16x16x32_bf16 v[44:47], v[150:153], v[190:193], v[44:47]
	v_mfma_f32_16x16x32_bf16 v[40:43], v[158:161], v[190:193], v[40:43]
	v_mfma_f32_16x16x32_bf16 v[28:31], v[150:153], v[198:201], v[28:31]
	v_mfma_f32_16x16x32_bf16 v[24:27], v[158:161], v[198:201], v[24:27]
	v_mfma_f32_16x16x32_bf16 v[12:15], v[150:153], v[206:209], v[12:15]
	v_mfma_f32_16x16x32_bf16 v[8:11], v[158:161], v[206:209], v[8:11]
	s_setprio 0
	s_setprio 1
	v_mfma_f32_16x16x32_bf16 v[54:57], v[162:165], v[178:181], 0
	v_mfma_f32_16x16x32_bf16 v[50:53], v[170:173], v[178:181], 0
	v_mfma_f32_16x16x32_bf16 v[36:39], v[162:165], v[186:189], 0
	v_mfma_f32_16x16x32_bf16 v[32:35], v[170:173], v[186:189], 0
	v_mfma_f32_16x16x32_bf16 v[20:23], v[162:165], v[194:197], 0
	v_mfma_f32_16x16x32_bf16 v[16:19], v[170:173], v[194:197], 0
	v_mfma_f32_16x16x32_bf16 v[4:7], v[162:165], v[202:205], 0
	v_mfma_f32_16x16x32_bf16 v[0:3], v[170:173], v[202:205], 0
	v_mfma_f32_16x16x32_bf16 v[54:57], v[166:169], v[182:185], v[54:57]
	v_mfma_f32_16x16x32_bf16 v[50:53], v[174:177], v[182:185], v[50:53]
	v_mfma_f32_16x16x32_bf16 v[36:39], v[166:169], v[190:193], v[36:39]
	v_mfma_f32_16x16x32_bf16 v[32:35], v[174:177], v[190:193], v[32:35]
	v_mfma_f32_16x16x32_bf16 v[20:23], v[166:169], v[198:201], v[20:23]
	v_mfma_f32_16x16x32_bf16 v[16:19], v[174:177], v[198:201], v[16:19]
	v_mfma_f32_16x16x32_bf16 v[4:7], v[166:169], v[206:209], v[4:7]
	v_mfma_f32_16x16x32_bf16 v[0:3], v[174:177], v[206:209], v[0:3]
	s_setprio 0
	s_barrier
	s_add_i32 s67, 0, 0x18000
	v_add_u32_e32 v145, s67, v49
	s_add_i32 s68, 0, 0x1c000
	ds_read_b128 v[146:149], v145
	ds_read_b128 v[150:153], v145 offset:1024
	ds_read_b128 v[154:157], v145 offset:2048
	ds_read_b128 v[158:161], v145 offset:3072
	v_add_u32_e32 v145, s68, v49
	ds_read_b128 v[162:165], v145
	ds_read_b128 v[166:169], v145 offset:1024
	ds_read_b128 v[170:173], v145 offset:2048
	ds_read_b128 v[174:177], v145 offset:3072
	s_add_u32 s54, s54, s8
	s_addc_u32 s55, s55, s9
	s_mov_b32 m0, s28
	v_lshl_add_u64 v[222:223], s[54:55], 0, v[130:131]
	ds_read_b128 v[178:181], v144 offset:32768
	ds_read_b128 v[182:185], v144 offset:33792
	ds_read_b128 v[186:189], v144 offset:34816
	ds_read_b128 v[190:193], v144 offset:35840
	ds_read_b128 v[194:197], v144 offset:36864
	ds_read_b128 v[198:201], v144 offset:37888
	ds_read_b128 v[202:205], v144 offset:38912
	ds_read_b128 v[206:209], v144 offset:39936
	global_load_lds_dwordx4 v[222:223], off
	v_lshl_add_u64 v[222:223], s[54:55], 0, v[134:135]
	s_mov_b32 m0, s29
	s_nop 0
	global_load_lds_dwordx4 v[222:223], off
	s_waitcnt vmcnt(8)
	s_waitcnt lgkmcnt(0)
	s_barrier
	s_setprio 1
	s_waitcnt lgkmcnt(0)
	v_mfma_f32_16x16x32_bf16 v[122:125], v[146:149], v[178:181], v[122:125]
	v_mfma_f32_16x16x32_bf16 v[126:129], v[154:157], v[178:181], v[126:129]
	v_mfma_f32_16x16x32_bf16 v[110:113], v[146:149], v[186:189], v[110:113]
	v_mfma_f32_16x16x32_bf16 v[106:109], v[154:157], v[186:189], v[106:109]
	v_mfma_f32_16x16x32_bf16 v[94:97], v[146:149], v[194:197], v[94:97]
	v_mfma_f32_16x16x32_bf16 v[90:93], v[154:157], v[194:197], v[90:93]
	v_mfma_f32_16x16x32_bf16 v[78:81], v[146:149], v[202:205], v[78:81]
	v_mfma_f32_16x16x32_bf16 v[74:77], v[154:157], v[202:205], v[74:77]
	v_mfma_f32_16x16x32_bf16 v[122:125], v[150:153], v[182:185], v[122:125]
	v_mfma_f32_16x16x32_bf16 v[126:129], v[158:161], v[182:185], v[126:129]
	v_mfma_f32_16x16x32_bf16 v[110:113], v[150:153], v[190:193], v[110:113]
	v_mfma_f32_16x16x32_bf16 v[106:109], v[158:161], v[190:193], v[106:109]
	v_mfma_f32_16x16x32_bf16 v[94:97], v[150:153], v[198:201], v[94:97]
	v_mfma_f32_16x16x32_bf16 v[90:93], v[158:161], v[198:201], v[90:93]
	v_mfma_f32_16x16x32_bf16 v[78:81], v[150:153], v[206:209], v[78:81]
	v_mfma_f32_16x16x32_bf16 v[74:77], v[158:161], v[206:209], v[74:77]
	s_setprio 0
	s_setprio 1
	v_mfma_f32_16x16x32_bf16 v[118:121], v[162:165], v[178:181], v[118:121]
	v_mfma_f32_16x16x32_bf16 v[114:117], v[170:173], v[178:181], v[114:117]
	v_mfma_f32_16x16x32_bf16 v[102:105], v[162:165], v[186:189], v[102:105]
	v_mfma_f32_16x16x32_bf16 v[98:101], v[170:173], v[186:189], v[98:101]
	v_mfma_f32_16x16x32_bf16 v[86:89], v[162:165], v[194:197], v[86:89]
	v_mfma_f32_16x16x32_bf16 v[82:85], v[170:173], v[194:197], v[82:85]
	v_mfma_f32_16x16x32_bf16 v[70:73], v[162:165], v[202:205], v[70:73]
	v_mfma_f32_16x16x32_bf16 v[66:69], v[170:173], v[202:205], v[66:69]
	v_mfma_f32_16x16x32_bf16 v[118:121], v[166:169], v[182:185], v[118:121]
	v_mfma_f32_16x16x32_bf16 v[114:117], v[174:177], v[182:185], v[114:117]
	v_mfma_f32_16x16x32_bf16 v[102:105], v[166:169], v[190:193], v[102:105]
	v_mfma_f32_16x16x32_bf16 v[98:101], v[174:177], v[190:193], v[98:101]
	v_mfma_f32_16x16x32_bf16 v[86:89], v[166:169], v[198:201], v[86:89]
	v_mfma_f32_16x16x32_bf16 v[82:85], v[174:177], v[198:201], v[82:85]
	v_mfma_f32_16x16x32_bf16 v[70:73], v[166:169], v[206:209], v[70:73]
	v_mfma_f32_16x16x32_bf16 v[66:69], v[174:177], v[206:209], v[66:69]
	s_setprio 0
	s_barrier
	s_add_i32 s54, s67, s24
	v_lshl_add_u64 v[210:211], v[210:211], 0, s[34:35]
	s_mov_b32 m0, s54
	ds_read_b128 v[178:181], v144 offset:49152
	ds_read_b128 v[182:185], v144 offset:50176
	ds_read_b128 v[186:189], v144 offset:51200
	ds_read_b128 v[190:193], v144 offset:52224
	ds_read_b128 v[194:197], v144 offset:53248
	ds_read_b128 v[198:201], v144 offset:54272
	ds_read_b128 v[202:205], v144 offset:55296
	ds_read_b128 v[206:209], v144 offset:56320
	global_load_lds_dwordx4 v[210:211], off
	v_lshl_add_u64 v[210:211], v[212:213], 0, s[34:35]
	s_add_i32 m0, s54, 0x2000
	s_add_i32 s54, s68, s24
	global_load_lds_dwordx4 v[210:211], off
	v_lshl_add_u64 v[210:211], v[214:215], 0, s[34:35]
	s_mov_b32 m0, s54
	s_nop 0
	global_load_lds_dwordx4 v[210:211], off
	v_lshl_add_u64 v[210:211], v[216:217], 0, s[34:35]
	s_add_i32 m0, s54, 0x2000
	s_nop 0
	global_load_lds_dwordx4 v[210:211], off
	v_lshl_add_u64 v[210:211], v[218:219], 0, s[34:35]
	s_mov_b32 m0, s56
	s_nop 0
	global_load_lds_dwordx4 v[210:211], off
	v_lshl_add_u64 v[210:211], v[220:221], 0, s[34:35]
	s_mov_b32 m0, s58
	s_nop 0
	global_load_lds_dwordx4 v[210:211], off
	s_waitcnt vmcnt(8)
	s_waitcnt lgkmcnt(0)
	s_barrier
	s_setprio 1
	s_waitcnt lgkmcnt(0)
	v_mfma_f32_16x16x32_bf16 v[62:65], v[146:149], v[178:181], v[62:65]
	v_mfma_f32_16x16x32_bf16 v[58:61], v[154:157], v[178:181], v[58:61]
	v_mfma_f32_16x16x32_bf16 v[44:47], v[146:149], v[186:189], v[44:47]
	v_mfma_f32_16x16x32_bf16 v[40:43], v[154:157], v[186:189], v[40:43]
	v_mfma_f32_16x16x32_bf16 v[28:31], v[146:149], v[194:197], v[28:31]
	v_mfma_f32_16x16x32_bf16 v[24:27], v[154:157], v[194:197], v[24:27]
	v_mfma_f32_16x16x32_bf16 v[12:15], v[146:149], v[202:205], v[12:15]
	v_mfma_f32_16x16x32_bf16 v[8:11], v[154:157], v[202:205], v[8:11]
	v_mfma_f32_16x16x32_bf16 v[62:65], v[150:153], v[182:185], v[62:65]
	v_mfma_f32_16x16x32_bf16 v[58:61], v[158:161], v[182:185], v[58:61]
	v_mfma_f32_16x16x32_bf16 v[44:47], v[150:153], v[190:193], v[44:47]
	v_mfma_f32_16x16x32_bf16 v[40:43], v[158:161], v[190:193], v[40:43]
	v_mfma_f32_16x16x32_bf16 v[28:31], v[150:153], v[198:201], v[28:31]
	v_mfma_f32_16x16x32_bf16 v[24:27], v[158:161], v[198:201], v[24:27]
	v_mfma_f32_16x16x32_bf16 v[12:15], v[150:153], v[206:209], v[12:15]
	v_mfma_f32_16x16x32_bf16 v[8:11], v[158:161], v[206:209], v[8:11]
	s_setprio 0
	s_setprio 1
	v_mfma_f32_16x16x32_bf16 v[54:57], v[162:165], v[178:181], v[54:57]
	v_mfma_f32_16x16x32_bf16 v[50:53], v[170:173], v[178:181], v[50:53]
	v_mfma_f32_16x16x32_bf16 v[36:39], v[162:165], v[186:189], v[36:39]
	v_mfma_f32_16x16x32_bf16 v[32:35], v[170:173], v[186:189], v[32:35]
	v_mfma_f32_16x16x32_bf16 v[20:23], v[162:165], v[194:197], v[20:23]
	v_mfma_f32_16x16x32_bf16 v[16:19], v[170:173], v[194:197], v[16:19]
	v_mfma_f32_16x16x32_bf16 v[4:7], v[162:165], v[202:205], v[4:7]
	v_mfma_f32_16x16x32_bf16 v[0:3], v[170:173], v[202:205], v[0:3]
	v_mfma_f32_16x16x32_bf16 v[54:57], v[166:169], v[182:185], v[54:57]
	v_mfma_f32_16x16x32_bf16 v[50:53], v[174:177], v[182:185], v[50:53]
	v_mfma_f32_16x16x32_bf16 v[36:39], v[166:169], v[190:193], v[36:39]
	v_mfma_f32_16x16x32_bf16 v[32:35], v[174:177], v[190:193], v[32:35]
	v_mfma_f32_16x16x32_bf16 v[20:23], v[166:169], v[198:201], v[20:23]
	v_mfma_f32_16x16x32_bf16 v[16:19], v[174:177], v[198:201], v[16:19]
	v_mfma_f32_16x16x32_bf16 v[4:7], v[166:169], v[206:209], v[4:7]
	v_mfma_f32_16x16x32_bf16 v[0:3], v[174:177], v[206:209], v[0:3]
	s_setprio 0
	s_barrier
	s_add_u32 s52, s52, 0x100
	s_addc_u32 s53, s53, 0
	s_add_u32 s64, s64, 0x100
	s_addc_u32 s65, s65, 0
	s_cmp_ge_i32 s66, s30
	s_mov_b32 s54, s66

.Lmy_z_9:
	s_add_u32 s6, s6, 0x80
	s_addc_u32 s7, s7, 0
	s_add_u32 s19, s8, 0x100
	s_addc_u32 s25, s9, 0
	s_mov_b32 s8, 0
	s_add_i32 s28, s8, 2
	s_add_u32 s29, s6, 0x80
	s_addc_u32 s9, s7, 0
	s_add_i32 s30, 0, 0x10000
	s_cmp_eq_u32 s94, s8
	s_cselect_b32 s9, s69, s9
	s_cselect_b32 s8, s68, s29
	s_cselect_b32 s45, s71, s25
	s_cselect_b32 s44, s70, s19
	s_add_i32 s29, 0, 0x14000
	v_add_u32_e32 v142, s30, v173
	v_add_u32_e32 v168, s29, v173
	ds_read_b128 v[130:133], v142
	ds_read_b128 v[134:137], v142 offset:1024
	ds_read_b128 v[138:141], v142 offset:2048
	ds_read_b128 v[142:145], v142 offset:3072
	ds_read_b128 v[146:149], v168
	ds_read_b128 v[150:153], v168 offset:1024
	ds_read_b128 v[178:181], v168 offset:2048
	ds_read_b128 v[182:185], v168 offset:3072
	v_lshl_add_u64 v[170:171], s[6:7], 0, v[164:165]
	s_add_i32 m0, s26, 0xc000
	ds_read_b128 v[210:213], v206
	ds_read_b128 v[214:217], v206 offset:1024
	ds_read_b128 v[218:221], v206 offset:2048
	ds_read_b128 v[222:225], v206 offset:3072
	ds_read_b128 v[226:229], v206 offset:4096
	ds_read_b128 v[230:233], v206 offset:5120
	ds_read_b128 v[246:249], v206 offset:6144
	ds_read_b128 v[250:253], v206 offset:7168
	global_load_lds_dwordx4 v[170:171], off
	v_lshl_add_u64 v[170:171], s[6:7], 0, v[166:167]
	s_add_i32 m0, s26, 0xe000
	s_nop 0
	global_load_lds_dwordx4 v[170:171], off
	s_waitcnt vmcnt(8)
	s_waitcnt lgkmcnt(0)
	s_barrier
	s_setprio 1
	s_waitcnt lgkmcnt(0)
	v_mfma_f32_16x16x32_bf16 v[126:129], v[130:133], v[210:213], 0
	v_mfma_f32_16x16x32_bf16 v[122:125], v[138:141], v[210:213], 0
	v_mfma_f32_16x16x32_bf16 v[110:113], v[130:133], v[218:221], 0
	v_mfma_f32_16x16x32_bf16 v[106:109], v[138:141], v[218:221], 0
	v_mfma_f32_16x16x32_bf16 v[94:97], v[130:133], v[226:229], 0
	v_mfma_f32_16x16x32_bf16 v[90:93], v[138:141], v[226:229], 0
	v_mfma_f32_16x16x32_bf16 v[78:81], v[130:133], v[246:249], 0
	v_mfma_f32_16x16x32_bf16 v[74:77], v[138:141], v[246:249], 0
	v_mfma_f32_16x16x32_bf16 v[126:129], v[134:137], v[214:217], v[126:129]
	v_mfma_f32_16x16x32_bf16 v[122:125], v[142:145], v[214:217], v[122:125]
	v_mfma_f32_16x16x32_bf16 v[110:113], v[134:137], v[222:225], v[110:113]
	v_mfma_f32_16x16x32_bf16 v[106:109], v[142:145], v[222:225], v[106:109]
	v_mfma_f32_16x16x32_bf16 v[94:97], v[134:137], v[230:233], v[94:97]
	v_mfma_f32_16x16x32_bf16 v[90:93], v[142:145], v[230:233], v[90:93]
	v_mfma_f32_16x16x32_bf16 v[78:81], v[134:137], v[250:253], v[78:81]
	v_mfma_f32_16x16x32_bf16 v[74:77], v[142:145], v[250:253], v[74:77]
	s_setprio 0
	s_setprio 1
	v_mfma_f32_16x16x32_bf16 v[118:121], v[146:149], v[210:213], 0
	v_mfma_f32_16x16x32_bf16 v[114:117], v[178:181], v[210:213], 0
	v_mfma_f32_16x16x32_bf16 v[102:105], v[146:149], v[218:221], 0
	v_mfma_f32_16x16x32_bf16 v[98:101], v[178:181], v[218:221], 0
	v_mfma_f32_16x16x32_bf16 v[86:89], v[146:149], v[226:229], 0
	v_mfma_f32_16x16x32_bf16 v[82:85], v[178:181], v[226:229], 0
	v_mfma_f32_16x16x32_bf16 v[70:73], v[146:149], v[246:249], 0
	v_mfma_f32_16x16x32_bf16 v[66:69], v[178:181], v[246:249], 0
	v_mfma_f32_16x16x32_bf16 v[118:121], v[150:153], v[214:217], v[118:121]
	v_mfma_f32_16x16x32_bf16 v[114:117], v[182:185], v[214:217], v[114:117]
	v_mfma_f32_16x16x32_bf16 v[102:105], v[150:153], v[222:225], v[102:105]
	v_mfma_f32_16x16x32_bf16 v[98:101], v[182:185], v[222:225], v[98:101]
	v_mfma_f32_16x16x32_bf16 v[86:89], v[150:153], v[230:233], v[86:89]
	v_mfma_f32_16x16x32_bf16 v[82:85], v[182:185], v[230:233], v[82:85]
	v_mfma_f32_16x16x32_bf16 v[70:73], v[150:153], v[250:253], v[70:73]
	v_mfma_f32_16x16x32_bf16 v[66:69], v[182:185], v[250:253], v[66:69]
	s_setprio 0
	s_barrier
	s_add_i32 s30, s30, s24
	v_lshl_add_u64 v[170:171], s[44:45], 0, v[156:157]
	s_mov_b32 m0, s30
	ds_read_b128 v[210:213], v206 offset:16384
	ds_read_b128 v[214:217], v206 offset:17408
	ds_read_b128 v[218:221], v206 offset:18432
	ds_read_b128 v[222:225], v206 offset:19456
	ds_read_b128 v[226:229], v206 offset:20480
	ds_read_b128 v[230:233], v206 offset:21504
	ds_read_b128 v[246:249], v206 offset:22528
	ds_read_b128 v[250:253], v206 offset:23552
	global_load_lds_dwordx4 v[170:171], off
	s_add_i32 m0, s30, 0x2000
	v_lshl_add_u64 v[174:175], s[44:45], 0, v[160:161]
	s_add_u32 s44, s44, s50
	s_addc_u32 s45, s45, s51
	s_add_i32 s29, s29, s24
	global_load_lds_dwordx4 v[174:175], off
	v_lshl_add_u64 v[188:189], s[44:45], 0, v[156:157]
	s_mov_b32 m0, s29
	v_lshl_add_u64 v[192:193], s[44:45], 0, v[160:161]
	global_load_lds_dwordx4 v[188:189], off
	s_add_i32 m0, s29, 0x2000
	v_lshl_add_u64 v[196:197], s[8:9], 0, v[154:155]
	global_load_lds_dwordx4 v[192:193], off
	s_mov_b32 m0, s26
	v_lshl_add_u64 v[200:201], s[8:9], 0, v[158:159]
	global_load_lds_dwordx4 v[196:197], off
	s_mov_b32 m0, s78
	s_nop 0
	global_load_lds_dwordx4 v[200:201], off
	s_waitcnt vmcnt(8)
	s_waitcnt lgkmcnt(0)
	s_barrier
	s_setprio 1
	s_waitcnt lgkmcnt(0)
	v_mfma_f32_16x16x32_bf16 v[62:65], v[130:133], v[210:213], 0
	v_mfma_f32_16x16x32_bf16 v[58:61], v[138:141], v[210:213], 0
	v_mfma_f32_16x16x32_bf16 v[44:47], v[130:133], v[218:221], 0
	v_mfma_f32_16x16x32_bf16 v[40:43], v[138:141], v[218:221], 0
	v_mfma_f32_16x16x32_bf16 v[28:31], v[130:133], v[226:229], 0
	v_mfma_f32_16x16x32_bf16 v[24:27], v[138:141], v[226:229], 0
	v_mfma_f32_16x16x32_bf16 v[12:15], v[130:133], v[246:249], 0
	v_mfma_f32_16x16x32_bf16 v[8:11], v[138:141], v[246:249], 0
	v_mfma_f32_16x16x32_bf16 v[62:65], v[134:137], v[214:217], v[62:65]
	v_mfma_f32_16x16x32_bf16 v[58:61], v[142:145], v[214:217], v[58:61]
	v_mfma_f32_16x16x32_bf16 v[44:47], v[134:137], v[222:225], v[44:47]
	v_mfma_f32_16x16x32_bf16 v[40:43], v[142:145], v[222:225], v[40:43]
	v_mfma_f32_16x16x32_bf16 v[28:31], v[134:137], v[230:233], v[28:31]
	v_mfma_f32_16x16x32_bf16 v[24:27], v[142:145], v[230:233], v[24:27]
	v_mfma_f32_16x16x32_bf16 v[12:15], v[134:137], v[250:253], v[12:15]
	v_mfma_f32_16x16x32_bf16 v[8:11], v[142:145], v[250:253], v[8:11]
	s_setprio 0
	s_setprio 1
	v_mfma_f32_16x16x32_bf16 v[54:57], v[146:149], v[210:213], 0
	v_mfma_f32_16x16x32_bf16 v[50:53], v[178:181], v[210:213], 0
	v_mfma_f32_16x16x32_bf16 v[36:39], v[146:149], v[218:221], 0
	v_mfma_f32_16x16x32_bf16 v[32:35], v[178:181], v[218:221], 0
	v_mfma_f32_16x16x32_bf16 v[20:23], v[146:149], v[226:229], 0
	v_mfma_f32_16x16x32_bf16 v[16:19], v[178:181], v[226:229], 0
	v_mfma_f32_16x16x32_bf16 v[4:7], v[146:149], v[246:249], 0
	v_mfma_f32_16x16x32_bf16 v[0:3], v[178:181], v[246:249], 0
	v_mfma_f32_16x16x32_bf16 v[54:57], v[150:153], v[214:217], v[54:57]
	v_mfma_f32_16x16x32_bf16 v[50:53], v[182:185], v[214:217], v[50:53]
	v_mfma_f32_16x16x32_bf16 v[36:39], v[150:153], v[222:225], v[36:39]
	v_mfma_f32_16x16x32_bf16 v[32:35], v[182:185], v[222:225], v[32:35]
	v_mfma_f32_16x16x32_bf16 v[20:23], v[150:153], v[230:233], v[20:23]
	v_mfma_f32_16x16x32_bf16 v[16:19], v[182:185], v[230:233], v[16:19]
	v_mfma_f32_16x16x32_bf16 v[4:7], v[150:153], v[250:253], v[4:7]
	v_mfma_f32_16x16x32_bf16 v[0:3], v[182:185], v[250:253], v[0:3]
	s_setprio 0
	s_barrier
	s_add_i32 s29, 0, 0x18000
	s_add_i32 s30, 0, 0x1c000
	v_add_u32_e32 v142, s29, v173
	v_add_u32_e32 v168, s30, v173
	ds_read_b128 v[130:133], v142
	ds_read_b128 v[134:137], v142 offset:1024
	ds_read_b128 v[138:141], v142 offset:2048
	ds_read_b128 v[142:145], v142 offset:3072
	ds_read_b128 v[146:149], v168
	ds_read_b128 v[150:153], v168 offset:1024
	ds_read_b128 v[178:181], v168 offset:2048
	ds_read_b128 v[182:185], v168 offset:3072
	s_add_u32 s8, s8, s50
	s_addc_u32 s9, s9, s51
	s_mov_b32 m0, s79
	v_lshl_add_u64 v[204:205], s[8:9], 0, v[154:155]
	ds_read_b128 v[210:213], v206 offset:32768
	ds_read_b128 v[214:217], v206 offset:33792
	ds_read_b128 v[218:221], v206 offset:34816
	ds_read_b128 v[222:225], v206 offset:35840
	ds_read_b128 v[226:229], v206 offset:36864
	ds_read_b128 v[230:233], v206 offset:37888
	ds_read_b128 v[246:249], v206 offset:38912
	ds_read_b128 v[250:253], v206 offset:39936
	global_load_lds_dwordx4 v[204:205], off
	v_lshl_add_u64 v[204:205], s[8:9], 0, v[158:159]
	s_mov_b32 m0, s88
	s_nop 0
	global_load_lds_dwordx4 v[204:205], off
	s_waitcnt vmcnt(8)
	s_waitcnt lgkmcnt(0)
	s_barrier
	s_setprio 1
	s_waitcnt lgkmcnt(0)
	v_mfma_f32_16x16x32_bf16 v[126:129], v[130:133], v[210:213], v[126:129]
	v_mfma_f32_16x16x32_bf16 v[122:125], v[138:141], v[210:213], v[122:125]
	v_mfma_f32_16x16x32_bf16 v[110:113], v[130:133], v[218:221], v[110:113]
	v_mfma_f32_16x16x32_bf16 v[106:109], v[138:141], v[218:221], v[106:109]
	v_mfma_f32_16x16x32_bf16 v[94:97], v[130:133], v[226:229], v[94:97]
	v_mfma_f32_16x16x32_bf16 v[90:93], v[138:141], v[226:229], v[90:93]
	v_mfma_f32_16x16x32_bf16 v[78:81], v[130:133], v[246:249], v[78:81]
	v_mfma_f32_16x16x32_bf16 v[74:77], v[138:141], v[246:249], v[74:77]
	v_mfma_f32_16x16x32_bf16 v[126:129], v[134:137], v[214:217], v[126:129]
	v_mfma_f32_16x16x32_bf16 v[122:125], v[142:145], v[214:217], v[122:125]
	v_mfma_f32_16x16x32_bf16 v[110:113], v[134:137], v[222:225], v[110:113]
	v_mfma_f32_16x16x32_bf16 v[106:109], v[142:145], v[222:225], v[106:109]
	v_mfma_f32_16x16x32_bf16 v[94:97], v[134:137], v[230:233], v[94:97]
	v_mfma_f32_16x16x32_bf16 v[90:93], v[142:145], v[230:233], v[90:93]
	v_mfma_f32_16x16x32_bf16 v[78:81], v[134:137], v[250:253], v[78:81]
	v_mfma_f32_16x16x32_bf16 v[74:77], v[142:145], v[250:253], v[74:77]
	s_setprio 0
	s_setprio 1
	v_mfma_f32_16x16x32_bf16 v[118:121], v[146:149], v[210:213], v[118:121]
	v_mfma_f32_16x16x32_bf16 v[114:117], v[178:181], v[210:213], v[114:117]
	v_mfma_f32_16x16x32_bf16 v[102:105], v[146:149], v[218:221], v[102:105]
	v_mfma_f32_16x16x32_bf16 v[98:101], v[178:181], v[218:221], v[98:101]
	v_mfma_f32_16x16x32_bf16 v[86:89], v[146:149], v[226:229], v[86:89]
	v_mfma_f32_16x16x32_bf16 v[82:85], v[178:181], v[226:229], v[82:85]
	v_mfma_f32_16x16x32_bf16 v[70:73], v[146:149], v[246:249], v[70:73]
	v_mfma_f32_16x16x32_bf16 v[66:69], v[178:181], v[246:249], v[66:69]
	v_mfma_f32_16x16x32_bf16 v[118:121], v[150:153], v[214:217], v[118:121]
	v_mfma_f32_16x16x32_bf16 v[114:117], v[182:185], v[214:217], v[114:117]
	v_mfma_f32_16x16x32_bf16 v[102:105], v[150:153], v[222:225], v[102:105]
	v_mfma_f32_16x16x32_bf16 v[98:101], v[182:185], v[222:225], v[98:101]
	v_mfma_f32_16x16x32_bf16 v[86:89], v[150:153], v[230:233], v[86:89]
	v_mfma_f32_16x16x32_bf16 v[82:85], v[182:185], v[230:233], v[82:85]
	v_mfma_f32_16x16x32_bf16 v[70:73], v[150:153], v[250:253], v[70:73]
	v_mfma_f32_16x16x32_bf16 v[66:69], v[182:185], v[250:253], v[66:69]
	s_setprio 0
	s_barrier
	s_add_i32 s8, s29, s24
	v_lshl_add_u64 v[170:171], v[170:171], 0, s[34:35]
	s_mov_b32 m0, s8
	ds_read_b128 v[210:213], v206 offset:49152
	ds_read_b128 v[214:217], v206 offset:50176
	ds_read_b128 v[218:221], v206 offset:51200
	ds_read_b128 v[222:225], v206 offset:52224
	ds_read_b128 v[226:229], v206 offset:53248
	ds_read_b128 v[230:233], v206 offset:54272
	ds_read_b128 v[246:249], v206 offset:55296
	ds_read_b128 v[250:253], v206 offset:56320
	global_load_lds_dwordx4 v[170:171], off
	v_lshl_add_u64 v[170:171], v[174:175], 0, s[34:35]
	s_add_i32 m0, s8, 0x2000
	s_add_i32 s8, s30, s24
	global_load_lds_dwordx4 v[170:171], off
	v_lshl_add_u64 v[170:171], v[188:189], 0, s[34:35]
	s_mov_b32 m0, s8
	s_nop 0
	global_load_lds_dwordx4 v[170:171], off
	v_lshl_add_u64 v[170:171], v[192:193], 0, s[34:35]
	s_add_i32 m0, s8, 0x2000
	s_nop 0
	global_load_lds_dwordx4 v[170:171], off
	v_lshl_add_u64 v[170:171], v[196:197], 0, s[34:35]
	s_mov_b32 m0, s92
	s_nop 0
	global_load_lds_dwordx4 v[170:171], off
	v_lshl_add_u64 v[170:171], v[200:201], 0, s[34:35]
	s_mov_b32 m0, s93
	s_nop 0
	global_load_lds_dwordx4 v[170:171], off
	s_waitcnt vmcnt(8)
	s_waitcnt lgkmcnt(0)
	s_barrier
	s_setprio 1
	s_waitcnt lgkmcnt(0)
	v_mfma_f32_16x16x32_bf16 v[62:65], v[130:133], v[210:213], v[62:65]
	v_mfma_f32_16x16x32_bf16 v[58:61], v[138:141], v[210:213], v[58:61]
	v_mfma_f32_16x16x32_bf16 v[44:47], v[130:133], v[218:221], v[44:47]
	v_mfma_f32_16x16x32_bf16 v[40:43], v[138:141], v[218:221], v[40:43]
	v_mfma_f32_16x16x32_bf16 v[28:31], v[130:133], v[226:229], v[28:31]
	v_mfma_f32_16x16x32_bf16 v[24:27], v[138:141], v[226:229], v[24:27]
	v_mfma_f32_16x16x32_bf16 v[12:15], v[130:133], v[246:249], v[12:15]
	v_mfma_f32_16x16x32_bf16 v[8:11], v[138:141], v[246:249], v[8:11]
	v_mfma_f32_16x16x32_bf16 v[62:65], v[134:137], v[214:217], v[62:65]
	v_mfma_f32_16x16x32_bf16 v[58:61], v[142:145], v[214:217], v[58:61]
	v_mfma_f32_16x16x32_bf16 v[44:47], v[134:137], v[222:225], v[44:47]
	v_mfma_f32_16x16x32_bf16 v[40:43], v[142:145], v[222:225], v[40:43]
	v_mfma_f32_16x16x32_bf16 v[28:31], v[134:137], v[230:233], v[28:31]
	v_mfma_f32_16x16x32_bf16 v[24:27], v[142:145], v[230:233], v[24:27]
	v_mfma_f32_16x16x32_bf16 v[12:15], v[134:137], v[250:253], v[12:15]
	v_mfma_f32_16x16x32_bf16 v[8:11], v[142:145], v[250:253], v[8:11]
	s_setprio 0
	s_setprio 1
	v_mfma_f32_16x16x32_bf16 v[54:57], v[146:149], v[210:213], v[54:57]
	v_mfma_f32_16x16x32_bf16 v[50:53], v[178:181], v[210:213], v[50:53]
	v_mfma_f32_16x16x32_bf16 v[36:39], v[146:149], v[218:221], v[36:39]
	v_mfma_f32_16x16x32_bf16 v[32:35], v[178:181], v[218:221], v[32:35]
	v_mfma_f32_16x16x32_bf16 v[20:23], v[146:149], v[226:229], v[20:23]
	v_mfma_f32_16x16x32_bf16 v[16:19], v[178:181], v[226:229], v[16:19]
	v_mfma_f32_16x16x32_bf16 v[4:7], v[146:149], v[246:249], v[4:7]
	v_mfma_f32_16x16x32_bf16 v[0:3], v[178:181], v[246:249], v[0:3]
	v_mfma_f32_16x16x32_bf16 v[54:57], v[150:153], v[214:217], v[54:57]
	v_mfma_f32_16x16x32_bf16 v[50:53], v[182:185], v[214:217], v[50:53]
	v_mfma_f32_16x16x32_bf16 v[36:39], v[150:153], v[222:225], v[36:39]
	v_mfma_f32_16x16x32_bf16 v[32:35], v[182:185], v[222:225], v[32:35]
	v_mfma_f32_16x16x32_bf16 v[20:23], v[150:153], v[230:233], v[20:23]
	v_mfma_f32_16x16x32_bf16 v[16:19], v[182:185], v[230:233], v[16:19]
	v_mfma_f32_16x16x32_bf16 v[4:7], v[150:153], v[250:253], v[4:7]
	v_mfma_f32_16x16x32_bf16 v[0:3], v[182:185], v[250:253], v[0:3]
	s_setprio 0
	s_barrier
	s_add_u32 s6, s6, 0x100
	s_addc_u32 s7, s7, 0
	s_add_u32 s19, s19, 0x100
	s_addc_u32 s25, s25, 0
	s_cmp_ge_i32 s28, s89
	s_mov_b32 s8, s28
